# instruction selection in the lock-step fp8 epilogues (M1, MoE, projections): 184 dead zero-fills in front of v_cvt_pk_fp8_f32 low/high pairs removed
# speedup vs baseline: 1.0168x; 1.0168x over previous
.LBB0_659:
	v_mul_f32_e32 v103, 0x45000000, v64
	v_mul_f32_e32 v104, 0x45000000, v68
	v_med3_f32 v103, v103, s25, v218
	v_med3_f32 v104, v104, s25, v218
	v_cvt_pk_fp8_f32 v106, v103, v104
	v_mul_f32_e32 v105, 0x45000000, v72
	v_mul_f32_e32 v103, 0x45000000, v76
	v_med3_f32 v104, v105, s25, v218
	v_med3_f32 v103, v103, s25, v218
	v_cvt_pk_fp8_f32 v106, v104, v103 op_sel:[0,0,1]
	v_mul_f32_e32 v103, 0x45000000, v65
	v_mul_f32_e32 v104, 0x45000000, v69
	v_med3_f32 v103, v103, s25, v218
	v_med3_f32 v104, v104, s25, v218
	v_cvt_pk_fp8_f32 v107, v103, v104
	v_mul_f32_e32 v105, 0x45000000, v73
	v_mul_f32_e32 v103, 0x45000000, v77
	v_med3_f32 v104, v105, s25, v218
	v_med3_f32 v103, v103, s25, v218
	v_cvt_pk_fp8_f32 v107, v104, v103 op_sel:[0,0,1]
	v_mul_f32_e32 v103, 0x45000000, v66
	v_mul_f32_e32 v104, 0x45000000, v70
	v_med3_f32 v103, v103, s25, v218
	v_med3_f32 v104, v104, s25, v218
	v_cvt_pk_fp8_f32 v108, v103, v104
	v_mul_f32_e32 v105, 0x45000000, v74
	v_mul_f32_e32 v103, 0x45000000, v78
	v_med3_f32 v104, v105, s25, v218
	v_med3_f32 v103, v103, s25, v218
	v_cvt_pk_fp8_f32 v108, v104, v103 op_sel:[0,0,1]
	v_mul_f32_e32 v103, 0x45000000, v67
	v_mul_f32_e32 v104, 0x45000000, v71
	v_med3_f32 v103, v103, s25, v218
	v_med3_f32 v104, v104, s25, v218
	v_cvt_pk_fp8_f32 v109, v103, v104
	v_mul_f32_e32 v105, 0x45000000, v75
	v_mul_f32_e32 v103, 0x45000000, v79
	v_med3_f32 v104, v105, s25, v218
	v_med3_f32 v103, v103, s25, v218
	v_cvt_pk_fp8_f32 v109, v104, v103 op_sel:[0,0,1]
	v_mul_f32_e32 v103, 0x45000000, v80
	v_mul_f32_e32 v104, 0x45000000, v84
	v_med3_f32 v103, v103, s25, v218
	v_med3_f32 v104, v104, s25, v218
	v_cvt_pk_fp8_f32 v110, v103, v104
	v_mul_f32_e32 v105, 0x45000000, v88
	v_mul_f32_e32 v103, 0x45000000, v92
	v_med3_f32 v104, v105, s25, v218
	v_med3_f32 v103, v103, s25, v218
	v_cvt_pk_fp8_f32 v110, v104, v103 op_sel:[0,0,1]
	v_mul_f32_e32 v104, 0x45000000, v81
	v_mul_f32_e32 v105, 0x45000000, v85
	v_med3_f32 v104, v104, s25, v218
	v_med3_f32 v105, v105, s25, v218
	v_cvt_pk_fp8_f32 v112, v104, v105
	v_mul_f32_e32 v111, 0x45000000, v89
	v_mul_f32_e32 v104, 0x45000000, v93
	v_med3_f32 v105, v111, s25, v218
	v_med3_f32 v104, v104, s25, v218
	v_cvt_pk_fp8_f32 v112, v105, v104 op_sel:[0,0,1]
	v_mul_f32_e32 v104, 0x45000000, v82
	v_mul_f32_e32 v105, 0x45000000, v86
	v_med3_f32 v104, v104, s25, v218
	v_med3_f32 v105, v105, s25, v218
	v_cvt_pk_fp8_f32 v114, v104, v105
	v_mul_f32_e32 v111, 0x45000000, v90
	v_mul_f32_e32 v104, 0x45000000, v94
	v_med3_f32 v105, v111, s25, v218
	v_med3_f32 v104, v104, s25, v218
	v_cvt_pk_fp8_f32 v114, v105, v104 op_sel:[0,0,1]
	v_mul_f32_e32 v104, 0x45000000, v83
	v_mul_f32_e32 v105, 0x45000000, v87
	v_med3_f32 v104, v104, s25, v218
	v_med3_f32 v105, v105, s25, v218
	v_cvt_pk_fp8_f32 v115, v104, v105
	v_mul_f32_e32 v111, 0x45000000, v91
	v_mul_f32_e32 v104, 0x45000000, v95
	v_med3_f32 v105, v111, s25, v218
	v_med3_f32 v104, v104, s25, v218
	v_add_u32_e32 v103, 0x8c00, v102
	v_cvt_pk_fp8_f32 v115, v105, v104 op_sel:[0,0,1]
	ds_write2_b32 v103, v106, v110 offset1:16
	ds_write2_b32 v103, v107, v112 offset0:34 offset1:50
	ds_write2_b32 v103, v108, v114 offset0:68 offset1:84
	ds_write2_b32 v103, v109, v115 offset0:102 offset1:118
	s_waitcnt lgkmcnt(0)
	s_barrier
	v_add_u32_e32 v103, 0x8c00, v101
	v_add_u32_e32 v108, 0x8c10, v101
	ds_read2_b64 v[104:107], v103 offset1:1
	ds_read2_b64 v[108:111], v108 offset1:1
	v_add_u32_e32 v103, s6, v97
	v_mov_b64_e32 v[114:115], s[2:3]
	v_mad_i64_i32 v[114:115], s[2:3], s4, v103, v[114:115]
	v_lshl_add_u64 v[114:115], v[114:115], 0, s[96:97]
	v_lshl_add_u64 v[114:115], v[114:115], 0, v[98:99]
	s_waitcnt lgkmcnt(1)
	global_store_dwordx4 v[114:115], v[104:107], off
	s_waitcnt lgkmcnt(0)
	global_store_dwordx4 v[114:115], v[108:111], off offset:16

.LBB0_671:
	s_waitcnt vmcnt(7)
	v_mul_f32_e32 v103, 0x45000000, v0
	s_waitcnt vmcnt(6)
	v_mul_f32_e32 v104, 0x45000000, v4
	v_med3_f32 v103, v103, s25, v218
	v_med3_f32 v104, v104, s25, v218
	v_cvt_pk_fp8_f32 v106, v103, v104
	s_waitcnt vmcnt(5)
	v_mul_f32_e32 v105, 0x45000000, v8
	s_waitcnt vmcnt(4)
	v_mul_f32_e32 v103, 0x45000000, v12
	v_med3_f32 v104, v105, s25, v218
	v_med3_f32 v103, v103, s25, v218
	v_cvt_pk_fp8_f32 v106, v104, v103 op_sel:[0,0,1]
	v_mul_f32_e32 v103, 0x45000000, v1
	v_mul_f32_e32 v104, 0x45000000, v5
	v_med3_f32 v103, v103, s25, v218
	v_med3_f32 v104, v104, s25, v218
	v_cvt_pk_fp8_f32 v107, v103, v104
	v_mul_f32_e32 v105, 0x45000000, v9
	v_mul_f32_e32 v103, 0x45000000, v13
	v_med3_f32 v104, v105, s25, v218
	v_med3_f32 v103, v103, s25, v218
	v_cvt_pk_fp8_f32 v107, v104, v103 op_sel:[0,0,1]
	v_mul_f32_e32 v103, 0x45000000, v2
	v_mul_f32_e32 v104, 0x45000000, v6
	v_med3_f32 v103, v103, s25, v218
	v_med3_f32 v104, v104, s25, v218
	v_cvt_pk_fp8_f32 v108, v103, v104
	v_mul_f32_e32 v105, 0x45000000, v10
	v_mul_f32_e32 v103, 0x45000000, v14
	v_med3_f32 v104, v105, s25, v218
	v_med3_f32 v103, v103, s25, v218
	v_cvt_pk_fp8_f32 v108, v104, v103 op_sel:[0,0,1]
	v_mul_f32_e32 v103, 0x45000000, v3
	v_mul_f32_e32 v104, 0x45000000, v7
	v_med3_f32 v103, v103, s25, v218
	v_med3_f32 v104, v104, s25, v218
	v_cvt_pk_fp8_f32 v109, v103, v104
	v_mul_f32_e32 v105, 0x45000000, v11
	v_mul_f32_e32 v103, 0x45000000, v15
	v_med3_f32 v104, v105, s25, v218
	v_med3_f32 v103, v103, s25, v218
	v_cvt_pk_fp8_f32 v109, v104, v103 op_sel:[0,0,1]
	s_waitcnt vmcnt(3)
	v_mul_f32_e32 v103, 0x45000000, v16
	s_waitcnt vmcnt(2)
	v_mul_f32_e32 v104, 0x45000000, v20
	v_med3_f32 v103, v103, s25, v218
	v_med3_f32 v104, v104, s25, v218
	v_cvt_pk_fp8_f32 v110, v103, v104
	s_waitcnt vmcnt(1)
	v_mul_f32_e32 v105, 0x45000000, v24
	s_waitcnt vmcnt(0)
	v_mul_f32_e32 v103, 0x45000000, v28
	v_med3_f32 v104, v105, s25, v218
	v_med3_f32 v103, v103, s25, v218
	v_cvt_pk_fp8_f32 v110, v104, v103 op_sel:[0,0,1]
	v_mul_f32_e32 v104, 0x45000000, v17
	v_mul_f32_e32 v105, 0x45000000, v21
	v_med3_f32 v104, v104, s25, v218
	v_med3_f32 v105, v105, s25, v218
	v_cvt_pk_fp8_f32 v112, v104, v105
	v_mul_f32_e32 v111, 0x45000000, v25
	v_mul_f32_e32 v104, 0x45000000, v29
	v_med3_f32 v105, v111, s25, v218
	v_med3_f32 v104, v104, s25, v218
	v_cvt_pk_fp8_f32 v112, v105, v104 op_sel:[0,0,1]
	v_mul_f32_e32 v104, 0x45000000, v18
	v_mul_f32_e32 v105, 0x45000000, v22
	v_med3_f32 v104, v104, s25, v218
	v_med3_f32 v105, v105, s25, v218
	v_cvt_pk_fp8_f32 v114, v104, v105
	v_mul_f32_e32 v111, 0x45000000, v26
	v_mul_f32_e32 v104, 0x45000000, v30
	v_med3_f32 v105, v111, s25, v218
	v_med3_f32 v104, v104, s25, v218
	v_cvt_pk_fp8_f32 v114, v105, v104 op_sel:[0,0,1]
	v_mul_f32_e32 v104, 0x45000000, v19
	v_mul_f32_e32 v105, 0x45000000, v23
	v_med3_f32 v104, v104, s25, v218
	v_med3_f32 v105, v105, s25, v218
	v_cvt_pk_fp8_f32 v115, v104, v105
	v_mul_f32_e32 v111, 0x45000000, v27
	v_mul_f32_e32 v104, 0x45000000, v31
	v_med3_f32 v105, v111, s25, v218
	v_med3_f32 v104, v104, s25, v218
	v_add_u32_e32 v103, 0x400, v102
	v_cvt_pk_fp8_f32 v115, v105, v104 op_sel:[0,0,1]
	ds_write2_b32 v103, v106, v110 offset1:16
	ds_write2_b32 v103, v107, v112 offset0:34 offset1:50
	ds_write2_b32 v103, v108, v114 offset0:68 offset1:84
	ds_write2_b32 v103, v109, v115 offset0:102 offset1:118
	s_waitcnt lgkmcnt(0)
	s_barrier
	ds_read2_b64 v[104:107], v101 offset0:128 offset1:129
	ds_read2_b64 v[108:111], v101 offset0:130 offset1:131
	v_add_u32_e32 v103, s8, v97
	v_mov_b64_e32 v[114:115], s[4:5]
	v_mad_i64_i32 v[114:115], s[4:5], s6, v103, v[114:115]
	v_lshl_add_u64 v[114:115], v[114:115], 0, s[96:97]
	s_add_i32 s4, s50, 1
	v_lshl_add_u64 v[114:115], v[114:115], 0, v[98:99]
	s_cmp_ge_i32 s4, s15
	s_waitcnt lgkmcnt(1)
	global_store_dwordx4 v[114:115], v[104:107], off
	s_waitcnt lgkmcnt(0)
	global_store_dwordx4 v[114:115], v[108:111], off offset:16
	s_cbranch_scc1 .LBB0_683
	s_cmp_ge_i32 s50, s21
	s_cbranch_scc1 .LBB0_678
	s_add_i32 s51, s22, s24
	s_cmpk_gt_i32 s51, 0x3fff
	s_mov_b64 s[10:11], -1
	s_cbranch_scc0 .LBB0_675
	s_add_i32 s4, s51, 0xffffc000
	s_lshr_b32 s96, s4, 7
	s_add_i32 s4, s28, s46
	s_add_i32 s5, s35, s45
	s_and_b32 s4, s4, 0x380
	s_and_b32 s5, s5, 0x780
	s_mov_b64 s[10:11], 0
	s_mov_b64 s[8:9], s[96:97]

.LBB0_682:
	v_mul_f32_e32 v103, 0x45000000, v32
	v_mul_f32_e32 v104, 0x45000000, v36
	v_med3_f32 v103, v103, s25, v218
	v_med3_f32 v104, v104, s25, v218
	v_cvt_pk_fp8_f32 v106, v103, v104
	v_mul_f32_e32 v105, 0x45000000, v40
	v_mul_f32_e32 v103, 0x45000000, v44
	v_med3_f32 v104, v105, s25, v218
	v_med3_f32 v103, v103, s25, v218
	v_cvt_pk_fp8_f32 v106, v104, v103 op_sel:[0,0,1]
	v_mul_f32_e32 v103, 0x45000000, v33
	v_mul_f32_e32 v104, 0x45000000, v37
	v_med3_f32 v103, v103, s25, v218
	v_med3_f32 v104, v104, s25, v218
	v_cvt_pk_fp8_f32 v107, v103, v104
	v_mul_f32_e32 v105, 0x45000000, v41
	v_mul_f32_e32 v103, 0x45000000, v45
	v_med3_f32 v104, v105, s25, v218
	v_med3_f32 v103, v103, s25, v218
	v_cvt_pk_fp8_f32 v107, v104, v103 op_sel:[0,0,1]
	v_mul_f32_e32 v103, 0x45000000, v34
	v_mul_f32_e32 v104, 0x45000000, v38
	v_med3_f32 v103, v103, s25, v218
	v_med3_f32 v104, v104, s25, v218
	v_cvt_pk_fp8_f32 v108, v103, v104
	v_mul_f32_e32 v105, 0x45000000, v42
	v_mul_f32_e32 v103, 0x45000000, v46
	v_med3_f32 v104, v105, s25, v218
	v_med3_f32 v103, v103, s25, v218
	v_cvt_pk_fp8_f32 v108, v104, v103 op_sel:[0,0,1]
	v_mul_f32_e32 v103, 0x45000000, v35
	v_mul_f32_e32 v104, 0x45000000, v39
	v_med3_f32 v103, v103, s25, v218
	v_med3_f32 v104, v104, s25, v218
	v_cvt_pk_fp8_f32 v109, v103, v104
	v_mul_f32_e32 v105, 0x45000000, v43
	v_mul_f32_e32 v103, 0x45000000, v47
	v_med3_f32 v104, v105, s25, v218
	v_med3_f32 v103, v103, s25, v218
	v_cvt_pk_fp8_f32 v109, v104, v103 op_sel:[0,0,1]
	v_mul_f32_e32 v103, 0x45000000, v48
	v_mul_f32_e32 v104, 0x45000000, v52
	v_med3_f32 v103, v103, s25, v218
	v_med3_f32 v104, v104, s25, v218
	v_cvt_pk_fp8_f32 v110, v103, v104
	v_mul_f32_e32 v105, 0x45000000, v56
	v_mul_f32_e32 v103, 0x45000000, v60
	v_med3_f32 v104, v105, s25, v218
	v_med3_f32 v103, v103, s25, v218
	v_cvt_pk_fp8_f32 v110, v104, v103 op_sel:[0,0,1]
	v_mul_f32_e32 v104, 0x45000000, v49
	v_mul_f32_e32 v105, 0x45000000, v53
	v_med3_f32 v104, v104, s25, v218
	v_med3_f32 v105, v105, s25, v218
	v_cvt_pk_fp8_f32 v112, v104, v105
	v_mul_f32_e32 v111, 0x45000000, v57
	v_mul_f32_e32 v104, 0x45000000, v61
	v_med3_f32 v105, v111, s25, v218
	v_med3_f32 v104, v104, s25, v218
	v_cvt_pk_fp8_f32 v112, v105, v104 op_sel:[0,0,1]
	v_mul_f32_e32 v104, 0x45000000, v50
	v_mul_f32_e32 v105, 0x45000000, v54
	v_med3_f32 v104, v104, s25, v218
	v_med3_f32 v105, v105, s25, v218
	v_cvt_pk_fp8_f32 v114, v104, v105
	v_mul_f32_e32 v111, 0x45000000, v58
	v_mul_f32_e32 v104, 0x45000000, v62
	v_med3_f32 v105, v111, s25, v218
	v_med3_f32 v104, v104, s25, v218
	v_cvt_pk_fp8_f32 v114, v105, v104 op_sel:[0,0,1]
	v_mul_f32_e32 v104, 0x45000000, v51
	v_mul_f32_e32 v105, 0x45000000, v55
	v_med3_f32 v104, v104, s25, v218
	v_med3_f32 v105, v105, s25, v218
	v_cvt_pk_fp8_f32 v115, v104, v105
	v_mul_f32_e32 v111, 0x45000000, v59
	v_mul_f32_e32 v104, 0x45000000, v63
	v_med3_f32 v105, v111, s25, v218
	v_med3_f32 v104, v104, s25, v218
	v_add_u32_e32 v103, 0x4800, v102
	v_cvt_pk_fp8_f32 v115, v105, v104 op_sel:[0,0,1]
	ds_write2_b32 v103, v106, v110 offset1:16
	ds_write2_b32 v103, v107, v112 offset0:34 offset1:50
	ds_write2_b32 v103, v108, v114 offset0:68 offset1:84
	ds_write2_b32 v103, v109, v115 offset0:102 offset1:118
	s_waitcnt lgkmcnt(0)
	s_barrier
	v_add_u32_e32 v103, 0x4800, v101
	v_add_u32_e32 v108, 0x4810, v101
	ds_read2_b64 v[104:107], v103 offset1:1
	ds_read2_b64 v[108:111], v108 offset1:1
	v_add_u32_e32 v103, s8, v97
	v_mov_b64_e32 v[114:115], s[4:5]
	v_mad_i64_i32 v[114:115], s[4:5], s6, v103, v[114:115]
	v_lshl_add_u64 v[114:115], v[114:115], 0, s[96:97]
	v_lshl_add_u64 v[114:115], v[114:115], 0, v[98:99]
	s_waitcnt lgkmcnt(1)
	global_store_dwordx4 v[114:115], v[104:107], off
	s_waitcnt lgkmcnt(0)
	global_store_dwordx4 v[114:115], v[108:111], off offset:16

.LBB0_844:
	s_waitcnt vmcnt(7)
	v_mul_f32_e32 v103, 0x45000000, v0
	s_waitcnt vmcnt(6)
	v_mul_f32_e32 v104, 0x45000000, v4
	v_med3_f32 v103, v103, s25, v218
	v_med3_f32 v104, v104, s25, v218
	v_cvt_pk_fp8_f32 v106, v103, v104
	s_waitcnt vmcnt(5)
	v_mul_f32_e32 v105, 0x45000000, v8
	s_waitcnt vmcnt(4)
	v_mul_f32_e32 v103, 0x45000000, v12
	v_med3_f32 v104, v105, s25, v218
	v_med3_f32 v103, v103, s25, v218
	v_cvt_pk_fp8_f32 v106, v104, v103 op_sel:[0,0,1]
	v_mul_f32_e32 v103, 0x45000000, v1
	v_mul_f32_e32 v104, 0x45000000, v5
	v_med3_f32 v103, v103, s25, v218
	v_med3_f32 v104, v104, s25, v218
	v_cvt_pk_fp8_f32 v107, v103, v104
	v_mul_f32_e32 v105, 0x45000000, v9
	v_mul_f32_e32 v103, 0x45000000, v13
	v_med3_f32 v104, v105, s25, v218
	v_med3_f32 v103, v103, s25, v218
	v_cvt_pk_fp8_f32 v107, v104, v103 op_sel:[0,0,1]
	v_mul_f32_e32 v103, 0x45000000, v2
	v_mul_f32_e32 v104, 0x45000000, v6
	v_med3_f32 v103, v103, s25, v218
	v_med3_f32 v104, v104, s25, v218
	v_cvt_pk_fp8_f32 v108, v103, v104
	v_mul_f32_e32 v105, 0x45000000, v10
	v_mul_f32_e32 v103, 0x45000000, v14
	v_med3_f32 v104, v105, s25, v218
	v_med3_f32 v103, v103, s25, v218
	v_cvt_pk_fp8_f32 v108, v104, v103 op_sel:[0,0,1]
	v_mul_f32_e32 v103, 0x45000000, v3
	v_mul_f32_e32 v104, 0x45000000, v7
	v_med3_f32 v103, v103, s25, v218
	v_med3_f32 v104, v104, s25, v218
	v_cvt_pk_fp8_f32 v109, v103, v104
	v_mul_f32_e32 v105, 0x45000000, v11
	v_mul_f32_e32 v103, 0x45000000, v15
	v_med3_f32 v104, v105, s25, v218
	v_med3_f32 v103, v103, s25, v218
	v_cvt_pk_fp8_f32 v109, v104, v103 op_sel:[0,0,1]
	s_waitcnt vmcnt(3)
	v_mul_f32_e32 v103, 0x45000000, v16
	s_waitcnt vmcnt(2)
	v_mul_f32_e32 v104, 0x45000000, v20
	v_med3_f32 v103, v103, s25, v218
	v_med3_f32 v104, v104, s25, v218
	v_cvt_pk_fp8_f32 v110, v103, v104
	s_waitcnt vmcnt(1)
	v_mul_f32_e32 v105, 0x45000000, v24
	s_waitcnt vmcnt(0)
	v_mul_f32_e32 v103, 0x45000000, v28
	v_med3_f32 v104, v105, s25, v218
	v_med3_f32 v103, v103, s25, v218
	v_cvt_pk_fp8_f32 v110, v104, v103 op_sel:[0,0,1]
	v_mul_f32_e32 v104, 0x45000000, v17
	v_mul_f32_e32 v105, 0x45000000, v21
	v_med3_f32 v104, v104, s25, v218
	v_med3_f32 v105, v105, s25, v218
	v_cvt_pk_fp8_f32 v112, v104, v105
	v_mul_f32_e32 v111, 0x45000000, v25
	v_mul_f32_e32 v104, 0x45000000, v29
	v_med3_f32 v105, v111, s25, v218
	v_med3_f32 v104, v104, s25, v218
	v_cvt_pk_fp8_f32 v112, v105, v104 op_sel:[0,0,1]
	v_mul_f32_e32 v104, 0x45000000, v18
	v_mul_f32_e32 v105, 0x45000000, v22
	v_med3_f32 v104, v104, s25, v218
	v_med3_f32 v105, v105, s25, v218
	v_cvt_pk_fp8_f32 v114, v104, v105
	v_mul_f32_e32 v111, 0x45000000, v26
	v_mul_f32_e32 v104, 0x45000000, v30
	v_med3_f32 v105, v111, s25, v218
	v_med3_f32 v104, v104, s25, v218
	v_cvt_pk_fp8_f32 v114, v105, v104 op_sel:[0,0,1]
	v_mul_f32_e32 v104, 0x45000000, v19
	v_mul_f32_e32 v105, 0x45000000, v23
	v_med3_f32 v104, v104, s25, v218
	v_med3_f32 v105, v105, s25, v218
	v_cvt_pk_fp8_f32 v115, v104, v105
	v_mul_f32_e32 v111, 0x45000000, v27
	v_mul_f32_e32 v104, 0x45000000, v31
	v_med3_f32 v105, v111, s25, v218
	v_med3_f32 v104, v104, s25, v218
	v_add_u32_e32 v103, 0x400, v102
	v_cvt_pk_fp8_f32 v115, v105, v104 op_sel:[0,0,1]
	ds_write2_b32 v103, v106, v110 offset1:16
	ds_write2_b32 v103, v107, v112 offset0:34 offset1:50
	ds_write2_b32 v103, v108, v114 offset0:68 offset1:84
	ds_write2_b32 v103, v109, v115 offset0:102 offset1:118
	s_waitcnt lgkmcnt(0)
	s_barrier
	ds_read2_b64 v[104:107], v101 offset0:128 offset1:129
	ds_read2_b64 v[108:111], v101 offset0:130 offset1:131
	v_add_u32_e32 v103, s8, v97
	v_mov_b64_e32 v[114:115], s[4:5]
	v_mad_i64_i32 v[114:115], s[4:5], s6, v103, v[114:115]
	v_lshl_add_u64 v[114:115], v[114:115], 0, s[96:97]
	s_add_i32 s4, s15, 1
	v_lshl_add_u64 v[114:115], v[114:115], 0, v[98:99]
	s_cmp_ge_i32 s4, s16
	s_waitcnt lgkmcnt(1)
	global_store_dwordx4 v[114:115], v[104:107], off
	s_waitcnt lgkmcnt(0)
	global_store_dwordx4 v[114:115], v[108:111], off offset:16
	s_cbranch_scc1 .LBB0_856
	s_cmp_ge_i32 s15, s21
	s_cbranch_scc1 .LBB0_851
	s_add_i32 s53, s13, s46
	s_cmpk_gt_i32 s53, 0x3fff
	s_mov_b64 s[10:11], -1
	s_cbranch_scc0 .LBB0_848
	s_add_i32 s4, s53, 0xffffc000
	s_lshr_b32 s96, s4, 7
	s_add_i32 s4, s24, s48
	s_add_i32 s5, s31, s47
	s_and_b32 s4, s4, 0x380
	s_and_b32 s5, s5, 0x780
	s_mov_b64 s[10:11], 0
	s_mov_b64 s[8:9], s[96:97]

.LBB0_1139:
	s_waitcnt vmcnt(7)
	v_mul_f32_e32 v103, 0x45000000, v0
	s_waitcnt vmcnt(6)
	v_mul_f32_e32 v104, 0x45000000, v4
	v_med3_f32 v103, v103, s25, v218
	v_med3_f32 v104, v104, s25, v218
	v_cvt_pk_fp8_f32 v106, v103, v104
	s_waitcnt vmcnt(5)
	v_mul_f32_e32 v105, 0x45000000, v8
	s_waitcnt vmcnt(4)
	v_mul_f32_e32 v103, 0x45000000, v12
	v_med3_f32 v104, v105, s25, v218
	v_med3_f32 v103, v103, s25, v218
	v_cvt_pk_fp8_f32 v106, v104, v103 op_sel:[0,0,1]
	v_mul_f32_e32 v103, 0x45000000, v1
	v_mul_f32_e32 v104, 0x45000000, v5
	v_med3_f32 v103, v103, s25, v218
	v_med3_f32 v104, v104, s25, v218
	v_cvt_pk_fp8_f32 v107, v103, v104
	v_mul_f32_e32 v105, 0x45000000, v9
	v_mul_f32_e32 v103, 0x45000000, v13
	v_med3_f32 v104, v105, s25, v218
	v_med3_f32 v103, v103, s25, v218
	v_cvt_pk_fp8_f32 v107, v104, v103 op_sel:[0,0,1]
	v_mul_f32_e32 v103, 0x45000000, v2
	v_mul_f32_e32 v104, 0x45000000, v6
	v_med3_f32 v103, v103, s25, v218
	v_med3_f32 v104, v104, s25, v218
	v_cvt_pk_fp8_f32 v108, v103, v104
	v_mul_f32_e32 v105, 0x45000000, v10
	v_mul_f32_e32 v103, 0x45000000, v14
	v_med3_f32 v104, v105, s25, v218
	v_med3_f32 v103, v103, s25, v218
	v_cvt_pk_fp8_f32 v108, v104, v103 op_sel:[0,0,1]
	v_mul_f32_e32 v103, 0x45000000, v3
	v_mul_f32_e32 v104, 0x45000000, v7
	v_med3_f32 v103, v103, s25, v218
	v_med3_f32 v104, v104, s25, v218
	v_cvt_pk_fp8_f32 v109, v103, v104
	v_mul_f32_e32 v105, 0x45000000, v11
	v_mul_f32_e32 v103, 0x45000000, v15
	v_med3_f32 v104, v105, s25, v218
	v_med3_f32 v103, v103, s25, v218
	v_cvt_pk_fp8_f32 v109, v104, v103 op_sel:[0,0,1]
	s_waitcnt vmcnt(3)
	v_mul_f32_e32 v103, 0x45000000, v16
	s_waitcnt vmcnt(2)
	v_mul_f32_e32 v104, 0x45000000, v20
	v_med3_f32 v103, v103, s25, v218
	v_med3_f32 v104, v104, s25, v218
	v_cvt_pk_fp8_f32 v110, v103, v104
	s_waitcnt vmcnt(1)
	v_mul_f32_e32 v105, 0x45000000, v24
	s_waitcnt vmcnt(0)
	v_mul_f32_e32 v103, 0x45000000, v28
	v_med3_f32 v104, v105, s25, v218
	v_med3_f32 v103, v103, s25, v218
	v_cvt_pk_fp8_f32 v110, v104, v103 op_sel:[0,0,1]
	v_mul_f32_e32 v104, 0x45000000, v17
	v_mul_f32_e32 v105, 0x45000000, v21
	v_med3_f32 v104, v104, s25, v218
	v_med3_f32 v105, v105, s25, v218
	v_cvt_pk_fp8_f32 v112, v104, v105
	v_mul_f32_e32 v111, 0x45000000, v25
	v_mul_f32_e32 v104, 0x45000000, v29
	v_med3_f32 v105, v111, s25, v218
	v_med3_f32 v104, v104, s25, v218
	v_cvt_pk_fp8_f32 v112, v105, v104 op_sel:[0,0,1]
	v_mul_f32_e32 v104, 0x45000000, v18
	v_mul_f32_e32 v105, 0x45000000, v22
	v_med3_f32 v104, v104, s25, v218
	v_med3_f32 v105, v105, s25, v218
	v_cvt_pk_fp8_f32 v114, v104, v105
	v_mul_f32_e32 v111, 0x45000000, v26
	v_mul_f32_e32 v104, 0x45000000, v30
	v_med3_f32 v105, v111, s25, v218
	v_med3_f32 v104, v104, s25, v218
	v_cvt_pk_fp8_f32 v114, v105, v104 op_sel:[0,0,1]
	v_mul_f32_e32 v104, 0x45000000, v19
	v_mul_f32_e32 v105, 0x45000000, v23
	v_med3_f32 v104, v104, s25, v218
	v_med3_f32 v105, v105, s25, v218
	v_cvt_pk_fp8_f32 v115, v104, v105
	v_mul_f32_e32 v111, 0x45000000, v27
	v_mul_f32_e32 v104, 0x45000000, v31
	v_med3_f32 v105, v111, s25, v218
	v_med3_f32 v104, v104, s25, v218
	v_add_u32_e32 v103, 0x400, v102
	v_cvt_pk_fp8_f32 v115, v105, v104 op_sel:[0,0,1]
	ds_write2_b32 v103, v106, v110 offset1:16
	ds_write2_b32 v103, v107, v112 offset0:34 offset1:50
	ds_write2_b32 v103, v108, v114 offset0:68 offset1:84
	ds_write2_b32 v103, v109, v115 offset0:102 offset1:118
	s_waitcnt lgkmcnt(0)
	s_barrier
	ds_read2_b64 v[104:107], v101 offset0:128 offset1:129
	ds_read2_b64 v[108:111], v101 offset0:130 offset1:131
	v_add_u32_e32 v103, s8, v97
	v_mov_b64_e32 v[114:115], s[4:5]
	v_mad_i64_i32 v[114:115], s[4:5], s6, v103, v[114:115]
	v_lshl_add_u64 v[114:115], v[114:115], 0, s[96:97]
	s_add_i32 s4, s39, -3
	v_lshl_add_u64 v[114:115], v[114:115], 0, v[98:99]
	s_cmp_ge_i32 s4, s15
	s_waitcnt lgkmcnt(1)
	global_store_dwordx4 v[114:115], v[104:107], off
	s_waitcnt lgkmcnt(0)
	global_store_dwordx4 v[114:115], v[108:111], off offset:16
	s_cbranch_scc1 .LBB0_1151
	s_add_i32 s4, s39, -1
	s_cmp_ge_i32 s4, s15
	s_cbranch_scc1 .LBB0_1146
	s_add_i32 s52, s13, s41
	s_cmpk_gt_i32 s52, 0x3fff
	s_mov_b64 s[10:11], -1
	s_cbranch_scc0 .LBB0_1143
	s_add_i32 s4, s52, 0xffffc000
	s_lshr_b32 s96, s4, 7
	s_add_i32 s4, s22, s47
	s_add_i32 s5, s28, s46
	s_and_b32 s4, s4, 0x380
	s_and_b32 s5, s5, 0x780
	s_mov_b64 s[10:11], 0
	s_mov_b64 s[8:9], s[96:97]

.LBB0_1230:
	s_mul_i32 s0, s5, s2
	s_add_i32 s5, s4, s0
	s_and_b64 s[0:1], s[40:41], exec
	s_cselect_b32 s6, s2, s3
	s_add_i32 s0, s6, -1
	v_min_i32_e32 v0, s0, v147
	v_max_i32_e32 v0, 0, v0
	v_add_u32_e32 v0, s5, v0
	v_min_i32_e32 v0, s12, v0
	v_min_i32_e32 v1, 0x8000, v0
	v_ashrrev_i32_e32 v112, 11, v1
	v_ashrrev_i32_e32 v1, 31, v0
	v_lshlrev_b64 v[130:131], 10, v[0:1]
	v_lshlrev_b64 v[0:1], 11, v[0:1]
	v_lshl_add_u64 v[0:1], v[138:139], 0, v[0:1]
	global_load_dwordx4 v[126:129], v[0:1], off
	global_load_dwordx4 v[122:125], v[0:1], off offset:64
	global_load_dwordx4 v[118:121], v[0:1], off offset:128
	global_load_dwordx4 v[114:117], v[0:1], off offset:192
	global_load_dwordx4 v[108:111], v[0:1], off offset:256
	global_load_dwordx4 v[104:107], v[0:1], off offset:320
	global_load_dwordx4 v[100:103], v[0:1], off offset:384
	global_load_dwordx4 v[96:99], v[0:1], off offset:448
	global_load_dwordx4 v[92:95], v[0:1], off offset:512
	global_load_dwordx4 v[88:91], v[0:1], off offset:576
	global_load_dwordx4 v[84:87], v[0:1], off offset:640
	global_load_dwordx4 v[80:83], v[0:1], off offset:704
	global_load_dwordx4 v[76:79], v[0:1], off offset:768
	global_load_dwordx4 v[72:75], v[0:1], off offset:832
	global_load_dwordx4 v[68:71], v[0:1], off offset:896
	global_load_dwordx4 v[64:67], v[0:1], off offset:960
	global_load_dwordx4 v[60:63], v[0:1], off offset:1024
	global_load_dwordx4 v[56:59], v[0:1], off offset:1088
	global_load_dwordx4 v[52:55], v[0:1], off offset:1152
	global_load_dwordx4 v[48:51], v[0:1], off offset:1216
	global_load_dwordx4 v[44:47], v[0:1], off offset:1280
	global_load_dwordx4 v[40:43], v[0:1], off offset:1344
	global_load_dwordx4 v[36:39], v[0:1], off offset:1408
	global_load_dwordx4 v[32:35], v[0:1], off offset:1472
	global_load_dwordx4 v[28:31], v[0:1], off offset:1536
	global_load_dwordx4 v[24:27], v[0:1], off offset:1600
	global_load_dwordx4 v[20:23], v[0:1], off offset:1664
	global_load_dwordx4 v[16:19], v[0:1], off offset:1728
	global_load_dwordx4 v[12:15], v[0:1], off offset:1792
	global_load_dwordx4 v[8:11], v[0:1], off offset:1856
	global_load_dwordx4 v[4:7], v[0:1], off offset:1920
	s_waitcnt lgkmcnt(0)
	global_load_dwordx4 v[0:3], v[0:1], off offset:1984
	v_cmp_lt_i32_e32 vcc, s5, v149
	v_cmp_gt_i32_e64 s[38:39], s6, v147
	s_and_b64 s[42:43], s[38:39], vcc
	v_cmp_eq_u32_e64 s[38:39], v112, v146
	s_waitcnt vmcnt(31)
	v_and_b32_e32 v133, 0xffff0000, v126
	v_lshlrev_b32_e32 v132, 16, v126
	v_mul_f32_e32 v133, v133, v133
	v_lshlrev_b32_e32 v134, 16, v127
	v_fmac_f32_e32 v133, v132, v132
	v_fmac_f32_e32 v133, v134, v134
	s_waitcnt vmcnt(30)
	v_and_b32_e32 v134, 0xffff0000, v122
	v_and_b32_e32 v135, 0xffff0000, v127
	v_lshlrev_b32_e32 v132, 16, v122
	v_mul_f32_e32 v134, v134, v134
	v_lshlrev_b32_e32 v136, 16, v128
	v_fmac_f32_e32 v133, v135, v135
	v_lshlrev_b32_e32 v135, 16, v123
	v_fmac_f32_e32 v134, v132, v132
	v_and_b32_e32 v137, 0xffff0000, v128
	v_fmac_f32_e32 v133, v136, v136
	v_and_b32_e32 v136, 0xffff0000, v123
	v_fmac_f32_e32 v134, v135, v135
	v_lshlrev_b32_e32 v144, 16, v129
	v_fmac_f32_e32 v133, v137, v137
	v_lshlrev_b32_e32 v137, 16, v124
	v_fmac_f32_e32 v134, v136, v136
	v_and_b32_e32 v145, 0xffff0000, v129
	v_fmac_f32_e32 v133, v144, v144
	v_and_b32_e32 v144, 0xffff0000, v124
	v_fmac_f32_e32 v134, v137, v137
	v_fmac_f32_e32 v133, v145, v145
	v_lshlrev_b32_e32 v145, 16, v125
	v_fmac_f32_e32 v134, v144, v144
	v_and_b32_e32 v162, 0xffff0000, v125
	v_fmac_f32_e32 v134, v145, v145
	v_fmac_f32_e32 v134, v162, v162
	v_add_f32_e32 v132, v133, v134
	s_waitcnt vmcnt(29)
	v_and_b32_e32 v134, 0xffff0000, v118
	v_lshlrev_b32_e32 v133, 16, v118
	v_mul_f32_e32 v134, v134, v134
	v_lshlrev_b32_e32 v135, 16, v119
	v_fmac_f32_e32 v134, v133, v133
	v_and_b32_e32 v136, 0xffff0000, v119
	v_fmac_f32_e32 v134, v135, v135
	v_lshlrev_b32_e32 v137, 16, v120
	v_fmac_f32_e32 v134, v136, v136
	v_and_b32_e32 v144, 0xffff0000, v120
	v_fmac_f32_e32 v134, v137, v137
	v_lshlrev_b32_e32 v145, 16, v121
	v_fmac_f32_e32 v134, v144, v144
	v_and_b32_e32 v162, 0xffff0000, v121
	v_fmac_f32_e32 v134, v145, v145
	v_fmac_f32_e32 v134, v162, v162
	v_add_f32_e32 v132, v132, v134
	s_waitcnt vmcnt(28)
	v_and_b32_e32 v134, 0xffff0000, v114
	v_lshlrev_b32_e32 v133, 16, v114
	v_mul_f32_e32 v134, v134, v134
	v_lshlrev_b32_e32 v135, 16, v115
	v_fmac_f32_e32 v134, v133, v133
	v_and_b32_e32 v136, 0xffff0000, v115
	v_fmac_f32_e32 v134, v135, v135
	v_lshlrev_b32_e32 v137, 16, v116
	v_fmac_f32_e32 v134, v136, v136
	v_and_b32_e32 v144, 0xffff0000, v116
	v_fmac_f32_e32 v134, v137, v137
	v_lshlrev_b32_e32 v145, 16, v117
	v_fmac_f32_e32 v134, v144, v144
	v_and_b32_e32 v162, 0xffff0000, v117
	v_fmac_f32_e32 v134, v145, v145
	v_fmac_f32_e32 v134, v162, v162
	v_add_f32_e32 v132, v132, v134
	s_waitcnt vmcnt(27)
	v_and_b32_e32 v134, 0xffff0000, v108
	v_lshlrev_b32_e32 v133, 16, v108
	v_mul_f32_e32 v134, v134, v134
	v_lshlrev_b32_e32 v135, 16, v109
	v_fmac_f32_e32 v134, v133, v133
	v_and_b32_e32 v136, 0xffff0000, v109
	v_fmac_f32_e32 v134, v135, v135
	v_lshlrev_b32_e32 v137, 16, v110
	v_fmac_f32_e32 v134, v136, v136
	v_and_b32_e32 v144, 0xffff0000, v110
	v_fmac_f32_e32 v134, v137, v137
	v_lshlrev_b32_e32 v145, 16, v111
	v_fmac_f32_e32 v134, v144, v144
	v_and_b32_e32 v162, 0xffff0000, v111
	v_fmac_f32_e32 v134, v145, v145
	v_fmac_f32_e32 v134, v162, v162
	v_add_f32_e32 v132, v132, v134
	s_waitcnt vmcnt(26)
	v_and_b32_e32 v134, 0xffff0000, v104
	v_lshlrev_b32_e32 v133, 16, v104
	v_mul_f32_e32 v134, v134, v134
	v_lshlrev_b32_e32 v135, 16, v105
	v_fmac_f32_e32 v134, v133, v133
	v_and_b32_e32 v136, 0xffff0000, v105
	v_fmac_f32_e32 v134, v135, v135
	v_lshlrev_b32_e32 v137, 16, v106
	v_fmac_f32_e32 v134, v136, v136
	v_and_b32_e32 v144, 0xffff0000, v106
	v_fmac_f32_e32 v134, v137, v137
	v_lshlrev_b32_e32 v145, 16, v107
	v_fmac_f32_e32 v134, v144, v144
	v_and_b32_e32 v162, 0xffff0000, v107
	v_fmac_f32_e32 v134, v145, v145
	v_fmac_f32_e32 v134, v162, v162
	v_add_f32_e32 v132, v132, v134
	s_waitcnt vmcnt(25)
	v_and_b32_e32 v134, 0xffff0000, v100
	v_lshlrev_b32_e32 v133, 16, v100
	v_mul_f32_e32 v134, v134, v134
	v_lshlrev_b32_e32 v135, 16, v101
	v_fmac_f32_e32 v134, v133, v133
	v_and_b32_e32 v136, 0xffff0000, v101
	v_fmac_f32_e32 v134, v135, v135
	v_lshlrev_b32_e32 v137, 16, v102
	v_fmac_f32_e32 v134, v136, v136
	v_and_b32_e32 v144, 0xffff0000, v102
	v_fmac_f32_e32 v134, v137, v137
	v_lshlrev_b32_e32 v145, 16, v103
	v_fmac_f32_e32 v134, v144, v144
	v_and_b32_e32 v162, 0xffff0000, v103
	v_fmac_f32_e32 v134, v145, v145
	v_fmac_f32_e32 v134, v162, v162
	v_add_f32_e32 v132, v132, v134
	s_waitcnt vmcnt(24)
	v_and_b32_e32 v134, 0xffff0000, v96
	v_lshlrev_b32_e32 v133, 16, v96
	v_mul_f32_e32 v134, v134, v134
	v_lshlrev_b32_e32 v135, 16, v97
	v_fmac_f32_e32 v134, v133, v133
	v_and_b32_e32 v136, 0xffff0000, v97
	v_fmac_f32_e32 v134, v135, v135
	v_lshlrev_b32_e32 v137, 16, v98
	v_fmac_f32_e32 v134, v136, v136
	v_and_b32_e32 v144, 0xffff0000, v98
	v_fmac_f32_e32 v134, v137, v137
	v_lshlrev_b32_e32 v145, 16, v99
	v_fmac_f32_e32 v134, v144, v144
	v_and_b32_e32 v162, 0xffff0000, v99
	v_fmac_f32_e32 v134, v145, v145
	v_fmac_f32_e32 v134, v162, v162
	v_add_f32_e32 v132, v132, v134
	s_waitcnt vmcnt(23)
	v_and_b32_e32 v134, 0xffff0000, v92
	v_lshlrev_b32_e32 v133, 16, v92
	v_mul_f32_e32 v134, v134, v134
	v_lshlrev_b32_e32 v135, 16, v93
	v_fmac_f32_e32 v134, v133, v133
	v_and_b32_e32 v136, 0xffff0000, v93
	v_fmac_f32_e32 v134, v135, v135
	v_lshlrev_b32_e32 v137, 16, v94
	v_fmac_f32_e32 v134, v136, v136
	v_and_b32_e32 v144, 0xffff0000, v94
	v_fmac_f32_e32 v134, v137, v137
	v_lshlrev_b32_e32 v145, 16, v95
	v_fmac_f32_e32 v134, v144, v144
	v_and_b32_e32 v162, 0xffff0000, v95
	v_fmac_f32_e32 v134, v145, v145
	v_fmac_f32_e32 v134, v162, v162
	v_add_f32_e32 v132, v132, v134
	s_waitcnt vmcnt(22)
	v_and_b32_e32 v134, 0xffff0000, v88
	v_lshlrev_b32_e32 v133, 16, v88
	v_mul_f32_e32 v134, v134, v134
	v_lshlrev_b32_e32 v135, 16, v89
	v_fmac_f32_e32 v134, v133, v133
	v_and_b32_e32 v136, 0xffff0000, v89
	v_fmac_f32_e32 v134, v135, v135
	v_lshlrev_b32_e32 v137, 16, v90
	v_fmac_f32_e32 v134, v136, v136
	v_and_b32_e32 v144, 0xffff0000, v90
	v_fmac_f32_e32 v134, v137, v137
	v_lshlrev_b32_e32 v145, 16, v91
	v_fmac_f32_e32 v134, v144, v144
	v_and_b32_e32 v162, 0xffff0000, v91
	v_fmac_f32_e32 v134, v145, v145
	v_fmac_f32_e32 v134, v162, v162
	v_add_f32_e32 v132, v132, v134
	s_waitcnt vmcnt(21)
	v_and_b32_e32 v134, 0xffff0000, v84
	v_lshlrev_b32_e32 v133, 16, v84
	v_mul_f32_e32 v134, v134, v134
	v_lshlrev_b32_e32 v135, 16, v85
	v_fmac_f32_e32 v134, v133, v133
	v_and_b32_e32 v136, 0xffff0000, v85
	v_fmac_f32_e32 v134, v135, v135
	v_lshlrev_b32_e32 v137, 16, v86
	v_fmac_f32_e32 v134, v136, v136
	v_and_b32_e32 v144, 0xffff0000, v86
	v_fmac_f32_e32 v134, v137, v137
	v_lshlrev_b32_e32 v145, 16, v87
	v_fmac_f32_e32 v134, v144, v144
	v_and_b32_e32 v162, 0xffff0000, v87
	v_fmac_f32_e32 v134, v145, v145
	v_fmac_f32_e32 v134, v162, v162
	v_add_f32_e32 v132, v132, v134
	s_waitcnt vmcnt(20)
	v_and_b32_e32 v134, 0xffff0000, v80
	v_lshlrev_b32_e32 v133, 16, v80
	v_mul_f32_e32 v134, v134, v134
	v_lshlrev_b32_e32 v135, 16, v81
	v_fmac_f32_e32 v134, v133, v133
	v_and_b32_e32 v136, 0xffff0000, v81
	v_fmac_f32_e32 v134, v135, v135
	v_lshlrev_b32_e32 v137, 16, v82
	v_fmac_f32_e32 v134, v136, v136
	v_and_b32_e32 v144, 0xffff0000, v82
	v_fmac_f32_e32 v134, v137, v137
	v_lshlrev_b32_e32 v145, 16, v83
	v_fmac_f32_e32 v134, v144, v144
	v_and_b32_e32 v162, 0xffff0000, v83
	v_fmac_f32_e32 v134, v145, v145
	v_fmac_f32_e32 v134, v162, v162
	v_add_f32_e32 v132, v132, v134
	s_waitcnt vmcnt(19)
	v_and_b32_e32 v134, 0xffff0000, v76
	v_lshlrev_b32_e32 v133, 16, v76
	v_mul_f32_e32 v134, v134, v134
	v_lshlrev_b32_e32 v135, 16, v77
	v_fmac_f32_e32 v134, v133, v133
	v_and_b32_e32 v136, 0xffff0000, v77
	v_fmac_f32_e32 v134, v135, v135
	v_lshlrev_b32_e32 v137, 16, v78
	v_fmac_f32_e32 v134, v136, v136
	v_and_b32_e32 v144, 0xffff0000, v78
	v_fmac_f32_e32 v134, v137, v137
	v_lshlrev_b32_e32 v145, 16, v79
	v_fmac_f32_e32 v134, v144, v144
	v_and_b32_e32 v162, 0xffff0000, v79
	v_fmac_f32_e32 v134, v145, v145
	v_fmac_f32_e32 v134, v162, v162
	v_add_f32_e32 v132, v132, v134
	s_waitcnt vmcnt(18)
	v_and_b32_e32 v134, 0xffff0000, v72
	v_lshlrev_b32_e32 v133, 16, v72
	v_mul_f32_e32 v134, v134, v134
	v_lshlrev_b32_e32 v135, 16, v73
	v_fmac_f32_e32 v134, v133, v133
	v_and_b32_e32 v136, 0xffff0000, v73
	v_fmac_f32_e32 v134, v135, v135
	v_lshlrev_b32_e32 v137, 16, v74
	v_fmac_f32_e32 v134, v136, v136
	v_and_b32_e32 v144, 0xffff0000, v74
	v_fmac_f32_e32 v134, v137, v137
	v_lshlrev_b32_e32 v145, 16, v75
	v_fmac_f32_e32 v134, v144, v144
	v_and_b32_e32 v162, 0xffff0000, v75
	v_fmac_f32_e32 v134, v145, v145
	v_fmac_f32_e32 v134, v162, v162
	v_add_f32_e32 v132, v132, v134
	s_waitcnt vmcnt(17)
	v_and_b32_e32 v134, 0xffff0000, v68
	v_lshlrev_b32_e32 v133, 16, v68
	v_mul_f32_e32 v134, v134, v134
	v_lshlrev_b32_e32 v135, 16, v69
	v_fmac_f32_e32 v134, v133, v133
	v_and_b32_e32 v136, 0xffff0000, v69
	v_fmac_f32_e32 v134, v135, v135
	v_lshlrev_b32_e32 v137, 16, v70
	v_fmac_f32_e32 v134, v136, v136
	v_and_b32_e32 v144, 0xffff0000, v70
	v_fmac_f32_e32 v134, v137, v137
	v_lshlrev_b32_e32 v145, 16, v71
	v_fmac_f32_e32 v134, v144, v144
	v_and_b32_e32 v162, 0xffff0000, v71
	v_fmac_f32_e32 v134, v145, v145
	v_fmac_f32_e32 v134, v162, v162
	v_add_f32_e32 v132, v132, v134
	s_waitcnt vmcnt(16)
	v_and_b32_e32 v134, 0xffff0000, v64
	v_lshlrev_b32_e32 v133, 16, v64
	v_mul_f32_e32 v134, v134, v134
	v_lshlrev_b32_e32 v135, 16, v65
	v_fmac_f32_e32 v134, v133, v133
	v_and_b32_e32 v136, 0xffff0000, v65
	v_fmac_f32_e32 v134, v135, v135
	v_lshlrev_b32_e32 v137, 16, v66
	v_fmac_f32_e32 v134, v136, v136
	v_and_b32_e32 v144, 0xffff0000, v66
	v_fmac_f32_e32 v134, v137, v137
	v_lshlrev_b32_e32 v145, 16, v67
	v_fmac_f32_e32 v134, v144, v144
	v_and_b32_e32 v162, 0xffff0000, v67
	v_fmac_f32_e32 v134, v145, v145
	v_fmac_f32_e32 v134, v162, v162
	v_add_f32_e32 v132, v132, v134
	s_waitcnt vmcnt(15)
	v_and_b32_e32 v134, 0xffff0000, v60
	v_lshlrev_b32_e32 v133, 16, v60
	v_mul_f32_e32 v134, v134, v134
	v_lshlrev_b32_e32 v135, 16, v61
	v_fmac_f32_e32 v134, v133, v133
	v_and_b32_e32 v136, 0xffff0000, v61
	v_fmac_f32_e32 v134, v135, v135
	v_lshlrev_b32_e32 v137, 16, v62
	v_fmac_f32_e32 v134, v136, v136
	v_and_b32_e32 v144, 0xffff0000, v62
	v_fmac_f32_e32 v134, v137, v137
	v_lshlrev_b32_e32 v145, 16, v63
	v_fmac_f32_e32 v134, v144, v144
	v_and_b32_e32 v162, 0xffff0000, v63
	v_fmac_f32_e32 v134, v145, v145
	v_fmac_f32_e32 v134, v162, v162
	v_add_f32_e32 v132, v132, v134
	s_waitcnt vmcnt(14)
	v_and_b32_e32 v134, 0xffff0000, v56
	v_lshlrev_b32_e32 v133, 16, v56
	v_mul_f32_e32 v134, v134, v134
	v_lshlrev_b32_e32 v135, 16, v57
	v_fmac_f32_e32 v134, v133, v133
	v_and_b32_e32 v136, 0xffff0000, v57
	v_fmac_f32_e32 v134, v135, v135
	v_lshlrev_b32_e32 v137, 16, v58
	v_fmac_f32_e32 v134, v136, v136
	v_and_b32_e32 v144, 0xffff0000, v58
	v_fmac_f32_e32 v134, v137, v137
	v_lshlrev_b32_e32 v145, 16, v59
	v_fmac_f32_e32 v134, v144, v144
	v_and_b32_e32 v162, 0xffff0000, v59
	v_fmac_f32_e32 v134, v145, v145
	v_fmac_f32_e32 v134, v162, v162
	v_add_f32_e32 v132, v132, v134
	s_waitcnt vmcnt(13)
	v_and_b32_e32 v134, 0xffff0000, v52
	v_lshlrev_b32_e32 v133, 16, v52
	v_mul_f32_e32 v134, v134, v134
	v_lshlrev_b32_e32 v135, 16, v53
	v_fmac_f32_e32 v134, v133, v133
	v_and_b32_e32 v136, 0xffff0000, v53
	v_fmac_f32_e32 v134, v135, v135
	v_lshlrev_b32_e32 v137, 16, v54
	v_fmac_f32_e32 v134, v136, v136
	v_and_b32_e32 v144, 0xffff0000, v54
	v_fmac_f32_e32 v134, v137, v137
	v_lshlrev_b32_e32 v145, 16, v55
	v_fmac_f32_e32 v134, v144, v144
	v_and_b32_e32 v162, 0xffff0000, v55
	v_fmac_f32_e32 v134, v145, v145
	v_fmac_f32_e32 v134, v162, v162
	v_add_f32_e32 v132, v132, v134
	s_waitcnt vmcnt(12)
	v_and_b32_e32 v134, 0xffff0000, v48
	v_lshlrev_b32_e32 v133, 16, v48
	v_mul_f32_e32 v134, v134, v134
	v_lshlrev_b32_e32 v135, 16, v49
	v_fmac_f32_e32 v134, v133, v133
	v_and_b32_e32 v136, 0xffff0000, v49
	v_fmac_f32_e32 v134, v135, v135
	v_lshlrev_b32_e32 v137, 16, v50
	v_fmac_f32_e32 v134, v136, v136
	v_and_b32_e32 v144, 0xffff0000, v50
	v_fmac_f32_e32 v134, v137, v137
	v_lshlrev_b32_e32 v145, 16, v51
	v_fmac_f32_e32 v134, v144, v144
	v_and_b32_e32 v162, 0xffff0000, v51
	v_fmac_f32_e32 v134, v145, v145
	v_fmac_f32_e32 v134, v162, v162
	v_add_f32_e32 v132, v132, v134
	s_waitcnt vmcnt(11)
	v_and_b32_e32 v134, 0xffff0000, v44
	v_lshlrev_b32_e32 v133, 16, v44
	v_mul_f32_e32 v134, v134, v134
	v_lshlrev_b32_e32 v135, 16, v45
	v_fmac_f32_e32 v134, v133, v133
	v_and_b32_e32 v136, 0xffff0000, v45
	v_fmac_f32_e32 v134, v135, v135
	v_lshlrev_b32_e32 v137, 16, v46
	v_fmac_f32_e32 v134, v136, v136
	v_and_b32_e32 v144, 0xffff0000, v46
	v_fmac_f32_e32 v134, v137, v137
	v_lshlrev_b32_e32 v145, 16, v47
	v_fmac_f32_e32 v134, v144, v144
	v_and_b32_e32 v162, 0xffff0000, v47
	v_fmac_f32_e32 v134, v145, v145
	v_fmac_f32_e32 v134, v162, v162
	v_add_f32_e32 v132, v132, v134
	s_waitcnt vmcnt(10)
	v_and_b32_e32 v134, 0xffff0000, v40
	v_lshlrev_b32_e32 v133, 16, v40
	v_mul_f32_e32 v134, v134, v134
	v_lshlrev_b32_e32 v135, 16, v41
	v_fmac_f32_e32 v134, v133, v133
	v_and_b32_e32 v136, 0xffff0000, v41
	v_fmac_f32_e32 v134, v135, v135
	v_lshlrev_b32_e32 v137, 16, v42
	v_fmac_f32_e32 v134, v136, v136
	v_and_b32_e32 v144, 0xffff0000, v42
	v_fmac_f32_e32 v134, v137, v137
	v_lshlrev_b32_e32 v145, 16, v43
	v_fmac_f32_e32 v134, v144, v144
	v_and_b32_e32 v162, 0xffff0000, v43
	v_fmac_f32_e32 v134, v145, v145
	v_fmac_f32_e32 v134, v162, v162
	v_add_f32_e32 v132, v132, v134
	s_waitcnt vmcnt(9)
	v_and_b32_e32 v134, 0xffff0000, v36
	v_lshlrev_b32_e32 v133, 16, v36
	v_mul_f32_e32 v134, v134, v134
	v_lshlrev_b32_e32 v135, 16, v37
	v_fmac_f32_e32 v134, v133, v133
	v_and_b32_e32 v136, 0xffff0000, v37
	v_fmac_f32_e32 v134, v135, v135
	v_lshlrev_b32_e32 v137, 16, v38
	v_fmac_f32_e32 v134, v136, v136
	v_and_b32_e32 v144, 0xffff0000, v38
	v_fmac_f32_e32 v134, v137, v137
	v_lshlrev_b32_e32 v145, 16, v39
	v_fmac_f32_e32 v134, v144, v144
	v_and_b32_e32 v162, 0xffff0000, v39
	v_fmac_f32_e32 v134, v145, v145
	v_fmac_f32_e32 v134, v162, v162
	v_add_f32_e32 v132, v132, v134
	s_waitcnt vmcnt(8)
	v_and_b32_e32 v134, 0xffff0000, v32
	v_lshlrev_b32_e32 v133, 16, v32
	v_mul_f32_e32 v134, v134, v134
	v_lshlrev_b32_e32 v135, 16, v33
	v_fmac_f32_e32 v134, v133, v133
	v_and_b32_e32 v136, 0xffff0000, v33
	v_fmac_f32_e32 v134, v135, v135
	v_lshlrev_b32_e32 v137, 16, v34
	v_fmac_f32_e32 v134, v136, v136
	v_and_b32_e32 v144, 0xffff0000, v34
	v_fmac_f32_e32 v134, v137, v137
	v_lshlrev_b32_e32 v145, 16, v35
	v_fmac_f32_e32 v134, v144, v144
	v_and_b32_e32 v162, 0xffff0000, v35
	v_fmac_f32_e32 v134, v145, v145
	v_fmac_f32_e32 v134, v162, v162
	v_add_f32_e32 v170, v132, v134
	s_waitcnt vmcnt(6)
	v_and_b32_e32 v135, 0xffff0000, v24
	v_and_b32_e32 v134, 0xffff0000, v28
	v_lshlrev_b32_e32 v133, 16, v24
	v_lshlrev_b32_e32 v132, 16, v28
	v_pk_mul_f32 v[134:135], v[134:135], v[134:135]
	v_lshlrev_b32_e32 v137, 16, v25
	v_lshlrev_b32_e32 v136, 16, v29
	v_pk_fma_f32 v[132:133], v[132:133], v[132:133], v[134:135]
	v_and_b32_e32 v145, 0xffff0000, v25
	v_and_b32_e32 v144, 0xffff0000, v29
	v_pk_fma_f32 v[132:133], v[136:137], v[136:137], v[132:133]
	v_lshlrev_b32_e32 v163, 16, v26
	v_lshlrev_b32_e32 v162, 16, v30
	v_pk_fma_f32 v[132:133], v[144:145], v[144:145], v[132:133]
	v_and_b32_e32 v165, 0xffff0000, v26
	v_and_b32_e32 v164, 0xffff0000, v30
	v_pk_fma_f32 v[132:133], v[162:163], v[162:163], v[132:133]
	v_lshlrev_b32_e32 v167, 16, v27
	v_lshlrev_b32_e32 v166, 16, v31
	v_pk_fma_f32 v[132:133], v[164:165], v[164:165], v[132:133]
	v_and_b32_e32 v169, 0xffff0000, v27
	v_and_b32_e32 v168, 0xffff0000, v31
	v_pk_fma_f32 v[132:133], v[166:167], v[166:167], v[132:133]
	s_waitcnt vmcnt(4)
	v_and_b32_e32 v135, 0xffff0000, v16
	v_pk_fma_f32 v[132:133], v[168:169], v[168:169], v[132:133]
	v_and_b32_e32 v134, 0xffff0000, v20
	v_add_f32_e32 v132, v170, v132
	v_add_f32_e32 v170, v132, v133
	v_lshlrev_b32_e32 v133, 16, v16
	v_lshlrev_b32_e32 v132, 16, v20
	v_pk_mul_f32 v[134:135], v[134:135], v[134:135]
	v_lshlrev_b32_e32 v137, 16, v17
	v_lshlrev_b32_e32 v136, 16, v21
	v_pk_fma_f32 v[132:133], v[132:133], v[132:133], v[134:135]
	v_and_b32_e32 v145, 0xffff0000, v17
	v_and_b32_e32 v144, 0xffff0000, v21
	v_pk_fma_f32 v[132:133], v[136:137], v[136:137], v[132:133]
	v_lshlrev_b32_e32 v163, 16, v18
	v_lshlrev_b32_e32 v162, 16, v22
	v_pk_fma_f32 v[132:133], v[144:145], v[144:145], v[132:133]
	v_and_b32_e32 v165, 0xffff0000, v18
	v_and_b32_e32 v164, 0xffff0000, v22
	v_pk_fma_f32 v[132:133], v[162:163], v[162:163], v[132:133]
	v_lshlrev_b32_e32 v167, 16, v19
	v_lshlrev_b32_e32 v166, 16, v23
	v_pk_fma_f32 v[132:133], v[164:165], v[164:165], v[132:133]
	v_and_b32_e32 v169, 0xffff0000, v19
	v_and_b32_e32 v168, 0xffff0000, v23
	v_pk_fma_f32 v[132:133], v[166:167], v[166:167], v[132:133]
	s_waitcnt vmcnt(2)
	v_and_b32_e32 v135, 0xffff0000, v8
	v_pk_fma_f32 v[132:133], v[168:169], v[168:169], v[132:133]
	v_and_b32_e32 v134, 0xffff0000, v12
	v_add_f32_e32 v132, v170, v132
	v_add_f32_e32 v170, v132, v133
	v_lshlrev_b32_e32 v133, 16, v8
	v_lshlrev_b32_e32 v132, 16, v12
	v_pk_mul_f32 v[134:135], v[134:135], v[134:135]
	v_lshlrev_b32_e32 v137, 16, v9
	v_lshlrev_b32_e32 v136, 16, v13
	v_pk_fma_f32 v[132:133], v[132:133], v[132:133], v[134:135]
	v_and_b32_e32 v145, 0xffff0000, v9
	v_and_b32_e32 v144, 0xffff0000, v13
	v_pk_fma_f32 v[132:133], v[136:137], v[136:137], v[132:133]
	v_lshlrev_b32_e32 v163, 16, v10
	v_lshlrev_b32_e32 v162, 16, v14
	v_pk_fma_f32 v[132:133], v[144:145], v[144:145], v[132:133]
	v_and_b32_e32 v165, 0xffff0000, v10
	v_and_b32_e32 v164, 0xffff0000, v14
	v_pk_fma_f32 v[132:133], v[162:163], v[162:163], v[132:133]
	v_lshlrev_b32_e32 v167, 16, v11
	v_lshlrev_b32_e32 v166, 16, v15
	v_pk_fma_f32 v[132:133], v[164:165], v[164:165], v[132:133]
	v_and_b32_e32 v169, 0xffff0000, v11
	v_and_b32_e32 v168, 0xffff0000, v15
	v_pk_fma_f32 v[132:133], v[166:167], v[166:167], v[132:133]
	s_waitcnt vmcnt(0)
	v_and_b32_e32 v135, 0xffff0000, v0
	v_pk_fma_f32 v[132:133], v[168:169], v[168:169], v[132:133]
	v_and_b32_e32 v134, 0xffff0000, v4
	v_add_f32_e32 v132, v170, v132
	v_add_f32_e32 v170, v132, v133
	v_lshlrev_b32_e32 v133, 16, v0
	v_lshlrev_b32_e32 v132, 16, v4
	v_pk_mul_f32 v[134:135], v[134:135], v[134:135]
	v_lshlrev_b32_e32 v137, 16, v1
	v_lshlrev_b32_e32 v136, 16, v5
	v_pk_fma_f32 v[132:133], v[132:133], v[132:133], v[134:135]
	v_and_b32_e32 v145, 0xffff0000, v1
	v_and_b32_e32 v144, 0xffff0000, v5
	v_pk_fma_f32 v[132:133], v[136:137], v[136:137], v[132:133]
	v_lshlrev_b32_e32 v163, 16, v2
	v_lshlrev_b32_e32 v162, 16, v6
	v_pk_fma_f32 v[132:133], v[144:145], v[144:145], v[132:133]
	v_and_b32_e32 v165, 0xffff0000, v2
	v_and_b32_e32 v164, 0xffff0000, v6
	v_pk_fma_f32 v[132:133], v[162:163], v[162:163], v[132:133]
	v_lshlrev_b32_e32 v167, 16, v3
	v_lshlrev_b32_e32 v166, 16, v7
	v_pk_fma_f32 v[132:133], v[164:165], v[164:165], v[132:133]
	v_and_b32_e32 v169, 0xffff0000, v3
	v_and_b32_e32 v168, 0xffff0000, v7
	v_pk_fma_f32 v[132:133], v[166:167], v[166:167], v[132:133]
	s_nop 0
	v_pk_fma_f32 v[132:133], v[168:169], v[168:169], v[132:133]
	s_nop 0
	v_add_f32_e32 v132, v170, v132
	v_add_f32_e32 v132, v132, v133
	ds_bpermute_b32 v133, v150, v132
	s_waitcnt lgkmcnt(0)
	v_add_f32_e32 v132, v132, v133
	ds_bpermute_b32 v133, v151, v132
	s_waitcnt lgkmcnt(0)
	v_add_f32_e32 v132, v132, v133
	v_fmamk_f32 v132, v132, 0x3a800000, v213
	v_cmp_gt_f32_e32 vcc, s63, v132
	v_mul_f32_e32 v133, 0x4b800000, v132
	s_nop 0
	v_cndmask_b32_e32 v132, v132, v133, vcc
	v_rsq_f32_e32 v132, v132
	s_nop 0
	v_mul_f32_e32 v133, 0x45800000, v132
	v_cndmask_b32_e32 v112, v132, v133, vcc
	v_mov_b32_e32 v132, 0x2000
	v_cndmask_b32_e64 v132, v132, 0, s[38:39]
	v_add_u32_e32 v162, v152, v132
	v_lshl_add_u64 v[144:145], v[140:141], 0, v[130:131]
	ds_read_b128 v[164:167], v162
	ds_read_b128 v[168:171], v162 offset:16
	ds_read_b128 v[134:137], v162 offset:4096
	ds_read_b128 v[130:133], v162 offset:4112
	v_lshlrev_b32_e32 v163, 16, v126
	v_and_b32_e32 v126, 0xffff0000, v126
	v_mul_f32_e32 v126, v112, v126
	s_waitcnt lgkmcnt(1)
	v_fma_f32 v126, v126, v165, v135
	v_lshlrev_b32_e32 v135, 16, v127
	v_and_b32_e32 v127, 0xffff0000, v127
	v_mul_f32_e32 v127, v112, v127
	v_fmac_f32_e32 v137, v127, v167
	v_lshlrev_b32_e32 v127, 16, v128
	v_mul_f32_e32 v127, v112, v127
	s_waitcnt lgkmcnt(0)
	v_fma_f32 v127, v127, v168, v130
	v_and_b32_e32 v128, 0xffff0000, v128
	v_lshlrev_b32_e32 v130, 16, v129
	v_and_b32_e32 v129, 0xffff0000, v129
	v_mul_f32_e32 v163, v112, v163
	v_mul_f32_e32 v135, v112, v135
	v_mul_f32_e32 v128, v112, v128
	v_mul_f32_e32 v130, v112, v130
	v_mul_f32_e32 v129, v112, v129
	v_fma_f32 v134, v163, v164, v134
	v_fma_f32 v135, v135, v166, v136
	v_fma_f32 v128, v128, v169, v131
	v_fma_f32 v130, v130, v170, v132
	v_fmac_f32_e32 v133, v129, v171
	s_and_saveexec_b64 s[0:1], s[42:43]
	s_cbranch_execz .LBB0_1232
	v_mul_f32_e32 v129, 0x41800000, v134
	v_mul_f32_e32 v131, 0x41800000, v126
	v_med3_f32 v129, v129, s25, v218
	v_med3_f32 v131, v131, s25, v218
	v_cvt_pk_fp8_f32 v164, v129, v131
	v_mul_f32_e32 v132, 0x41800000, v135
	v_mul_f32_e32 v129, 0x41800000, v137
	v_med3_f32 v131, v132, s25, v218
	v_med3_f32 v129, v129, s25, v218
	v_cvt_pk_fp8_f32 v164, v131, v129 op_sel:[0,0,1]
	v_mul_f32_e32 v129, 0x41800000, v127
	v_mul_f32_e32 v131, 0x41800000, v128
	v_med3_f32 v129, v129, s25, v218
	v_med3_f32 v131, v131, s25, v218
	v_cvt_pk_fp8_f32 v165, v129, v131
	v_mul_f32_e32 v132, 0x41800000, v130
	v_mul_f32_e32 v129, 0x41800000, v133
	v_med3_f32 v131, v132, s25, v218
	v_med3_f32 v129, v129, s25, v218
	v_cvt_pk_fp8_f32 v165, v131, v129 op_sel:[0,0,1]
	global_store_dwordx2 v[144:145], v[164:165], off
.LBB0_1232:
	s_or_b64 exec, exec, s[0:1]
	v_cvt_pk_bf16_f32 v164, v134, v126
	v_cvt_pk_bf16_f32 v165, v135, v137
	v_cvt_pk_bf16_f32 v166, v127, v128
	v_cvt_pk_bf16_f32 v167, v130, v133
	v_lshlrev_b32_e32 v163, 16, v122
	v_and_b32_e32 v131, 0xffff0000, v164
	v_lshlrev_b32_e32 v129, 16, v164
	v_sub_f32_e32 v126, v126, v131
	v_sub_f32_e32 v129, v134, v129
	v_cvt_pk_bf16_f32 v134, v129, v126
	v_lshlrev_b32_e32 v126, 16, v165
	v_sub_f32_e32 v126, v135, v126
	v_and_b32_e32 v129, 0xffff0000, v165
	v_sub_f32_e32 v129, v137, v129
	v_cvt_pk_bf16_f32 v135, v126, v129
	v_lshlrev_b32_e32 v126, 16, v166
	v_sub_f32_e32 v126, v127, v126
	v_and_b32_e32 v127, 0xffff0000, v166
	v_sub_f32_e32 v127, v128, v127
	v_cvt_pk_bf16_f32 v136, v126, v127
	v_lshlrev_b32_e32 v126, 16, v167
	v_and_b32_e32 v127, 0xffff0000, v167
	v_sub_f32_e32 v126, v130, v126
	v_sub_f32_e32 v127, v133, v127
	v_cvt_pk_bf16_f32 v137, v126, v127
	ds_read_b128 v[126:129], v153 offset:1024
	v_and_b32_e32 v122, 0xffff0000, v122
	s_waitcnt lgkmcnt(0)
	v_mfma_f32_16x16x32_bf16 v[130:133], v[164:167], v[126:129], 0
	v_mul_f32_e32 v122, v112, v122
	v_mul_f32_e32 v163, v112, v163
	v_mfma_f32_16x16x32_bf16 v[126:129], v[134:137], v[126:129], v[130:133]
	s_nop 4
	ds_read_b128 v[130:133], v153 offset:34048
	s_waitcnt lgkmcnt(0)
	v_mfma_f32_16x16x32_bf16 v[126:129], v[164:167], v[130:133], v[126:129]
	ds_read_b128 v[134:137], v162 offset:4224
	ds_read_b128 v[164:167], v162 offset:128
	ds_read_b128 v[130:133], v162 offset:4240
	ds_read_b128 v[168:171], v162 offset:144
	s_waitcnt lgkmcnt(2)
	v_fma_f32 v122, v122, v165, v135
	v_lshlrev_b32_e32 v135, 16, v123
	v_and_b32_e32 v123, 0xffff0000, v123
	v_mul_f32_e32 v123, v112, v123
	v_fmac_f32_e32 v137, v123, v167
	v_lshlrev_b32_e32 v123, 16, v124
	v_mul_f32_e32 v123, v112, v123
	s_waitcnt lgkmcnt(0)
	v_fma_f32 v123, v123, v168, v130
	v_and_b32_e32 v124, 0xffff0000, v124
	v_lshlrev_b32_e32 v130, 16, v125
	v_and_b32_e32 v125, 0xffff0000, v125
	v_mul_f32_e32 v135, v112, v135
	v_mul_f32_e32 v124, v112, v124
	v_mul_f32_e32 v130, v112, v130
	v_mul_f32_e32 v125, v112, v125
	v_fma_f32 v134, v163, v164, v134
	v_fma_f32 v135, v135, v166, v136
	v_fma_f32 v124, v124, v169, v131
	v_fma_f32 v130, v130, v170, v132
	v_fmac_f32_e32 v133, v125, v171
	s_and_saveexec_b64 s[0:1], s[42:43]
	s_cbranch_execz .LBB0_1234
	v_mul_f32_e32 v125, 0x41800000, v134
	v_mul_f32_e32 v131, 0x41800000, v122
	v_med3_f32 v125, v125, s25, v218
	v_med3_f32 v131, v131, s25, v218
	v_cvt_pk_fp8_f32 v164, v125, v131
	v_mul_f32_e32 v132, 0x41800000, v135
	v_mul_f32_e32 v125, 0x41800000, v137
	v_med3_f32 v131, v132, s25, v218
	v_med3_f32 v125, v125, s25, v218
	v_cvt_pk_fp8_f32 v164, v131, v125 op_sel:[0,0,1]
	v_mul_f32_e32 v125, 0x41800000, v123
	v_mul_f32_e32 v131, 0x41800000, v124
	v_med3_f32 v125, v125, s25, v218
	v_med3_f32 v131, v131, s25, v218
	v_cvt_pk_fp8_f32 v165, v125, v131
	v_mul_f32_e32 v132, 0x41800000, v130
	v_mul_f32_e32 v125, 0x41800000, v133
	v_med3_f32 v131, v132, s25, v218
	v_med3_f32 v125, v125, s25, v218
	v_cvt_pk_fp8_f32 v165, v131, v125 op_sel:[0,0,1]
	global_store_dwordx2 v[144:145], v[164:165], off offset:32
.LBB0_1234:
	s_or_b64 exec, exec, s[0:1]
	v_cvt_pk_bf16_f32 v164, v134, v122
	v_cvt_pk_bf16_f32 v165, v135, v137
	v_cvt_pk_bf16_f32 v166, v123, v124
	v_cvt_pk_bf16_f32 v167, v130, v133
	s_nop 0
	v_and_b32_e32 v131, 0xffff0000, v164
	v_lshlrev_b32_e32 v125, 16, v164
	v_sub_f32_e32 v122, v122, v131
	v_sub_f32_e32 v125, v134, v125
	v_cvt_pk_bf16_f32 v134, v125, v122
	v_lshlrev_b32_e32 v122, 16, v165
	v_sub_f32_e32 v122, v135, v122
	v_and_b32_e32 v125, 0xffff0000, v165
	v_sub_f32_e32 v125, v137, v125
	v_cvt_pk_bf16_f32 v135, v122, v125
	v_lshlrev_b32_e32 v122, 16, v166
	v_sub_f32_e32 v122, v123, v122
	v_and_b32_e32 v123, 0xffff0000, v166
	v_sub_f32_e32 v123, v124, v123
	v_cvt_pk_bf16_f32 v136, v122, v123
	v_lshlrev_b32_e32 v122, 16, v167
	v_and_b32_e32 v123, 0xffff0000, v167
	v_sub_f32_e32 v122, v130, v122
	v_sub_f32_e32 v123, v133, v123
	v_cvt_pk_bf16_f32 v137, v122, v123
	ds_read_b128 v[122:125], v153 offset:1088
	s_waitcnt lgkmcnt(0)
	v_mfma_f32_16x16x32_bf16 v[126:129], v[164:167], v[122:125], v[126:129]
	v_mfma_f32_16x16x32_bf16 v[122:125], v[134:137], v[122:125], v[126:129]
	s_nop 6
	ds_read_b128 v[126:129], v153 offset:34112
	s_waitcnt lgkmcnt(0)
	v_mfma_f32_16x16x32_bf16 v[122:125], v[164:167], v[126:129], v[122:125]
	ds_read_b128 v[130:133], v162 offset:4352
	ds_read_b128 v[134:137], v162 offset:256
	ds_read_b128 v[164:167], v162 offset:272
	ds_read_b128 v[126:129], v162 offset:4368
	v_lshlrev_b32_e32 v163, 16, v118
	v_and_b32_e32 v118, 0xffff0000, v118
	v_mul_f32_e32 v118, v112, v118
	s_waitcnt lgkmcnt(2)
	v_fma_f32 v118, v118, v135, v131
	v_lshlrev_b32_e32 v131, 16, v119
	v_and_b32_e32 v119, 0xffff0000, v119
	v_mul_f32_e32 v119, v112, v119
	v_fmac_f32_e32 v133, v119, v137
	v_lshlrev_b32_e32 v119, 16, v120
	v_mul_f32_e32 v119, v112, v119
	s_waitcnt lgkmcnt(0)
	v_fma_f32 v119, v119, v164, v126
	v_and_b32_e32 v120, 0xffff0000, v120
	v_lshlrev_b32_e32 v126, 16, v121
	v_and_b32_e32 v121, 0xffff0000, v121
	v_mul_f32_e32 v163, v112, v163
	v_mul_f32_e32 v131, v112, v131
	v_mul_f32_e32 v120, v112, v120
	v_mul_f32_e32 v126, v112, v126
	v_mul_f32_e32 v121, v112, v121
	v_fma_f32 v130, v163, v134, v130
	v_fma_f32 v131, v131, v136, v132
	v_fma_f32 v120, v120, v165, v127
	v_fma_f32 v126, v126, v166, v128
	v_fmac_f32_e32 v129, v121, v167
	s_and_saveexec_b64 s[0:1], s[42:43]
	s_cbranch_execz .LBB0_1236
	v_mul_f32_e32 v121, 0x41800000, v130
	v_mul_f32_e32 v127, 0x41800000, v118
	v_med3_f32 v121, v121, s25, v218
	v_med3_f32 v127, v127, s25, v218
	v_cvt_pk_fp8_f32 v134, v121, v127
	v_mul_f32_e32 v128, 0x41800000, v131
	v_mul_f32_e32 v121, 0x41800000, v133
	v_med3_f32 v127, v128, s25, v218
	v_med3_f32 v121, v121, s25, v218
	v_cvt_pk_fp8_f32 v134, v127, v121 op_sel:[0,0,1]
	v_mul_f32_e32 v121, 0x41800000, v119
	v_mul_f32_e32 v127, 0x41800000, v120
	v_med3_f32 v121, v121, s25, v218
	v_med3_f32 v127, v127, s25, v218
	v_cvt_pk_fp8_f32 v135, v121, v127
	v_mul_f32_e32 v128, 0x41800000, v126
	v_mul_f32_e32 v121, 0x41800000, v129
	v_med3_f32 v127, v128, s25, v218
	v_med3_f32 v121, v121, s25, v218
	v_cvt_pk_fp8_f32 v135, v127, v121 op_sel:[0,0,1]
	global_store_dwordx2 v[144:145], v[134:135], off offset:64
.LBB0_1236:
	s_or_b64 exec, exec, s[0:1]
	v_cvt_pk_bf16_f32 v134, v130, v118
	v_cvt_pk_bf16_f32 v135, v131, v133
	v_cvt_pk_bf16_f32 v136, v119, v120
	v_cvt_pk_bf16_f32 v137, v126, v129
	v_lshlrev_b32_e32 v163, 16, v114
	v_and_b32_e32 v127, 0xffff0000, v134
	v_lshlrev_b32_e32 v121, 16, v134
	v_sub_f32_e32 v118, v118, v127
	v_sub_f32_e32 v121, v130, v121
	v_cvt_pk_bf16_f32 v130, v121, v118
	v_lshlrev_b32_e32 v118, 16, v135
	v_sub_f32_e32 v118, v131, v118
	v_and_b32_e32 v121, 0xffff0000, v135
	v_sub_f32_e32 v121, v133, v121
	v_cvt_pk_bf16_f32 v131, v118, v121
	v_lshlrev_b32_e32 v118, 16, v136
	v_sub_f32_e32 v118, v119, v118
	v_and_b32_e32 v119, 0xffff0000, v136
	v_sub_f32_e32 v119, v120, v119
	v_cvt_pk_bf16_f32 v132, v118, v119
	v_lshlrev_b32_e32 v118, 16, v137
	v_and_b32_e32 v119, 0xffff0000, v137
	v_sub_f32_e32 v118, v126, v118
	v_sub_f32_e32 v119, v129, v119
	v_cvt_pk_bf16_f32 v133, v118, v119
	ds_read_b128 v[118:121], v153 offset:1152
	v_and_b32_e32 v114, 0xffff0000, v114
	s_waitcnt lgkmcnt(0)
	v_mfma_f32_16x16x32_bf16 v[122:125], v[134:137], v[118:121], v[122:125]
	v_mul_f32_e32 v114, v112, v114
	v_mul_f32_e32 v163, v112, v163
	v_mfma_f32_16x16x32_bf16 v[118:121], v[130:133], v[118:121], v[122:125]
	s_nop 4
	ds_read_b128 v[122:125], v153 offset:34176
	s_waitcnt lgkmcnt(0)
	v_mfma_f32_16x16x32_bf16 v[118:121], v[134:137], v[122:125], v[118:121]
	ds_read_b128 v[126:129], v162 offset:4480
	ds_read_b128 v[130:133], v162 offset:384
	ds_read_b128 v[122:125], v162 offset:4496
	ds_read_b128 v[134:137], v162 offset:400
	s_waitcnt lgkmcnt(2)
	v_fma_f32 v114, v114, v131, v127
	v_lshlrev_b32_e32 v127, 16, v115
	v_and_b32_e32 v115, 0xffff0000, v115
	v_mul_f32_e32 v115, v112, v115
	v_fmac_f32_e32 v129, v115, v133
	v_lshlrev_b32_e32 v115, 16, v116
	v_mul_f32_e32 v115, v112, v115
	s_waitcnt lgkmcnt(0)
	v_fma_f32 v115, v115, v134, v122
	v_and_b32_e32 v116, 0xffff0000, v116
	v_lshlrev_b32_e32 v122, 16, v117
	v_and_b32_e32 v117, 0xffff0000, v117
	v_mul_f32_e32 v127, v112, v127
	v_mul_f32_e32 v116, v112, v116
	v_mul_f32_e32 v122, v112, v122
	v_mul_f32_e32 v117, v112, v117
	v_fma_f32 v126, v163, v130, v126
	v_fma_f32 v127, v127, v132, v128
	v_fma_f32 v116, v116, v135, v123
	v_fma_f32 v122, v122, v136, v124
	v_fmac_f32_e32 v125, v117, v137
	s_and_saveexec_b64 s[0:1], s[42:43]
	s_cbranch_execz .LBB0_1238
	v_mul_f32_e32 v117, 0x41800000, v126
	v_mul_f32_e32 v123, 0x41800000, v114
	v_med3_f32 v117, v117, s25, v218
	v_med3_f32 v123, v123, s25, v218
	v_cvt_pk_fp8_f32 v130, v117, v123
	v_mul_f32_e32 v124, 0x41800000, v127
	v_mul_f32_e32 v117, 0x41800000, v129
	v_med3_f32 v123, v124, s25, v218
	v_med3_f32 v117, v117, s25, v218
	v_cvt_pk_fp8_f32 v130, v123, v117 op_sel:[0,0,1]
	v_mul_f32_e32 v117, 0x41800000, v115
	v_mul_f32_e32 v123, 0x41800000, v116
	v_med3_f32 v117, v117, s25, v218
	v_med3_f32 v123, v123, s25, v218
	v_cvt_pk_fp8_f32 v131, v117, v123
	v_mul_f32_e32 v124, 0x41800000, v122
	v_mul_f32_e32 v117, 0x41800000, v125
	v_med3_f32 v123, v124, s25, v218
	v_med3_f32 v117, v117, s25, v218
	v_cvt_pk_fp8_f32 v131, v123, v117 op_sel:[0,0,1]
	global_store_dwordx2 v[144:145], v[130:131], off offset:96
.LBB0_1238:
	s_or_b64 exec, exec, s[0:1]
	v_cvt_pk_bf16_f32 v130, v126, v114
	v_cvt_pk_bf16_f32 v131, v127, v129
	v_cvt_pk_bf16_f32 v132, v115, v116
	v_cvt_pk_bf16_f32 v133, v122, v125
	s_nop 0
	v_and_b32_e32 v123, 0xffff0000, v130
	v_lshlrev_b32_e32 v117, 16, v130
	v_sub_f32_e32 v114, v114, v123
	v_sub_f32_e32 v117, v126, v117
	v_cvt_pk_bf16_f32 v126, v117, v114
	v_lshlrev_b32_e32 v114, 16, v131
	v_sub_f32_e32 v114, v127, v114
	v_and_b32_e32 v117, 0xffff0000, v131
	v_sub_f32_e32 v117, v129, v117
	v_cvt_pk_bf16_f32 v127, v114, v117
	v_lshlrev_b32_e32 v114, 16, v132
	v_sub_f32_e32 v114, v115, v114
	v_and_b32_e32 v115, 0xffff0000, v132
	v_sub_f32_e32 v115, v116, v115
	v_cvt_pk_bf16_f32 v128, v114, v115
	v_lshlrev_b32_e32 v114, 16, v133
	v_and_b32_e32 v115, 0xffff0000, v133
	v_sub_f32_e32 v114, v122, v114
	v_sub_f32_e32 v115, v125, v115
	v_cvt_pk_bf16_f32 v129, v114, v115
	ds_read_b128 v[114:117], v153 offset:1216
	s_waitcnt lgkmcnt(0)
	v_mfma_f32_16x16x32_bf16 v[118:121], v[130:133], v[114:117], v[118:121]
	v_mfma_f32_16x16x32_bf16 v[114:117], v[126:129], v[114:117], v[118:121]
	s_nop 6
	ds_read_b128 v[118:121], v153 offset:34240
	s_waitcnt lgkmcnt(0)
	v_mfma_f32_16x16x32_bf16 v[114:117], v[130:133], v[118:121], v[114:117]
	ds_read_b128 v[122:125], v162 offset:4608
	ds_read_b128 v[126:129], v162 offset:512
	ds_read_b128 v[130:133], v162 offset:528
	ds_read_b128 v[118:121], v162 offset:4624
	v_lshlrev_b32_e32 v134, 16, v108
	v_and_b32_e32 v108, 0xffff0000, v108
	v_mul_f32_e32 v108, v112, v108
	s_waitcnt lgkmcnt(2)
	v_fma_f32 v108, v108, v127, v123
	v_lshlrev_b32_e32 v123, 16, v109
	v_and_b32_e32 v109, 0xffff0000, v109
	v_mul_f32_e32 v109, v112, v109
	v_fmac_f32_e32 v125, v109, v129
	v_lshlrev_b32_e32 v109, 16, v110
	v_mul_f32_e32 v109, v112, v109
	s_waitcnt lgkmcnt(0)
	v_fma_f32 v109, v109, v130, v118
	v_and_b32_e32 v110, 0xffff0000, v110
	v_lshlrev_b32_e32 v118, 16, v111
	v_and_b32_e32 v111, 0xffff0000, v111
	v_mul_f32_e32 v134, v112, v134
	v_mul_f32_e32 v123, v112, v123
	v_mul_f32_e32 v110, v112, v110
	v_mul_f32_e32 v118, v112, v118
	v_mul_f32_e32 v111, v112, v111
	v_fma_f32 v122, v134, v126, v122
	v_fma_f32 v123, v123, v128, v124
	v_fma_f32 v110, v110, v131, v119
	v_fma_f32 v118, v118, v132, v120
	v_fmac_f32_e32 v121, v111, v133
	s_and_saveexec_b64 s[0:1], s[42:43]
	s_cbranch_execz .LBB0_1240
	v_mul_f32_e32 v111, 0x41800000, v122
	v_mul_f32_e32 v119, 0x41800000, v108
	v_med3_f32 v111, v111, s25, v218
	v_med3_f32 v119, v119, s25, v218
	v_cvt_pk_fp8_f32 v126, v111, v119
	v_mul_f32_e32 v120, 0x41800000, v123
	v_mul_f32_e32 v111, 0x41800000, v125
	v_med3_f32 v119, v120, s25, v218
	v_med3_f32 v111, v111, s25, v218
	v_cvt_pk_fp8_f32 v126, v119, v111 op_sel:[0,0,1]
	v_mul_f32_e32 v111, 0x41800000, v109
	v_mul_f32_e32 v119, 0x41800000, v110
	v_med3_f32 v111, v111, s25, v218
	v_med3_f32 v119, v119, s25, v218
	v_cvt_pk_fp8_f32 v127, v111, v119
	v_mul_f32_e32 v120, 0x41800000, v118
	v_mul_f32_e32 v111, 0x41800000, v121
	v_med3_f32 v119, v120, s25, v218
	v_med3_f32 v111, v111, s25, v218
	v_cvt_pk_fp8_f32 v127, v119, v111 op_sel:[0,0,1]
	global_store_dwordx2 v[144:145], v[126:127], off offset:128
.LBB0_1240:
	s_or_b64 exec, exec, s[0:1]
	v_cvt_pk_bf16_f32 v126, v122, v108
	v_cvt_pk_bf16_f32 v127, v123, v125
	v_cvt_pk_bf16_f32 v128, v109, v110
	v_cvt_pk_bf16_f32 v129, v118, v121
	v_lshlrev_b32_e32 v130, 16, v104
	v_and_b32_e32 v119, 0xffff0000, v126
	v_lshlrev_b32_e32 v111, 16, v126
	v_sub_f32_e32 v108, v108, v119
	v_sub_f32_e32 v111, v122, v111
	v_cvt_pk_bf16_f32 v122, v111, v108
	v_lshlrev_b32_e32 v108, 16, v127
	v_sub_f32_e32 v108, v123, v108
	v_and_b32_e32 v111, 0xffff0000, v127
	v_sub_f32_e32 v111, v125, v111
	v_cvt_pk_bf16_f32 v123, v108, v111
	v_lshlrev_b32_e32 v108, 16, v128
	v_sub_f32_e32 v108, v109, v108
	v_and_b32_e32 v109, 0xffff0000, v128
	v_sub_f32_e32 v109, v110, v109
	v_cvt_pk_bf16_f32 v124, v108, v109
	v_lshlrev_b32_e32 v108, 16, v129
	v_and_b32_e32 v109, 0xffff0000, v129
	v_sub_f32_e32 v108, v118, v108
	v_sub_f32_e32 v109, v121, v109
	v_cvt_pk_bf16_f32 v125, v108, v109
	ds_read_b128 v[108:111], v153 offset:1280
	v_and_b32_e32 v104, 0xffff0000, v104
	s_waitcnt lgkmcnt(0)
	v_mfma_f32_16x16x32_bf16 v[114:117], v[126:129], v[108:111], v[114:117]
	v_mul_f32_e32 v104, v112, v104
	v_mul_f32_e32 v130, v112, v130
	v_mfma_f32_16x16x32_bf16 v[108:111], v[122:125], v[108:111], v[114:117]
	s_nop 4
	ds_read_b128 v[114:117], v153 offset:34304
	s_waitcnt lgkmcnt(0)
	v_mfma_f32_16x16x32_bf16 v[108:111], v[126:129], v[114:117], v[108:111]
	ds_read_b128 v[118:121], v162 offset:4736
	ds_read_b128 v[122:125], v162 offset:640
	ds_read_b128 v[114:117], v162 offset:4752
	ds_read_b128 v[126:129], v162 offset:656
	s_waitcnt lgkmcnt(2)
	v_fma_f32 v104, v104, v123, v119
	v_lshlrev_b32_e32 v119, 16, v105
	v_and_b32_e32 v105, 0xffff0000, v105
	v_mul_f32_e32 v105, v112, v105
	v_fmac_f32_e32 v121, v105, v125
	v_lshlrev_b32_e32 v105, 16, v106
	v_mul_f32_e32 v105, v112, v105
	s_waitcnt lgkmcnt(0)
	v_fma_f32 v105, v105, v126, v114
	v_and_b32_e32 v106, 0xffff0000, v106
	v_lshlrev_b32_e32 v114, 16, v107
	v_and_b32_e32 v107, 0xffff0000, v107
	v_mul_f32_e32 v119, v112, v119
	v_mul_f32_e32 v106, v112, v106
	v_mul_f32_e32 v114, v112, v114
	v_mul_f32_e32 v107, v112, v107
	v_fma_f32 v118, v130, v122, v118
	v_fma_f32 v119, v119, v124, v120
	v_fma_f32 v106, v106, v127, v115
	v_fma_f32 v114, v114, v128, v116
	v_fmac_f32_e32 v117, v107, v129
	s_and_saveexec_b64 s[0:1], s[42:43]
	s_cbranch_execz .LBB0_1242
	v_mul_f32_e32 v107, 0x41800000, v118
	v_mul_f32_e32 v115, 0x41800000, v104
	v_med3_f32 v107, v107, s25, v218
	v_med3_f32 v115, v115, s25, v218
	v_cvt_pk_fp8_f32 v122, v107, v115
	v_mul_f32_e32 v116, 0x41800000, v119
	v_mul_f32_e32 v107, 0x41800000, v121
	v_med3_f32 v115, v116, s25, v218
	v_med3_f32 v107, v107, s25, v218
	v_cvt_pk_fp8_f32 v122, v115, v107 op_sel:[0,0,1]
	v_mul_f32_e32 v107, 0x41800000, v105
	v_mul_f32_e32 v115, 0x41800000, v106
	v_med3_f32 v107, v107, s25, v218
	v_med3_f32 v115, v115, s25, v218
	v_cvt_pk_fp8_f32 v123, v107, v115
	v_mul_f32_e32 v116, 0x41800000, v114
	v_mul_f32_e32 v107, 0x41800000, v117
	v_med3_f32 v115, v116, s25, v218
	v_med3_f32 v107, v107, s25, v218
	v_cvt_pk_fp8_f32 v123, v115, v107 op_sel:[0,0,1]
	global_store_dwordx2 v[144:145], v[122:123], off offset:160
.LBB0_1242:
	s_or_b64 exec, exec, s[0:1]
	v_cvt_pk_bf16_f32 v122, v118, v104
	v_cvt_pk_bf16_f32 v123, v119, v121
	v_cvt_pk_bf16_f32 v124, v105, v106
	v_cvt_pk_bf16_f32 v125, v114, v117
	s_nop 0
	v_and_b32_e32 v115, 0xffff0000, v122
	v_lshlrev_b32_e32 v107, 16, v122
	v_sub_f32_e32 v104, v104, v115
	v_sub_f32_e32 v107, v118, v107
	v_cvt_pk_bf16_f32 v118, v107, v104
	v_lshlrev_b32_e32 v104, 16, v123
	v_sub_f32_e32 v104, v119, v104
	v_and_b32_e32 v107, 0xffff0000, v123
	v_sub_f32_e32 v107, v121, v107
	v_cvt_pk_bf16_f32 v119, v104, v107
	v_lshlrev_b32_e32 v104, 16, v124
	v_sub_f32_e32 v104, v105, v104
	v_and_b32_e32 v105, 0xffff0000, v124
	v_sub_f32_e32 v105, v106, v105
	v_cvt_pk_bf16_f32 v120, v104, v105
	v_lshlrev_b32_e32 v104, 16, v125
	v_and_b32_e32 v105, 0xffff0000, v125
	v_sub_f32_e32 v104, v114, v104
	v_sub_f32_e32 v105, v117, v105
	v_cvt_pk_bf16_f32 v121, v104, v105
	ds_read_b128 v[104:107], v153 offset:1344
	s_waitcnt lgkmcnt(0)
	v_mfma_f32_16x16x32_bf16 v[108:111], v[122:125], v[104:107], v[108:111]
	v_mfma_f32_16x16x32_bf16 v[104:107], v[118:121], v[104:107], v[108:111]
	s_nop 6
	ds_read_b128 v[108:111], v153 offset:34368
	s_waitcnt lgkmcnt(0)
	v_mfma_f32_16x16x32_bf16 v[104:107], v[122:125], v[108:111], v[104:107]
	ds_read_b128 v[114:117], v162 offset:4864
	ds_read_b128 v[118:121], v162 offset:768
	ds_read_b128 v[122:125], v162 offset:784
	ds_read_b128 v[108:111], v162 offset:4880
	v_lshlrev_b32_e32 v126, 16, v100
	v_and_b32_e32 v100, 0xffff0000, v100
	v_mul_f32_e32 v100, v112, v100
	s_waitcnt lgkmcnt(2)
	v_fma_f32 v100, v100, v119, v115
	v_lshlrev_b32_e32 v115, 16, v101
	v_and_b32_e32 v101, 0xffff0000, v101
	v_mul_f32_e32 v101, v112, v101
	v_fmac_f32_e32 v117, v101, v121
	v_lshlrev_b32_e32 v101, 16, v102
	v_mul_f32_e32 v101, v112, v101
	s_waitcnt lgkmcnt(0)
	v_fma_f32 v101, v101, v122, v108
	v_and_b32_e32 v102, 0xffff0000, v102
	v_lshlrev_b32_e32 v108, 16, v103
	v_and_b32_e32 v103, 0xffff0000, v103
	v_mul_f32_e32 v126, v112, v126
	v_mul_f32_e32 v115, v112, v115
	v_mul_f32_e32 v102, v112, v102
	v_mul_f32_e32 v108, v112, v108
	v_mul_f32_e32 v103, v112, v103
	v_fma_f32 v114, v126, v118, v114
	v_fma_f32 v115, v115, v120, v116
	v_fma_f32 v102, v102, v123, v109
	v_fma_f32 v108, v108, v124, v110
	v_fmac_f32_e32 v111, v103, v125
	s_and_saveexec_b64 s[0:1], s[42:43]
	s_cbranch_execz .LBB0_1244
	v_mul_f32_e32 v103, 0x41800000, v114
	v_mul_f32_e32 v109, 0x41800000, v100
	v_med3_f32 v103, v103, s25, v218
	v_med3_f32 v109, v109, s25, v218
	v_cvt_pk_fp8_f32 v118, v103, v109
	v_mul_f32_e32 v110, 0x41800000, v115
	v_mul_f32_e32 v103, 0x41800000, v117
	v_med3_f32 v109, v110, s25, v218
	v_med3_f32 v103, v103, s25, v218
	v_cvt_pk_fp8_f32 v118, v109, v103 op_sel:[0,0,1]
	v_mul_f32_e32 v103, 0x41800000, v101
	v_mul_f32_e32 v109, 0x41800000, v102
	v_med3_f32 v103, v103, s25, v218
	v_med3_f32 v109, v109, s25, v218
	v_cvt_pk_fp8_f32 v119, v103, v109
	v_mul_f32_e32 v110, 0x41800000, v108
	v_mul_f32_e32 v103, 0x41800000, v111
	v_med3_f32 v109, v110, s25, v218
	v_med3_f32 v103, v103, s25, v218
	v_cvt_pk_fp8_f32 v119, v109, v103 op_sel:[0,0,1]
	global_store_dwordx2 v[144:145], v[118:119], off offset:192
.LBB0_1244:
	s_or_b64 exec, exec, s[0:1]
	v_cvt_pk_bf16_f32 v118, v114, v100
	v_cvt_pk_bf16_f32 v119, v115, v117
	v_cvt_pk_bf16_f32 v120, v101, v102
	v_cvt_pk_bf16_f32 v121, v108, v111
	v_lshlrev_b32_e32 v122, 16, v96
	v_and_b32_e32 v109, 0xffff0000, v118
	v_lshlrev_b32_e32 v103, 16, v118
	v_sub_f32_e32 v100, v100, v109
	v_sub_f32_e32 v103, v114, v103
	v_cvt_pk_bf16_f32 v114, v103, v100
	v_lshlrev_b32_e32 v100, 16, v119
	v_sub_f32_e32 v100, v115, v100
	v_and_b32_e32 v103, 0xffff0000, v119
	v_sub_f32_e32 v103, v117, v103
	v_cvt_pk_bf16_f32 v115, v100, v103
	v_lshlrev_b32_e32 v100, 16, v120
	v_sub_f32_e32 v100, v101, v100
	v_and_b32_e32 v101, 0xffff0000, v120
	v_sub_f32_e32 v101, v102, v101
	v_cvt_pk_bf16_f32 v116, v100, v101
	v_lshlrev_b32_e32 v100, 16, v121
	v_and_b32_e32 v101, 0xffff0000, v121
	v_sub_f32_e32 v100, v108, v100
	v_sub_f32_e32 v101, v111, v101
	v_cvt_pk_bf16_f32 v117, v100, v101
	ds_read_b128 v[100:103], v153 offset:1408
	v_and_b32_e32 v96, 0xffff0000, v96
	s_waitcnt lgkmcnt(0)
	v_mfma_f32_16x16x32_bf16 v[104:107], v[118:121], v[100:103], v[104:107]
	v_mul_f32_e32 v96, v112, v96
	v_mul_f32_e32 v122, v112, v122
	v_mfma_f32_16x16x32_bf16 v[100:103], v[114:117], v[100:103], v[104:107]
	s_nop 4
	ds_read_b128 v[104:107], v153 offset:34432
	s_waitcnt lgkmcnt(0)
	v_mfma_f32_16x16x32_bf16 v[100:103], v[118:121], v[104:107], v[100:103]
	ds_read_b128 v[108:111], v162 offset:4992
	ds_read_b128 v[114:117], v162 offset:896
	ds_read_b128 v[104:107], v162 offset:5008
	ds_read_b128 v[118:121], v162 offset:912
	s_waitcnt lgkmcnt(2)
	v_fma_f32 v96, v96, v115, v109
	v_lshlrev_b32_e32 v109, 16, v97
	v_and_b32_e32 v97, 0xffff0000, v97
	v_mul_f32_e32 v97, v112, v97
	v_fmac_f32_e32 v111, v97, v117
	v_lshlrev_b32_e32 v97, 16, v98
	v_mul_f32_e32 v97, v112, v97
	s_waitcnt lgkmcnt(0)
	v_fma_f32 v97, v97, v118, v104
	v_and_b32_e32 v98, 0xffff0000, v98
	v_lshlrev_b32_e32 v104, 16, v99
	v_and_b32_e32 v99, 0xffff0000, v99
	v_mul_f32_e32 v109, v112, v109
	v_mul_f32_e32 v98, v112, v98
	v_mul_f32_e32 v104, v112, v104
	v_mul_f32_e32 v99, v112, v99
	v_fma_f32 v108, v122, v114, v108
	v_fma_f32 v109, v109, v116, v110
	v_fma_f32 v98, v98, v119, v105
	v_fma_f32 v104, v104, v120, v106
	v_fmac_f32_e32 v107, v99, v121
	s_and_saveexec_b64 s[0:1], s[42:43]
	s_cbranch_execz .LBB0_1246
	v_mul_f32_e32 v99, 0x41800000, v108
	v_mul_f32_e32 v105, 0x41800000, v96
	v_med3_f32 v99, v99, s25, v218
	v_med3_f32 v105, v105, s25, v218
	v_cvt_pk_fp8_f32 v114, v99, v105
	v_mul_f32_e32 v106, 0x41800000, v109
	v_mul_f32_e32 v99, 0x41800000, v111
	v_med3_f32 v105, v106, s25, v218
	v_med3_f32 v99, v99, s25, v218
	v_cvt_pk_fp8_f32 v114, v105, v99 op_sel:[0,0,1]
	v_mul_f32_e32 v99, 0x41800000, v97
	v_mul_f32_e32 v105, 0x41800000, v98
	v_med3_f32 v99, v99, s25, v218
	v_med3_f32 v105, v105, s25, v218
	v_cvt_pk_fp8_f32 v115, v99, v105
	v_mul_f32_e32 v106, 0x41800000, v104
	v_mul_f32_e32 v99, 0x41800000, v107
	v_med3_f32 v105, v106, s25, v218
	v_med3_f32 v99, v99, s25, v218
	v_cvt_pk_fp8_f32 v115, v105, v99 op_sel:[0,0,1]
	global_store_dwordx2 v[144:145], v[114:115], off offset:224
.LBB0_1246:
	s_or_b64 exec, exec, s[0:1]
	v_cvt_pk_bf16_f32 v114, v108, v96
	v_cvt_pk_bf16_f32 v115, v109, v111
	v_cvt_pk_bf16_f32 v116, v97, v98
	v_cvt_pk_bf16_f32 v117, v104, v107
	s_nop 0
	v_and_b32_e32 v105, 0xffff0000, v114
	v_lshlrev_b32_e32 v99, 16, v114
	v_sub_f32_e32 v96, v96, v105
	v_sub_f32_e32 v99, v108, v99
	v_cvt_pk_bf16_f32 v108, v99, v96
	v_lshlrev_b32_e32 v96, 16, v115
	v_sub_f32_e32 v96, v109, v96
	v_and_b32_e32 v99, 0xffff0000, v115
	v_sub_f32_e32 v99, v111, v99
	v_cvt_pk_bf16_f32 v109, v96, v99
	v_lshlrev_b32_e32 v96, 16, v116
	v_sub_f32_e32 v96, v97, v96
	v_and_b32_e32 v97, 0xffff0000, v116
	v_sub_f32_e32 v97, v98, v97
	v_cvt_pk_bf16_f32 v110, v96, v97
	v_lshlrev_b32_e32 v96, 16, v117
	v_and_b32_e32 v97, 0xffff0000, v117
	v_sub_f32_e32 v96, v104, v96
	v_sub_f32_e32 v97, v107, v97
	v_cvt_pk_bf16_f32 v111, v96, v97
	ds_read_b128 v[96:99], v153 offset:1472
	s_waitcnt lgkmcnt(0)
	v_mfma_f32_16x16x32_bf16 v[100:103], v[114:117], v[96:99], v[100:103]
	v_mfma_f32_16x16x32_bf16 v[96:99], v[108:111], v[96:99], v[100:103]
	s_nop 6
	ds_read_b128 v[100:103], v153 offset:34496
	s_waitcnt lgkmcnt(0)
	v_mfma_f32_16x16x32_bf16 v[96:99], v[114:117], v[100:103], v[96:99]
	ds_read_b128 v[104:107], v162 offset:5120
	ds_read_b128 v[108:111], v162 offset:1024
	ds_read_b128 v[114:117], v162 offset:1040
	ds_read_b128 v[100:103], v162 offset:5136
	v_lshlrev_b32_e32 v118, 16, v92
	v_and_b32_e32 v92, 0xffff0000, v92
	v_mul_f32_e32 v92, v112, v92
	s_waitcnt lgkmcnt(2)
	v_fma_f32 v92, v92, v109, v105
	v_lshlrev_b32_e32 v105, 16, v93
	v_and_b32_e32 v93, 0xffff0000, v93
	v_mul_f32_e32 v93, v112, v93
	v_fmac_f32_e32 v107, v93, v111
	v_lshlrev_b32_e32 v93, 16, v94
	v_mul_f32_e32 v93, v112, v93
	s_waitcnt lgkmcnt(0)
	v_fma_f32 v93, v93, v114, v100
	v_and_b32_e32 v94, 0xffff0000, v94
	v_lshlrev_b32_e32 v100, 16, v95
	v_and_b32_e32 v95, 0xffff0000, v95
	v_mul_f32_e32 v118, v112, v118
	v_mul_f32_e32 v105, v112, v105
	v_mul_f32_e32 v94, v112, v94
	v_mul_f32_e32 v100, v112, v100
	v_mul_f32_e32 v95, v112, v95
	v_fma_f32 v104, v118, v108, v104
	v_fma_f32 v105, v105, v110, v106
	v_fma_f32 v94, v94, v115, v101
	v_fma_f32 v100, v100, v116, v102
	v_fmac_f32_e32 v103, v95, v117
	s_and_saveexec_b64 s[0:1], s[42:43]
	s_cbranch_execz .LBB0_1248
	v_mul_f32_e32 v95, 0x41800000, v104
	v_mul_f32_e32 v101, 0x41800000, v92
	v_med3_f32 v95, v95, s25, v218
	v_med3_f32 v101, v101, s25, v218
	v_cvt_pk_fp8_f32 v108, v95, v101
	v_mul_f32_e32 v102, 0x41800000, v105
	v_mul_f32_e32 v95, 0x41800000, v107
	v_med3_f32 v101, v102, s25, v218
	v_med3_f32 v95, v95, s25, v218
	v_cvt_pk_fp8_f32 v108, v101, v95 op_sel:[0,0,1]
	v_mul_f32_e32 v95, 0x41800000, v93
	v_mul_f32_e32 v101, 0x41800000, v94
	v_med3_f32 v95, v95, s25, v218
	v_med3_f32 v101, v101, s25, v218
	v_cvt_pk_fp8_f32 v109, v95, v101
	v_mul_f32_e32 v102, 0x41800000, v100
	v_mul_f32_e32 v95, 0x41800000, v103
	v_med3_f32 v101, v102, s25, v218
	v_med3_f32 v95, v95, s25, v218
	v_cvt_pk_fp8_f32 v109, v101, v95 op_sel:[0,0,1]
	global_store_dwordx2 v[144:145], v[108:109], off offset:256
.LBB0_1248:
	s_or_b64 exec, exec, s[0:1]
	v_cvt_pk_bf16_f32 v108, v104, v92
	v_cvt_pk_bf16_f32 v109, v105, v107
	v_cvt_pk_bf16_f32 v110, v93, v94
	v_cvt_pk_bf16_f32 v111, v100, v103
	v_lshlrev_b32_e32 v114, 16, v88
	v_and_b32_e32 v101, 0xffff0000, v108
	v_lshlrev_b32_e32 v95, 16, v108
	v_sub_f32_e32 v92, v92, v101
	v_sub_f32_e32 v95, v104, v95
	v_cvt_pk_bf16_f32 v104, v95, v92
	v_lshlrev_b32_e32 v92, 16, v109
	v_sub_f32_e32 v92, v105, v92
	v_and_b32_e32 v95, 0xffff0000, v109
	v_sub_f32_e32 v95, v107, v95
	v_cvt_pk_bf16_f32 v105, v92, v95
	v_lshlrev_b32_e32 v92, 16, v110
	v_sub_f32_e32 v92, v93, v92
	v_and_b32_e32 v93, 0xffff0000, v110
	v_sub_f32_e32 v93, v94, v93
	v_cvt_pk_bf16_f32 v106, v92, v93
	v_lshlrev_b32_e32 v92, 16, v111
	v_and_b32_e32 v93, 0xffff0000, v111
	v_sub_f32_e32 v92, v100, v92
	v_sub_f32_e32 v93, v103, v93
	v_cvt_pk_bf16_f32 v107, v92, v93
	ds_read_b128 v[92:95], v153 offset:1536
	v_and_b32_e32 v88, 0xffff0000, v88
	s_waitcnt lgkmcnt(0)
	v_mfma_f32_16x16x32_bf16 v[96:99], v[108:111], v[92:95], v[96:99]
	v_mul_f32_e32 v88, v112, v88
	v_mul_f32_e32 v114, v112, v114
	v_mfma_f32_16x16x32_bf16 v[92:95], v[104:107], v[92:95], v[96:99]
	s_nop 4
	ds_read_b128 v[96:99], v153 offset:34560
	s_waitcnt lgkmcnt(0)
	v_mfma_f32_16x16x32_bf16 v[92:95], v[108:111], v[96:99], v[92:95]
	ds_read_b128 v[100:103], v162 offset:5248
	ds_read_b128 v[104:107], v162 offset:1152
	ds_read_b128 v[96:99], v162 offset:5264
	ds_read_b128 v[108:111], v162 offset:1168
	s_waitcnt lgkmcnt(2)
	v_fma_f32 v88, v88, v105, v101
	v_lshlrev_b32_e32 v101, 16, v89
	v_and_b32_e32 v89, 0xffff0000, v89
	v_mul_f32_e32 v89, v112, v89
	v_fmac_f32_e32 v103, v89, v107
	v_lshlrev_b32_e32 v89, 16, v90
	v_mul_f32_e32 v89, v112, v89
	s_waitcnt lgkmcnt(0)
	v_fma_f32 v89, v89, v108, v96
	v_and_b32_e32 v90, 0xffff0000, v90
	v_lshlrev_b32_e32 v96, 16, v91
	v_and_b32_e32 v91, 0xffff0000, v91
	v_mul_f32_e32 v101, v112, v101
	v_mul_f32_e32 v90, v112, v90
	v_mul_f32_e32 v96, v112, v96
	v_mul_f32_e32 v91, v112, v91
	v_fma_f32 v100, v114, v104, v100
	v_fma_f32 v101, v101, v106, v102
	v_fma_f32 v90, v90, v109, v97
	v_fma_f32 v96, v96, v110, v98
	v_fmac_f32_e32 v99, v91, v111
	s_and_saveexec_b64 s[0:1], s[42:43]
	s_cbranch_execz .LBB0_1250
	v_mul_f32_e32 v91, 0x41800000, v100
	v_mul_f32_e32 v97, 0x41800000, v88
	v_med3_f32 v91, v91, s25, v218
	v_med3_f32 v97, v97, s25, v218
	v_cvt_pk_fp8_f32 v104, v91, v97
	v_mul_f32_e32 v98, 0x41800000, v101
	v_mul_f32_e32 v91, 0x41800000, v103
	v_med3_f32 v97, v98, s25, v218
	v_med3_f32 v91, v91, s25, v218
	v_cvt_pk_fp8_f32 v104, v97, v91 op_sel:[0,0,1]
	v_mul_f32_e32 v91, 0x41800000, v89
	v_mul_f32_e32 v97, 0x41800000, v90
	v_med3_f32 v91, v91, s25, v218
	v_med3_f32 v97, v97, s25, v218
	v_cvt_pk_fp8_f32 v105, v91, v97
	v_mul_f32_e32 v98, 0x41800000, v96
	v_mul_f32_e32 v91, 0x41800000, v99
	v_med3_f32 v97, v98, s25, v218
	v_med3_f32 v91, v91, s25, v218
	v_cvt_pk_fp8_f32 v105, v97, v91 op_sel:[0,0,1]
	global_store_dwordx2 v[144:145], v[104:105], off offset:288
.LBB0_1250:
	s_or_b64 exec, exec, s[0:1]
	v_cvt_pk_bf16_f32 v104, v100, v88
	v_cvt_pk_bf16_f32 v105, v101, v103
	v_cvt_pk_bf16_f32 v106, v89, v90
	v_cvt_pk_bf16_f32 v107, v96, v99
	s_nop 0
	v_and_b32_e32 v97, 0xffff0000, v104
	v_lshlrev_b32_e32 v91, 16, v104
	v_sub_f32_e32 v88, v88, v97
	v_sub_f32_e32 v91, v100, v91
	v_cvt_pk_bf16_f32 v100, v91, v88
	v_lshlrev_b32_e32 v88, 16, v105
	v_sub_f32_e32 v88, v101, v88
	v_and_b32_e32 v91, 0xffff0000, v105
	v_sub_f32_e32 v91, v103, v91
	v_cvt_pk_bf16_f32 v101, v88, v91
	v_lshlrev_b32_e32 v88, 16, v106
	v_sub_f32_e32 v88, v89, v88
	v_and_b32_e32 v89, 0xffff0000, v106
	v_sub_f32_e32 v89, v90, v89
	v_cvt_pk_bf16_f32 v102, v88, v89
	v_lshlrev_b32_e32 v88, 16, v107
	v_and_b32_e32 v89, 0xffff0000, v107
	v_sub_f32_e32 v88, v96, v88
	v_sub_f32_e32 v89, v99, v89
	v_cvt_pk_bf16_f32 v103, v88, v89
	ds_read_b128 v[88:91], v153 offset:1600
	s_waitcnt lgkmcnt(0)
	v_mfma_f32_16x16x32_bf16 v[92:95], v[104:107], v[88:91], v[92:95]
	v_mfma_f32_16x16x32_bf16 v[88:91], v[100:103], v[88:91], v[92:95]
	s_nop 6
	ds_read_b128 v[92:95], v153 offset:34624
	s_waitcnt lgkmcnt(0)
	v_mfma_f32_16x16x32_bf16 v[88:91], v[104:107], v[92:95], v[88:91]
	ds_read_b128 v[96:99], v162 offset:5376
	ds_read_b128 v[100:103], v162 offset:1280
	ds_read_b128 v[104:107], v162 offset:1296
	ds_read_b128 v[92:95], v162 offset:5392
	v_lshlrev_b32_e32 v108, 16, v84
	v_and_b32_e32 v84, 0xffff0000, v84
	v_mul_f32_e32 v84, v112, v84
	s_waitcnt lgkmcnt(2)
	v_fma_f32 v84, v84, v101, v97
	v_lshlrev_b32_e32 v97, 16, v85
	v_and_b32_e32 v85, 0xffff0000, v85
	v_mul_f32_e32 v85, v112, v85
	v_fmac_f32_e32 v99, v85, v103
	v_lshlrev_b32_e32 v85, 16, v86
	v_mul_f32_e32 v85, v112, v85
	s_waitcnt lgkmcnt(0)
	v_fma_f32 v85, v85, v104, v92
	v_and_b32_e32 v86, 0xffff0000, v86
	v_lshlrev_b32_e32 v92, 16, v87
	v_and_b32_e32 v87, 0xffff0000, v87
	v_mul_f32_e32 v108, v112, v108
	v_mul_f32_e32 v97, v112, v97
	v_mul_f32_e32 v86, v112, v86
	v_mul_f32_e32 v92, v112, v92
	v_mul_f32_e32 v87, v112, v87
	v_fma_f32 v96, v108, v100, v96
	v_fma_f32 v97, v97, v102, v98
	v_fma_f32 v86, v86, v105, v93
	v_fma_f32 v92, v92, v106, v94
	v_fmac_f32_e32 v95, v87, v107
	s_and_saveexec_b64 s[0:1], s[42:43]
	s_cbranch_execz .LBB0_1252
	v_mul_f32_e32 v87, 0x41800000, v96
	v_mul_f32_e32 v93, 0x41800000, v84
	v_med3_f32 v87, v87, s25, v218
	v_med3_f32 v93, v93, s25, v218
	v_cvt_pk_fp8_f32 v100, v87, v93
	v_mul_f32_e32 v94, 0x41800000, v97
	v_mul_f32_e32 v87, 0x41800000, v99
	v_med3_f32 v93, v94, s25, v218
	v_med3_f32 v87, v87, s25, v218
	v_cvt_pk_fp8_f32 v100, v93, v87 op_sel:[0,0,1]
	v_mul_f32_e32 v87, 0x41800000, v85
	v_mul_f32_e32 v93, 0x41800000, v86
	v_med3_f32 v87, v87, s25, v218
	v_med3_f32 v93, v93, s25, v218
	v_cvt_pk_fp8_f32 v101, v87, v93
	v_mul_f32_e32 v94, 0x41800000, v92
	v_mul_f32_e32 v87, 0x41800000, v95
	v_med3_f32 v93, v94, s25, v218
	v_med3_f32 v87, v87, s25, v218
	v_cvt_pk_fp8_f32 v101, v93, v87 op_sel:[0,0,1]
	global_store_dwordx2 v[144:145], v[100:101], off offset:320
.LBB0_1252:
	s_or_b64 exec, exec, s[0:1]
	v_cvt_pk_bf16_f32 v100, v96, v84
	v_cvt_pk_bf16_f32 v101, v97, v99
	v_cvt_pk_bf16_f32 v102, v85, v86
	v_cvt_pk_bf16_f32 v103, v92, v95
	v_lshlrev_b32_e32 v104, 16, v80
	v_and_b32_e32 v93, 0xffff0000, v100
	v_lshlrev_b32_e32 v87, 16, v100
	v_sub_f32_e32 v84, v84, v93
	v_sub_f32_e32 v87, v96, v87
	v_cvt_pk_bf16_f32 v96, v87, v84
	v_lshlrev_b32_e32 v84, 16, v101
	v_sub_f32_e32 v84, v97, v84
	v_and_b32_e32 v87, 0xffff0000, v101
	v_sub_f32_e32 v87, v99, v87
	v_cvt_pk_bf16_f32 v97, v84, v87
	v_lshlrev_b32_e32 v84, 16, v102
	v_sub_f32_e32 v84, v85, v84
	v_and_b32_e32 v85, 0xffff0000, v102
	v_sub_f32_e32 v85, v86, v85
	v_cvt_pk_bf16_f32 v98, v84, v85
	v_lshlrev_b32_e32 v84, 16, v103
	v_and_b32_e32 v85, 0xffff0000, v103
	v_sub_f32_e32 v84, v92, v84
	v_sub_f32_e32 v85, v95, v85
	v_cvt_pk_bf16_f32 v99, v84, v85
	ds_read_b128 v[84:87], v153 offset:1664
	v_and_b32_e32 v80, 0xffff0000, v80
	s_waitcnt lgkmcnt(0)
	v_mfma_f32_16x16x32_bf16 v[88:91], v[100:103], v[84:87], v[88:91]
	v_mul_f32_e32 v80, v112, v80
	v_mul_f32_e32 v104, v112, v104
	v_mfma_f32_16x16x32_bf16 v[84:87], v[96:99], v[84:87], v[88:91]
	s_nop 4
	ds_read_b128 v[88:91], v153 offset:34688
	s_waitcnt lgkmcnt(0)
	v_mfma_f32_16x16x32_bf16 v[84:87], v[100:103], v[88:91], v[84:87]
	ds_read_b128 v[92:95], v162 offset:5504
	ds_read_b128 v[96:99], v162 offset:1408
	ds_read_b128 v[88:91], v162 offset:5520
	ds_read_b128 v[100:103], v162 offset:1424
	s_waitcnt lgkmcnt(2)
	v_fma_f32 v80, v80, v97, v93
	v_lshlrev_b32_e32 v93, 16, v81
	v_and_b32_e32 v81, 0xffff0000, v81
	v_mul_f32_e32 v81, v112, v81
	v_fmac_f32_e32 v95, v81, v99
	v_lshlrev_b32_e32 v81, 16, v82
	v_mul_f32_e32 v81, v112, v81
	s_waitcnt lgkmcnt(0)
	v_fma_f32 v81, v81, v100, v88
	v_and_b32_e32 v82, 0xffff0000, v82
	v_lshlrev_b32_e32 v88, 16, v83
	v_and_b32_e32 v83, 0xffff0000, v83
	v_mul_f32_e32 v93, v112, v93
	v_mul_f32_e32 v82, v112, v82
	v_mul_f32_e32 v88, v112, v88
	v_mul_f32_e32 v83, v112, v83
	v_fma_f32 v92, v104, v96, v92
	v_fma_f32 v93, v93, v98, v94
	v_fma_f32 v82, v82, v101, v89
	v_fma_f32 v88, v88, v102, v90
	v_fmac_f32_e32 v91, v83, v103
	s_and_saveexec_b64 s[0:1], s[42:43]
	s_cbranch_execz .LBB0_1254
	v_mul_f32_e32 v83, 0x41800000, v92
	v_mul_f32_e32 v89, 0x41800000, v80
	v_med3_f32 v83, v83, s25, v218
	v_med3_f32 v89, v89, s25, v218
	v_cvt_pk_fp8_f32 v96, v83, v89
	v_mul_f32_e32 v90, 0x41800000, v93
	v_mul_f32_e32 v83, 0x41800000, v95
	v_med3_f32 v89, v90, s25, v218
	v_med3_f32 v83, v83, s25, v218
	v_cvt_pk_fp8_f32 v96, v89, v83 op_sel:[0,0,1]
	v_mul_f32_e32 v83, 0x41800000, v81
	v_mul_f32_e32 v89, 0x41800000, v82
	v_med3_f32 v83, v83, s25, v218
	v_med3_f32 v89, v89, s25, v218
	v_cvt_pk_fp8_f32 v97, v83, v89
	v_mul_f32_e32 v90, 0x41800000, v88
	v_mul_f32_e32 v83, 0x41800000, v91
	v_med3_f32 v89, v90, s25, v218
	v_med3_f32 v83, v83, s25, v218
	v_cvt_pk_fp8_f32 v97, v89, v83 op_sel:[0,0,1]
	global_store_dwordx2 v[144:145], v[96:97], off offset:352
.LBB0_1254:
	s_or_b64 exec, exec, s[0:1]
	v_cvt_pk_bf16_f32 v96, v92, v80
	v_cvt_pk_bf16_f32 v97, v93, v95
	v_cvt_pk_bf16_f32 v98, v81, v82
	v_cvt_pk_bf16_f32 v99, v88, v91
	s_nop 0
	v_and_b32_e32 v89, 0xffff0000, v96
	v_lshlrev_b32_e32 v83, 16, v96
	v_sub_f32_e32 v80, v80, v89
	v_sub_f32_e32 v83, v92, v83
	v_cvt_pk_bf16_f32 v92, v83, v80
	v_lshlrev_b32_e32 v80, 16, v97
	v_sub_f32_e32 v80, v93, v80
	v_and_b32_e32 v83, 0xffff0000, v97
	v_sub_f32_e32 v83, v95, v83
	v_cvt_pk_bf16_f32 v93, v80, v83
	v_lshlrev_b32_e32 v80, 16, v98
	v_sub_f32_e32 v80, v81, v80
	v_and_b32_e32 v81, 0xffff0000, v98
	v_sub_f32_e32 v81, v82, v81
	v_cvt_pk_bf16_f32 v94, v80, v81
	v_lshlrev_b32_e32 v80, 16, v99
	v_and_b32_e32 v81, 0xffff0000, v99
	v_sub_f32_e32 v80, v88, v80
	v_sub_f32_e32 v81, v91, v81
	v_cvt_pk_bf16_f32 v95, v80, v81
	ds_read_b128 v[80:83], v153 offset:1728
	s_waitcnt lgkmcnt(0)
	v_mfma_f32_16x16x32_bf16 v[84:87], v[96:99], v[80:83], v[84:87]
	v_mfma_f32_16x16x32_bf16 v[80:83], v[92:95], v[80:83], v[84:87]
	s_nop 6
	ds_read_b128 v[84:87], v153 offset:34752
	s_waitcnt lgkmcnt(0)
	v_mfma_f32_16x16x32_bf16 v[80:83], v[96:99], v[84:87], v[80:83]
	ds_read_b128 v[88:91], v162 offset:5632
	ds_read_b128 v[92:95], v162 offset:1536
	ds_read_b128 v[96:99], v162 offset:1552
	ds_read_b128 v[84:87], v162 offset:5648
	v_lshlrev_b32_e32 v100, 16, v76
	v_and_b32_e32 v76, 0xffff0000, v76
	v_mul_f32_e32 v76, v112, v76
	s_waitcnt lgkmcnt(2)
	v_fma_f32 v76, v76, v93, v89
	v_lshlrev_b32_e32 v89, 16, v77
	v_and_b32_e32 v77, 0xffff0000, v77
	v_mul_f32_e32 v77, v112, v77
	v_fmac_f32_e32 v91, v77, v95
	v_lshlrev_b32_e32 v77, 16, v78
	v_mul_f32_e32 v77, v112, v77
	s_waitcnt lgkmcnt(0)
	v_fma_f32 v77, v77, v96, v84
	v_and_b32_e32 v78, 0xffff0000, v78
	v_lshlrev_b32_e32 v84, 16, v79
	v_and_b32_e32 v79, 0xffff0000, v79
	v_mul_f32_e32 v100, v112, v100
	v_mul_f32_e32 v89, v112, v89
	v_mul_f32_e32 v78, v112, v78
	v_mul_f32_e32 v84, v112, v84
	v_mul_f32_e32 v79, v112, v79
	v_fma_f32 v88, v100, v92, v88
	v_fma_f32 v89, v89, v94, v90
	v_fma_f32 v78, v78, v97, v85
	v_fma_f32 v84, v84, v98, v86
	v_fmac_f32_e32 v87, v79, v99
	s_and_saveexec_b64 s[0:1], s[42:43]
	s_cbranch_execz .LBB0_1256
	v_mul_f32_e32 v79, 0x41800000, v88
	v_mul_f32_e32 v85, 0x41800000, v76
	v_med3_f32 v79, v79, s25, v218
	v_med3_f32 v85, v85, s25, v218
	v_cvt_pk_fp8_f32 v92, v79, v85
	v_mul_f32_e32 v86, 0x41800000, v89
	v_mul_f32_e32 v79, 0x41800000, v91
	v_med3_f32 v85, v86, s25, v218
	v_med3_f32 v79, v79, s25, v218
	v_cvt_pk_fp8_f32 v92, v85, v79 op_sel:[0,0,1]
	v_mul_f32_e32 v79, 0x41800000, v77
	v_mul_f32_e32 v85, 0x41800000, v78
	v_med3_f32 v79, v79, s25, v218
	v_med3_f32 v85, v85, s25, v218
	v_cvt_pk_fp8_f32 v93, v79, v85
	v_mul_f32_e32 v86, 0x41800000, v84
	v_mul_f32_e32 v79, 0x41800000, v87
	v_med3_f32 v85, v86, s25, v218
	v_med3_f32 v79, v79, s25, v218
	v_cvt_pk_fp8_f32 v93, v85, v79 op_sel:[0,0,1]
	global_store_dwordx2 v[144:145], v[92:93], off offset:384
.LBB0_1256:
	s_or_b64 exec, exec, s[0:1]
	v_cvt_pk_bf16_f32 v92, v88, v76
	v_cvt_pk_bf16_f32 v93, v89, v91
	v_cvt_pk_bf16_f32 v94, v77, v78
	v_cvt_pk_bf16_f32 v95, v84, v87
	v_lshlrev_b32_e32 v96, 16, v72
	v_and_b32_e32 v85, 0xffff0000, v92
	v_lshlrev_b32_e32 v79, 16, v92
	v_sub_f32_e32 v76, v76, v85
	v_sub_f32_e32 v79, v88, v79
	v_cvt_pk_bf16_f32 v88, v79, v76
	v_lshlrev_b32_e32 v76, 16, v93
	v_sub_f32_e32 v76, v89, v76
	v_and_b32_e32 v79, 0xffff0000, v93
	v_sub_f32_e32 v79, v91, v79
	v_cvt_pk_bf16_f32 v89, v76, v79
	v_lshlrev_b32_e32 v76, 16, v94
	v_sub_f32_e32 v76, v77, v76
	v_and_b32_e32 v77, 0xffff0000, v94
	v_sub_f32_e32 v77, v78, v77
	v_cvt_pk_bf16_f32 v90, v76, v77
	v_lshlrev_b32_e32 v76, 16, v95
	v_and_b32_e32 v77, 0xffff0000, v95
	v_sub_f32_e32 v76, v84, v76
	v_sub_f32_e32 v77, v87, v77
	v_cvt_pk_bf16_f32 v91, v76, v77
	ds_read_b128 v[76:79], v153 offset:1792
	v_and_b32_e32 v72, 0xffff0000, v72
	s_waitcnt lgkmcnt(0)
	v_mfma_f32_16x16x32_bf16 v[80:83], v[92:95], v[76:79], v[80:83]
	v_mul_f32_e32 v72, v112, v72
	v_mul_f32_e32 v96, v112, v96
	v_mfma_f32_16x16x32_bf16 v[76:79], v[88:91], v[76:79], v[80:83]
	s_nop 4
	ds_read_b128 v[80:83], v153 offset:34816
	s_waitcnt lgkmcnt(0)
	v_mfma_f32_16x16x32_bf16 v[76:79], v[92:95], v[80:83], v[76:79]
	ds_read_b128 v[84:87], v162 offset:5760
	ds_read_b128 v[88:91], v162 offset:1664
	ds_read_b128 v[80:83], v162 offset:5776
	ds_read_b128 v[92:95], v162 offset:1680
	s_waitcnt lgkmcnt(2)
	v_fma_f32 v72, v72, v89, v85
	v_lshlrev_b32_e32 v85, 16, v73
	v_and_b32_e32 v73, 0xffff0000, v73
	v_mul_f32_e32 v73, v112, v73
	v_fmac_f32_e32 v87, v73, v91
	v_lshlrev_b32_e32 v73, 16, v74
	v_mul_f32_e32 v73, v112, v73
	s_waitcnt lgkmcnt(0)
	v_fma_f32 v73, v73, v92, v80
	v_and_b32_e32 v74, 0xffff0000, v74
	v_lshlrev_b32_e32 v80, 16, v75
	v_and_b32_e32 v75, 0xffff0000, v75
	v_mul_f32_e32 v85, v112, v85
	v_mul_f32_e32 v74, v112, v74
	v_mul_f32_e32 v80, v112, v80
	v_mul_f32_e32 v75, v112, v75
	v_fma_f32 v84, v96, v88, v84
	v_fma_f32 v85, v85, v90, v86
	v_fma_f32 v74, v74, v93, v81
	v_fma_f32 v80, v80, v94, v82
	v_fmac_f32_e32 v83, v75, v95
	s_and_saveexec_b64 s[0:1], s[42:43]
	s_cbranch_execz .LBB0_1258
	v_mul_f32_e32 v75, 0x41800000, v84
	v_mul_f32_e32 v81, 0x41800000, v72
	v_med3_f32 v75, v75, s25, v218
	v_med3_f32 v81, v81, s25, v218
	v_cvt_pk_fp8_f32 v88, v75, v81
	v_mul_f32_e32 v82, 0x41800000, v85
	v_mul_f32_e32 v75, 0x41800000, v87
	v_med3_f32 v81, v82, s25, v218
	v_med3_f32 v75, v75, s25, v218
	v_cvt_pk_fp8_f32 v88, v81, v75 op_sel:[0,0,1]
	v_mul_f32_e32 v75, 0x41800000, v73
	v_mul_f32_e32 v81, 0x41800000, v74
	v_med3_f32 v75, v75, s25, v218
	v_med3_f32 v81, v81, s25, v218
	v_cvt_pk_fp8_f32 v89, v75, v81
	v_mul_f32_e32 v82, 0x41800000, v80
	v_mul_f32_e32 v75, 0x41800000, v83
	v_med3_f32 v81, v82, s25, v218
	v_med3_f32 v75, v75, s25, v218
	v_cvt_pk_fp8_f32 v89, v81, v75 op_sel:[0,0,1]
	global_store_dwordx2 v[144:145], v[88:89], off offset:416
.LBB0_1258:
	s_or_b64 exec, exec, s[0:1]
	v_cvt_pk_bf16_f32 v88, v84, v72
	v_cvt_pk_bf16_f32 v89, v85, v87
	v_cvt_pk_bf16_f32 v90, v73, v74
	v_cvt_pk_bf16_f32 v91, v80, v83
	s_nop 0
	v_and_b32_e32 v81, 0xffff0000, v88
	v_lshlrev_b32_e32 v75, 16, v88
	v_sub_f32_e32 v72, v72, v81
	v_sub_f32_e32 v75, v84, v75
	v_cvt_pk_bf16_f32 v84, v75, v72
	v_lshlrev_b32_e32 v72, 16, v89
	v_sub_f32_e32 v72, v85, v72
	v_and_b32_e32 v75, 0xffff0000, v89
	v_sub_f32_e32 v75, v87, v75
	v_cvt_pk_bf16_f32 v85, v72, v75
	v_lshlrev_b32_e32 v72, 16, v90
	v_sub_f32_e32 v72, v73, v72
	v_and_b32_e32 v73, 0xffff0000, v90
	v_sub_f32_e32 v73, v74, v73
	v_cvt_pk_bf16_f32 v86, v72, v73
	v_lshlrev_b32_e32 v72, 16, v91
	v_and_b32_e32 v73, 0xffff0000, v91
	v_sub_f32_e32 v72, v80, v72
	v_sub_f32_e32 v73, v83, v73
	v_cvt_pk_bf16_f32 v87, v72, v73
	ds_read_b128 v[72:75], v153 offset:1856
	s_waitcnt lgkmcnt(0)
	v_mfma_f32_16x16x32_bf16 v[76:79], v[88:91], v[72:75], v[76:79]
	v_mfma_f32_16x16x32_bf16 v[72:75], v[84:87], v[72:75], v[76:79]
	s_nop 6
	ds_read_b128 v[76:79], v153 offset:34880
	s_waitcnt lgkmcnt(0)
	v_mfma_f32_16x16x32_bf16 v[72:75], v[88:91], v[76:79], v[72:75]
	ds_read_b128 v[80:83], v162 offset:5888
	ds_read_b128 v[84:87], v162 offset:1792
	ds_read_b128 v[88:91], v162 offset:1808
	ds_read_b128 v[76:79], v162 offset:5904
	v_lshlrev_b32_e32 v92, 16, v68
	v_and_b32_e32 v68, 0xffff0000, v68
	v_mul_f32_e32 v68, v112, v68
	s_waitcnt lgkmcnt(2)
	v_fma_f32 v68, v68, v85, v81
	v_lshlrev_b32_e32 v81, 16, v69
	v_and_b32_e32 v69, 0xffff0000, v69
	v_mul_f32_e32 v69, v112, v69
	v_fmac_f32_e32 v83, v69, v87
	v_lshlrev_b32_e32 v69, 16, v70
	v_mul_f32_e32 v69, v112, v69
	s_waitcnt lgkmcnt(0)
	v_fma_f32 v69, v69, v88, v76
	v_and_b32_e32 v70, 0xffff0000, v70
	v_lshlrev_b32_e32 v76, 16, v71
	v_and_b32_e32 v71, 0xffff0000, v71
	v_mul_f32_e32 v92, v112, v92
	v_mul_f32_e32 v81, v112, v81
	v_mul_f32_e32 v70, v112, v70
	v_mul_f32_e32 v76, v112, v76
	v_mul_f32_e32 v71, v112, v71
	v_fma_f32 v80, v92, v84, v80
	v_fma_f32 v81, v81, v86, v82
	v_fma_f32 v70, v70, v89, v77
	v_fma_f32 v76, v76, v90, v78
	v_fmac_f32_e32 v79, v71, v91
	s_and_saveexec_b64 s[0:1], s[42:43]
	s_cbranch_execz .LBB0_1260
	v_mul_f32_e32 v71, 0x41800000, v80
	v_mul_f32_e32 v77, 0x41800000, v68
	v_med3_f32 v71, v71, s25, v218
	v_med3_f32 v77, v77, s25, v218
	v_cvt_pk_fp8_f32 v84, v71, v77
	v_mul_f32_e32 v78, 0x41800000, v81
	v_mul_f32_e32 v71, 0x41800000, v83
	v_med3_f32 v77, v78, s25, v218
	v_med3_f32 v71, v71, s25, v218
	v_cvt_pk_fp8_f32 v84, v77, v71 op_sel:[0,0,1]
	v_mul_f32_e32 v71, 0x41800000, v69
	v_mul_f32_e32 v77, 0x41800000, v70
	v_med3_f32 v71, v71, s25, v218
	v_med3_f32 v77, v77, s25, v218
	v_cvt_pk_fp8_f32 v85, v71, v77
	v_mul_f32_e32 v78, 0x41800000, v76
	v_mul_f32_e32 v71, 0x41800000, v79
	v_med3_f32 v77, v78, s25, v218
	v_med3_f32 v71, v71, s25, v218
	v_cvt_pk_fp8_f32 v85, v77, v71 op_sel:[0,0,1]
	global_store_dwordx2 v[144:145], v[84:85], off offset:448
.LBB0_1260:
	s_or_b64 exec, exec, s[0:1]
	v_cvt_pk_bf16_f32 v84, v80, v68
	v_cvt_pk_bf16_f32 v85, v81, v83
	v_cvt_pk_bf16_f32 v86, v69, v70
	v_cvt_pk_bf16_f32 v87, v76, v79
	v_lshlrev_b32_e32 v88, 16, v64
	v_and_b32_e32 v77, 0xffff0000, v84
	v_lshlrev_b32_e32 v71, 16, v84
	v_sub_f32_e32 v68, v68, v77
	v_sub_f32_e32 v71, v80, v71
	v_cvt_pk_bf16_f32 v80, v71, v68
	v_lshlrev_b32_e32 v68, 16, v85
	v_sub_f32_e32 v68, v81, v68
	v_and_b32_e32 v71, 0xffff0000, v85
	v_sub_f32_e32 v71, v83, v71
	v_cvt_pk_bf16_f32 v81, v68, v71
	v_lshlrev_b32_e32 v68, 16, v86
	v_sub_f32_e32 v68, v69, v68
	v_and_b32_e32 v69, 0xffff0000, v86
	v_sub_f32_e32 v69, v70, v69
	v_cvt_pk_bf16_f32 v82, v68, v69
	v_lshlrev_b32_e32 v68, 16, v87
	v_and_b32_e32 v69, 0xffff0000, v87
	v_sub_f32_e32 v68, v76, v68
	v_sub_f32_e32 v69, v79, v69
	v_cvt_pk_bf16_f32 v83, v68, v69
	ds_read_b128 v[68:71], v153 offset:1920
	v_and_b32_e32 v64, 0xffff0000, v64
	s_waitcnt lgkmcnt(0)
	v_mfma_f32_16x16x32_bf16 v[72:75], v[84:87], v[68:71], v[72:75]
	v_mul_f32_e32 v64, v112, v64
	v_mul_f32_e32 v88, v112, v88
	v_mfma_f32_16x16x32_bf16 v[68:71], v[80:83], v[68:71], v[72:75]
	s_nop 4
	ds_read_b128 v[72:75], v153 offset:34944
	s_waitcnt lgkmcnt(0)
	v_mfma_f32_16x16x32_bf16 v[68:71], v[84:87], v[72:75], v[68:71]
	ds_read_b128 v[76:79], v162 offset:6016
	ds_read_b128 v[80:83], v162 offset:1920
	ds_read_b128 v[72:75], v162 offset:6032
	ds_read_b128 v[84:87], v162 offset:1936
	s_waitcnt lgkmcnt(2)
	v_fma_f32 v64, v64, v81, v77
	v_lshlrev_b32_e32 v77, 16, v65
	v_and_b32_e32 v65, 0xffff0000, v65
	v_mul_f32_e32 v65, v112, v65
	v_fmac_f32_e32 v79, v65, v83
	v_lshlrev_b32_e32 v65, 16, v66
	v_mul_f32_e32 v65, v112, v65
	s_waitcnt lgkmcnt(0)
	v_fma_f32 v65, v65, v84, v72
	v_and_b32_e32 v66, 0xffff0000, v66
	v_lshlrev_b32_e32 v72, 16, v67
	v_and_b32_e32 v67, 0xffff0000, v67
	v_mul_f32_e32 v77, v112, v77
	v_mul_f32_e32 v66, v112, v66
	v_mul_f32_e32 v72, v112, v72
	v_mul_f32_e32 v67, v112, v67
	v_fma_f32 v76, v88, v80, v76
	v_fma_f32 v77, v77, v82, v78
	v_fma_f32 v66, v66, v85, v73
	v_fma_f32 v72, v72, v86, v74
	v_fmac_f32_e32 v75, v67, v87
	s_and_saveexec_b64 s[0:1], s[42:43]
	s_cbranch_execz .LBB0_1262
	v_mul_f32_e32 v67, 0x41800000, v76
	v_mul_f32_e32 v73, 0x41800000, v64
	v_med3_f32 v67, v67, s25, v218
	v_med3_f32 v73, v73, s25, v218
	v_cvt_pk_fp8_f32 v80, v67, v73
	v_mul_f32_e32 v74, 0x41800000, v77
	v_mul_f32_e32 v67, 0x41800000, v79
	v_med3_f32 v73, v74, s25, v218
	v_med3_f32 v67, v67, s25, v218
	v_cvt_pk_fp8_f32 v80, v73, v67 op_sel:[0,0,1]
	v_mul_f32_e32 v67, 0x41800000, v65
	v_mul_f32_e32 v73, 0x41800000, v66
	v_med3_f32 v67, v67, s25, v218
	v_med3_f32 v73, v73, s25, v218
	v_cvt_pk_fp8_f32 v81, v67, v73
	v_mul_f32_e32 v74, 0x41800000, v72
	v_mul_f32_e32 v67, 0x41800000, v75
	v_med3_f32 v73, v74, s25, v218
	v_med3_f32 v67, v67, s25, v218
	v_cvt_pk_fp8_f32 v81, v73, v67 op_sel:[0,0,1]
	global_store_dwordx2 v[144:145], v[80:81], off offset:480
.LBB0_1262:
	s_or_b64 exec, exec, s[0:1]
	v_cvt_pk_bf16_f32 v80, v76, v64
	v_cvt_pk_bf16_f32 v81, v77, v79
	v_cvt_pk_bf16_f32 v82, v65, v66
	v_cvt_pk_bf16_f32 v83, v72, v75
	s_nop 0
	v_and_b32_e32 v73, 0xffff0000, v80
	v_lshlrev_b32_e32 v67, 16, v80
	v_sub_f32_e32 v64, v64, v73
	v_sub_f32_e32 v67, v76, v67
	v_cvt_pk_bf16_f32 v76, v67, v64
	v_lshlrev_b32_e32 v64, 16, v81
	v_sub_f32_e32 v64, v77, v64
	v_and_b32_e32 v67, 0xffff0000, v81
	v_sub_f32_e32 v67, v79, v67
	v_cvt_pk_bf16_f32 v77, v64, v67
	v_lshlrev_b32_e32 v64, 16, v82
	v_sub_f32_e32 v64, v65, v64
	v_and_b32_e32 v65, 0xffff0000, v82
	v_sub_f32_e32 v65, v66, v65
	v_cvt_pk_bf16_f32 v78, v64, v65
	v_lshlrev_b32_e32 v64, 16, v83
	v_and_b32_e32 v65, 0xffff0000, v83
	v_sub_f32_e32 v64, v72, v64
	v_sub_f32_e32 v65, v75, v65
	v_cvt_pk_bf16_f32 v79, v64, v65
	ds_read_b128 v[64:67], v153 offset:1984
	s_waitcnt lgkmcnt(0)
	v_mfma_f32_16x16x32_bf16 v[68:71], v[80:83], v[64:67], v[68:71]
	v_mfma_f32_16x16x32_bf16 v[64:67], v[76:79], v[64:67], v[68:71]
	s_nop 6
	ds_read_b128 v[68:71], v153 offset:35008
	s_waitcnt lgkmcnt(0)
	v_mfma_f32_16x16x32_bf16 v[64:67], v[80:83], v[68:71], v[64:67]
	ds_read_b128 v[72:75], v162 offset:6144
	ds_read_b128 v[76:79], v162 offset:2048
	ds_read_b128 v[80:83], v162 offset:2064
	ds_read_b128 v[68:71], v162 offset:6160
	v_lshlrev_b32_e32 v84, 16, v60
	v_and_b32_e32 v60, 0xffff0000, v60
	v_mul_f32_e32 v60, v112, v60
	s_waitcnt lgkmcnt(2)
	v_fma_f32 v60, v60, v77, v73
	v_lshlrev_b32_e32 v73, 16, v61
	v_and_b32_e32 v61, 0xffff0000, v61
	v_mul_f32_e32 v61, v112, v61
	v_fmac_f32_e32 v75, v61, v79
	v_lshlrev_b32_e32 v61, 16, v62
	v_mul_f32_e32 v61, v112, v61
	s_waitcnt lgkmcnt(0)
	v_fma_f32 v61, v61, v80, v68
	v_and_b32_e32 v62, 0xffff0000, v62
	v_lshlrev_b32_e32 v68, 16, v63
	v_and_b32_e32 v63, 0xffff0000, v63
	v_mul_f32_e32 v84, v112, v84
	v_mul_f32_e32 v73, v112, v73
	v_mul_f32_e32 v62, v112, v62
	v_mul_f32_e32 v68, v112, v68
	v_mul_f32_e32 v63, v112, v63
	v_fma_f32 v72, v84, v76, v72
	v_fma_f32 v73, v73, v78, v74
	v_fma_f32 v62, v62, v81, v69
	v_fma_f32 v68, v68, v82, v70
	v_fmac_f32_e32 v71, v63, v83
	s_and_saveexec_b64 s[0:1], s[42:43]
	s_cbranch_execz .LBB0_1264
	v_mul_f32_e32 v63, 0x41800000, v72
	v_mul_f32_e32 v69, 0x41800000, v60
	v_med3_f32 v63, v63, s25, v218
	v_med3_f32 v69, v69, s25, v218
	v_cvt_pk_fp8_f32 v76, v63, v69
	v_mul_f32_e32 v70, 0x41800000, v73
	v_mul_f32_e32 v63, 0x41800000, v75
	v_med3_f32 v69, v70, s25, v218
	v_med3_f32 v63, v63, s25, v218
	v_cvt_pk_fp8_f32 v76, v69, v63 op_sel:[0,0,1]
	v_mul_f32_e32 v63, 0x41800000, v61
	v_mul_f32_e32 v69, 0x41800000, v62
	v_med3_f32 v63, v63, s25, v218
	v_med3_f32 v69, v69, s25, v218
	v_cvt_pk_fp8_f32 v77, v63, v69
	v_mul_f32_e32 v70, 0x41800000, v68
	v_mul_f32_e32 v63, 0x41800000, v71
	v_med3_f32 v69, v70, s25, v218
	v_med3_f32 v63, v63, s25, v218
	v_cvt_pk_fp8_f32 v77, v69, v63 op_sel:[0,0,1]
	global_store_dwordx2 v[144:145], v[76:77], off offset:512
.LBB0_1264:
	s_or_b64 exec, exec, s[0:1]
	v_cvt_pk_bf16_f32 v76, v72, v60
	v_cvt_pk_bf16_f32 v77, v73, v75
	v_cvt_pk_bf16_f32 v78, v61, v62
	v_cvt_pk_bf16_f32 v79, v68, v71
	v_lshlrev_b32_e32 v80, 16, v56
	v_and_b32_e32 v69, 0xffff0000, v76
	v_lshlrev_b32_e32 v63, 16, v76
	v_sub_f32_e32 v60, v60, v69
	v_sub_f32_e32 v63, v72, v63
	v_cvt_pk_bf16_f32 v72, v63, v60
	v_lshlrev_b32_e32 v60, 16, v77
	v_sub_f32_e32 v60, v73, v60
	v_and_b32_e32 v63, 0xffff0000, v77
	v_sub_f32_e32 v63, v75, v63
	v_cvt_pk_bf16_f32 v73, v60, v63
	v_lshlrev_b32_e32 v60, 16, v78
	v_sub_f32_e32 v60, v61, v60
	v_and_b32_e32 v61, 0xffff0000, v78
	v_sub_f32_e32 v61, v62, v61
	v_cvt_pk_bf16_f32 v74, v60, v61
	v_lshlrev_b32_e32 v60, 16, v79
	v_and_b32_e32 v61, 0xffff0000, v79
	v_sub_f32_e32 v60, v68, v60
	v_sub_f32_e32 v61, v71, v61
	v_cvt_pk_bf16_f32 v75, v60, v61
	ds_read_b128 v[60:63], v153 offset:2048
	v_and_b32_e32 v56, 0xffff0000, v56
	s_waitcnt lgkmcnt(0)
	v_mfma_f32_16x16x32_bf16 v[64:67], v[76:79], v[60:63], v[64:67]
	v_mul_f32_e32 v56, v112, v56
	v_mul_f32_e32 v80, v112, v80
	v_mfma_f32_16x16x32_bf16 v[60:63], v[72:75], v[60:63], v[64:67]
	s_nop 4
	ds_read_b128 v[64:67], v153 offset:35072
	s_waitcnt lgkmcnt(0)
	v_mfma_f32_16x16x32_bf16 v[60:63], v[76:79], v[64:67], v[60:63]
	ds_read_b128 v[68:71], v162 offset:6272
	ds_read_b128 v[72:75], v162 offset:2176
	ds_read_b128 v[64:67], v162 offset:6288
	ds_read_b128 v[76:79], v162 offset:2192
	s_waitcnt lgkmcnt(2)
	v_fma_f32 v56, v56, v73, v69
	v_lshlrev_b32_e32 v69, 16, v57
	v_and_b32_e32 v57, 0xffff0000, v57
	v_mul_f32_e32 v57, v112, v57
	v_fmac_f32_e32 v71, v57, v75
	v_lshlrev_b32_e32 v57, 16, v58
	v_mul_f32_e32 v57, v112, v57
	s_waitcnt lgkmcnt(0)
	v_fma_f32 v57, v57, v76, v64
	v_and_b32_e32 v58, 0xffff0000, v58
	v_lshlrev_b32_e32 v64, 16, v59
	v_and_b32_e32 v59, 0xffff0000, v59
	v_mul_f32_e32 v69, v112, v69
	v_mul_f32_e32 v58, v112, v58
	v_mul_f32_e32 v64, v112, v64
	v_mul_f32_e32 v59, v112, v59
	v_fma_f32 v68, v80, v72, v68
	v_fma_f32 v69, v69, v74, v70
	v_fma_f32 v58, v58, v77, v65
	v_fma_f32 v64, v64, v78, v66
	v_fmac_f32_e32 v67, v59, v79
	s_and_saveexec_b64 s[0:1], s[42:43]
	s_cbranch_execz .LBB0_1266
	v_mul_f32_e32 v59, 0x41800000, v68
	v_mul_f32_e32 v65, 0x41800000, v56
	v_med3_f32 v59, v59, s25, v218
	v_med3_f32 v65, v65, s25, v218
	v_cvt_pk_fp8_f32 v72, v59, v65
	v_mul_f32_e32 v66, 0x41800000, v69
	v_mul_f32_e32 v59, 0x41800000, v71
	v_med3_f32 v65, v66, s25, v218
	v_med3_f32 v59, v59, s25, v218
	v_cvt_pk_fp8_f32 v72, v65, v59 op_sel:[0,0,1]
	v_mul_f32_e32 v59, 0x41800000, v57
	v_mul_f32_e32 v65, 0x41800000, v58
	v_med3_f32 v59, v59, s25, v218
	v_med3_f32 v65, v65, s25, v218
	v_cvt_pk_fp8_f32 v73, v59, v65
	v_mul_f32_e32 v66, 0x41800000, v64
	v_mul_f32_e32 v59, 0x41800000, v67
	v_med3_f32 v65, v66, s25, v218
	v_med3_f32 v59, v59, s25, v218
	v_cvt_pk_fp8_f32 v73, v65, v59 op_sel:[0,0,1]
	global_store_dwordx2 v[144:145], v[72:73], off offset:544
.LBB0_1266:
	s_or_b64 exec, exec, s[0:1]
	v_cvt_pk_bf16_f32 v72, v68, v56
	v_cvt_pk_bf16_f32 v73, v69, v71
	v_cvt_pk_bf16_f32 v74, v57, v58
	v_cvt_pk_bf16_f32 v75, v64, v67
	s_nop 0
	v_and_b32_e32 v65, 0xffff0000, v72
	v_lshlrev_b32_e32 v59, 16, v72
	v_sub_f32_e32 v56, v56, v65
	v_sub_f32_e32 v59, v68, v59
	v_cvt_pk_bf16_f32 v68, v59, v56
	v_lshlrev_b32_e32 v56, 16, v73
	v_sub_f32_e32 v56, v69, v56
	v_and_b32_e32 v59, 0xffff0000, v73
	v_sub_f32_e32 v59, v71, v59
	v_cvt_pk_bf16_f32 v69, v56, v59
	v_lshlrev_b32_e32 v56, 16, v74
	v_sub_f32_e32 v56, v57, v56
	v_and_b32_e32 v57, 0xffff0000, v74
	v_sub_f32_e32 v57, v58, v57
	v_cvt_pk_bf16_f32 v70, v56, v57
	v_lshlrev_b32_e32 v56, 16, v75
	v_and_b32_e32 v57, 0xffff0000, v75
	v_sub_f32_e32 v56, v64, v56
	v_sub_f32_e32 v57, v67, v57
	v_cvt_pk_bf16_f32 v71, v56, v57
	ds_read_b128 v[56:59], v153 offset:2112
	s_waitcnt lgkmcnt(0)
	v_mfma_f32_16x16x32_bf16 v[60:63], v[72:75], v[56:59], v[60:63]
	v_mfma_f32_16x16x32_bf16 v[56:59], v[68:71], v[56:59], v[60:63]
	s_nop 6
	ds_read_b128 v[60:63], v153 offset:35136
	s_waitcnt lgkmcnt(0)
	v_mfma_f32_16x16x32_bf16 v[56:59], v[72:75], v[60:63], v[56:59]
	ds_read_b128 v[64:67], v162 offset:6400
	ds_read_b128 v[68:71], v162 offset:2304
	ds_read_b128 v[72:75], v162 offset:2320
	ds_read_b128 v[60:63], v162 offset:6416
	v_lshlrev_b32_e32 v76, 16, v52
	v_and_b32_e32 v52, 0xffff0000, v52
	v_mul_f32_e32 v52, v112, v52
	s_waitcnt lgkmcnt(2)
	v_fma_f32 v52, v52, v69, v65
	v_lshlrev_b32_e32 v65, 16, v53
	v_and_b32_e32 v53, 0xffff0000, v53
	v_mul_f32_e32 v53, v112, v53
	v_fmac_f32_e32 v67, v53, v71
	v_lshlrev_b32_e32 v53, 16, v54
	v_mul_f32_e32 v53, v112, v53
	s_waitcnt lgkmcnt(0)
	v_fma_f32 v53, v53, v72, v60
	v_and_b32_e32 v54, 0xffff0000, v54
	v_lshlrev_b32_e32 v60, 16, v55
	v_and_b32_e32 v55, 0xffff0000, v55
	v_mul_f32_e32 v76, v112, v76
	v_mul_f32_e32 v65, v112, v65
	v_mul_f32_e32 v54, v112, v54
	v_mul_f32_e32 v60, v112, v60
	v_mul_f32_e32 v55, v112, v55
	v_fma_f32 v64, v76, v68, v64
	v_fma_f32 v65, v65, v70, v66
	v_fma_f32 v54, v54, v73, v61
	v_fma_f32 v60, v60, v74, v62
	v_fmac_f32_e32 v63, v55, v75
	s_and_saveexec_b64 s[0:1], s[42:43]
	s_cbranch_execz .LBB0_1268
	v_mul_f32_e32 v55, 0x41800000, v64
	v_mul_f32_e32 v61, 0x41800000, v52
	v_med3_f32 v55, v55, s25, v218
	v_med3_f32 v61, v61, s25, v218
	v_cvt_pk_fp8_f32 v68, v55, v61
	v_mul_f32_e32 v62, 0x41800000, v65
	v_mul_f32_e32 v55, 0x41800000, v67
	v_med3_f32 v61, v62, s25, v218
	v_med3_f32 v55, v55, s25, v218
	v_cvt_pk_fp8_f32 v68, v61, v55 op_sel:[0,0,1]
	v_mul_f32_e32 v55, 0x41800000, v53
	v_mul_f32_e32 v61, 0x41800000, v54
	v_med3_f32 v55, v55, s25, v218
	v_med3_f32 v61, v61, s25, v218
	v_cvt_pk_fp8_f32 v69, v55, v61
	v_mul_f32_e32 v62, 0x41800000, v60
	v_mul_f32_e32 v55, 0x41800000, v63
	v_med3_f32 v61, v62, s25, v218
	v_med3_f32 v55, v55, s25, v218
	v_cvt_pk_fp8_f32 v69, v61, v55 op_sel:[0,0,1]
	global_store_dwordx2 v[144:145], v[68:69], off offset:576
.LBB0_1268:
	s_or_b64 exec, exec, s[0:1]
	v_cvt_pk_bf16_f32 v68, v64, v52
	v_cvt_pk_bf16_f32 v69, v65, v67
	v_cvt_pk_bf16_f32 v70, v53, v54
	v_cvt_pk_bf16_f32 v71, v60, v63
	v_lshlrev_b32_e32 v72, 16, v48
	v_and_b32_e32 v61, 0xffff0000, v68
	v_lshlrev_b32_e32 v55, 16, v68
	v_sub_f32_e32 v52, v52, v61
	v_sub_f32_e32 v55, v64, v55
	v_cvt_pk_bf16_f32 v64, v55, v52
	v_lshlrev_b32_e32 v52, 16, v69
	v_sub_f32_e32 v52, v65, v52
	v_and_b32_e32 v55, 0xffff0000, v69
	v_sub_f32_e32 v55, v67, v55
	v_cvt_pk_bf16_f32 v65, v52, v55
	v_lshlrev_b32_e32 v52, 16, v70
	v_sub_f32_e32 v52, v53, v52
	v_and_b32_e32 v53, 0xffff0000, v70
	v_sub_f32_e32 v53, v54, v53
	v_cvt_pk_bf16_f32 v66, v52, v53
	v_lshlrev_b32_e32 v52, 16, v71
	v_and_b32_e32 v53, 0xffff0000, v71
	v_sub_f32_e32 v52, v60, v52
	v_sub_f32_e32 v53, v63, v53
	v_cvt_pk_bf16_f32 v67, v52, v53
	ds_read_b128 v[52:55], v153 offset:2176
	v_and_b32_e32 v48, 0xffff0000, v48
	s_waitcnt lgkmcnt(0)
	v_mfma_f32_16x16x32_bf16 v[56:59], v[68:71], v[52:55], v[56:59]
	v_mul_f32_e32 v48, v112, v48
	v_mul_f32_e32 v72, v112, v72
	v_mfma_f32_16x16x32_bf16 v[52:55], v[64:67], v[52:55], v[56:59]
	s_nop 4
	ds_read_b128 v[56:59], v153 offset:35200
	s_waitcnt lgkmcnt(0)
	v_mfma_f32_16x16x32_bf16 v[52:55], v[68:71], v[56:59], v[52:55]
	ds_read_b128 v[60:63], v162 offset:6528
	ds_read_b128 v[64:67], v162 offset:2432
	ds_read_b128 v[56:59], v162 offset:6544
	ds_read_b128 v[68:71], v162 offset:2448
	s_waitcnt lgkmcnt(2)
	v_fma_f32 v48, v48, v65, v61
	v_lshlrev_b32_e32 v61, 16, v49
	v_and_b32_e32 v49, 0xffff0000, v49
	v_mul_f32_e32 v49, v112, v49
	v_fmac_f32_e32 v63, v49, v67
	v_lshlrev_b32_e32 v49, 16, v50
	v_mul_f32_e32 v49, v112, v49
	s_waitcnt lgkmcnt(0)
	v_fma_f32 v49, v49, v68, v56
	v_and_b32_e32 v50, 0xffff0000, v50
	v_lshlrev_b32_e32 v56, 16, v51
	v_and_b32_e32 v51, 0xffff0000, v51
	v_mul_f32_e32 v61, v112, v61
	v_mul_f32_e32 v50, v112, v50
	v_mul_f32_e32 v56, v112, v56
	v_mul_f32_e32 v51, v112, v51
	v_fma_f32 v60, v72, v64, v60
	v_fma_f32 v61, v61, v66, v62
	v_fma_f32 v50, v50, v69, v57
	v_fma_f32 v56, v56, v70, v58
	v_fmac_f32_e32 v59, v51, v71
	s_and_saveexec_b64 s[0:1], s[42:43]
	s_cbranch_execz .LBB0_1270
	v_mul_f32_e32 v51, 0x41800000, v60
	v_mul_f32_e32 v57, 0x41800000, v48
	v_med3_f32 v51, v51, s25, v218
	v_med3_f32 v57, v57, s25, v218
	v_cvt_pk_fp8_f32 v64, v51, v57
	v_mul_f32_e32 v58, 0x41800000, v61
	v_mul_f32_e32 v51, 0x41800000, v63
	v_med3_f32 v57, v58, s25, v218
	v_med3_f32 v51, v51, s25, v218
	v_cvt_pk_fp8_f32 v64, v57, v51 op_sel:[0,0,1]
	v_mul_f32_e32 v51, 0x41800000, v49
	v_mul_f32_e32 v57, 0x41800000, v50
	v_med3_f32 v51, v51, s25, v218
	v_med3_f32 v57, v57, s25, v218
	v_cvt_pk_fp8_f32 v65, v51, v57
	v_mul_f32_e32 v58, 0x41800000, v56
	v_mul_f32_e32 v51, 0x41800000, v59
	v_med3_f32 v57, v58, s25, v218
	v_med3_f32 v51, v51, s25, v218
	v_cvt_pk_fp8_f32 v65, v57, v51 op_sel:[0,0,1]
	global_store_dwordx2 v[144:145], v[64:65], off offset:608
.LBB0_1270:
	s_or_b64 exec, exec, s[0:1]
	v_cvt_pk_bf16_f32 v64, v60, v48
	v_cvt_pk_bf16_f32 v65, v61, v63
	v_cvt_pk_bf16_f32 v66, v49, v50
	v_cvt_pk_bf16_f32 v67, v56, v59
	s_nop 0
	v_and_b32_e32 v57, 0xffff0000, v64
	v_lshlrev_b32_e32 v51, 16, v64
	v_sub_f32_e32 v48, v48, v57
	v_sub_f32_e32 v51, v60, v51
	v_cvt_pk_bf16_f32 v60, v51, v48
	v_lshlrev_b32_e32 v48, 16, v65
	v_sub_f32_e32 v48, v61, v48
	v_and_b32_e32 v51, 0xffff0000, v65
	v_sub_f32_e32 v51, v63, v51
	v_cvt_pk_bf16_f32 v61, v48, v51
	v_lshlrev_b32_e32 v48, 16, v66
	v_sub_f32_e32 v48, v49, v48
	v_and_b32_e32 v49, 0xffff0000, v66
	v_sub_f32_e32 v49, v50, v49
	v_cvt_pk_bf16_f32 v62, v48, v49
	v_lshlrev_b32_e32 v48, 16, v67
	v_and_b32_e32 v49, 0xffff0000, v67
	v_sub_f32_e32 v48, v56, v48
	v_sub_f32_e32 v49, v59, v49
	v_cvt_pk_bf16_f32 v63, v48, v49
	ds_read_b128 v[48:51], v153 offset:2240
	s_waitcnt lgkmcnt(0)
	v_mfma_f32_16x16x32_bf16 v[52:55], v[64:67], v[48:51], v[52:55]
	v_mfma_f32_16x16x32_bf16 v[48:51], v[60:63], v[48:51], v[52:55]
	s_nop 6
	ds_read_b128 v[52:55], v153 offset:35264
	s_waitcnt lgkmcnt(0)
	v_mfma_f32_16x16x32_bf16 v[48:51], v[64:67], v[52:55], v[48:51]
	ds_read_b128 v[56:59], v162 offset:6656
	ds_read_b128 v[60:63], v162 offset:2560
	ds_read_b128 v[64:67], v162 offset:2576
	ds_read_b128 v[52:55], v162 offset:6672
	v_lshlrev_b32_e32 v68, 16, v44
	v_and_b32_e32 v44, 0xffff0000, v44
	v_mul_f32_e32 v44, v112, v44
	s_waitcnt lgkmcnt(2)
	v_fma_f32 v44, v44, v61, v57
	v_lshlrev_b32_e32 v57, 16, v45
	v_and_b32_e32 v45, 0xffff0000, v45
	v_mul_f32_e32 v45, v112, v45
	v_fmac_f32_e32 v59, v45, v63
	v_lshlrev_b32_e32 v45, 16, v46
	v_mul_f32_e32 v45, v112, v45
	s_waitcnt lgkmcnt(0)
	v_fma_f32 v45, v45, v64, v52
	v_and_b32_e32 v46, 0xffff0000, v46
	v_lshlrev_b32_e32 v52, 16, v47
	v_and_b32_e32 v47, 0xffff0000, v47
	v_mul_f32_e32 v68, v112, v68
	v_mul_f32_e32 v57, v112, v57
	v_mul_f32_e32 v46, v112, v46
	v_mul_f32_e32 v52, v112, v52
	v_mul_f32_e32 v47, v112, v47
	v_fma_f32 v56, v68, v60, v56
	v_fma_f32 v57, v57, v62, v58
	v_fma_f32 v46, v46, v65, v53
	v_fma_f32 v52, v52, v66, v54
	v_fmac_f32_e32 v55, v47, v67
	s_and_saveexec_b64 s[0:1], s[42:43]
	s_cbranch_execz .LBB0_1272
	v_mul_f32_e32 v47, 0x41800000, v56
	v_mul_f32_e32 v53, 0x41800000, v44
	v_med3_f32 v47, v47, s25, v218
	v_med3_f32 v53, v53, s25, v218
	v_cvt_pk_fp8_f32 v60, v47, v53
	v_mul_f32_e32 v54, 0x41800000, v57
	v_mul_f32_e32 v47, 0x41800000, v59
	v_med3_f32 v53, v54, s25, v218
	v_med3_f32 v47, v47, s25, v218
	v_cvt_pk_fp8_f32 v60, v53, v47 op_sel:[0,0,1]
	v_mul_f32_e32 v47, 0x41800000, v45
	v_mul_f32_e32 v53, 0x41800000, v46
	v_med3_f32 v47, v47, s25, v218
	v_med3_f32 v53, v53, s25, v218
	v_cvt_pk_fp8_f32 v61, v47, v53
	v_mul_f32_e32 v54, 0x41800000, v52
	v_mul_f32_e32 v47, 0x41800000, v55
	v_med3_f32 v53, v54, s25, v218
	v_med3_f32 v47, v47, s25, v218
	v_cvt_pk_fp8_f32 v61, v53, v47 op_sel:[0,0,1]
	global_store_dwordx2 v[144:145], v[60:61], off offset:640
.LBB0_1272:
	s_or_b64 exec, exec, s[0:1]
	v_cvt_pk_bf16_f32 v60, v56, v44
	v_cvt_pk_bf16_f32 v61, v57, v59
	v_cvt_pk_bf16_f32 v62, v45, v46
	v_cvt_pk_bf16_f32 v63, v52, v55
	v_lshlrev_b32_e32 v64, 16, v40
	v_and_b32_e32 v53, 0xffff0000, v60
	v_lshlrev_b32_e32 v47, 16, v60
	v_sub_f32_e32 v44, v44, v53
	v_sub_f32_e32 v47, v56, v47
	v_cvt_pk_bf16_f32 v56, v47, v44
	v_lshlrev_b32_e32 v44, 16, v61
	v_sub_f32_e32 v44, v57, v44
	v_and_b32_e32 v47, 0xffff0000, v61
	v_sub_f32_e32 v47, v59, v47
	v_cvt_pk_bf16_f32 v57, v44, v47
	v_lshlrev_b32_e32 v44, 16, v62
	v_sub_f32_e32 v44, v45, v44
	v_and_b32_e32 v45, 0xffff0000, v62
	v_sub_f32_e32 v45, v46, v45
	v_cvt_pk_bf16_f32 v58, v44, v45
	v_lshlrev_b32_e32 v44, 16, v63
	v_and_b32_e32 v45, 0xffff0000, v63
	v_sub_f32_e32 v44, v52, v44
	v_sub_f32_e32 v45, v55, v45
	v_cvt_pk_bf16_f32 v59, v44, v45
	ds_read_b128 v[44:47], v153 offset:2304
	v_and_b32_e32 v40, 0xffff0000, v40
	s_waitcnt lgkmcnt(0)
	v_mfma_f32_16x16x32_bf16 v[48:51], v[60:63], v[44:47], v[48:51]
	v_mul_f32_e32 v40, v112, v40
	v_mul_f32_e32 v64, v112, v64
	v_mfma_f32_16x16x32_bf16 v[44:47], v[56:59], v[44:47], v[48:51]
	s_nop 4
	ds_read_b128 v[48:51], v153 offset:35328
	s_waitcnt lgkmcnt(0)
	v_mfma_f32_16x16x32_bf16 v[44:47], v[60:63], v[48:51], v[44:47]
	ds_read_b128 v[52:55], v162 offset:6784
	ds_read_b128 v[56:59], v162 offset:2688
	ds_read_b128 v[48:51], v162 offset:6800
	ds_read_b128 v[60:63], v162 offset:2704
	s_waitcnt lgkmcnt(2)
	v_fma_f32 v40, v40, v57, v53
	v_lshlrev_b32_e32 v53, 16, v41
	v_and_b32_e32 v41, 0xffff0000, v41
	v_mul_f32_e32 v41, v112, v41
	v_fmac_f32_e32 v55, v41, v59
	v_lshlrev_b32_e32 v41, 16, v42
	v_mul_f32_e32 v41, v112, v41
	s_waitcnt lgkmcnt(0)
	v_fma_f32 v41, v41, v60, v48
	v_and_b32_e32 v42, 0xffff0000, v42
	v_lshlrev_b32_e32 v48, 16, v43
	v_and_b32_e32 v43, 0xffff0000, v43
	v_mul_f32_e32 v53, v112, v53
	v_mul_f32_e32 v42, v112, v42
	v_mul_f32_e32 v48, v112, v48
	v_mul_f32_e32 v43, v112, v43
	v_fma_f32 v52, v64, v56, v52
	v_fma_f32 v53, v53, v58, v54
	v_fma_f32 v42, v42, v61, v49
	v_fma_f32 v48, v48, v62, v50
	v_fmac_f32_e32 v51, v43, v63
	s_and_saveexec_b64 s[0:1], s[42:43]
	s_cbranch_execz .LBB0_1274
	v_mul_f32_e32 v43, 0x41800000, v52
	v_mul_f32_e32 v49, 0x41800000, v40
	v_med3_f32 v43, v43, s25, v218
	v_med3_f32 v49, v49, s25, v218
	v_cvt_pk_fp8_f32 v56, v43, v49
	v_mul_f32_e32 v50, 0x41800000, v53
	v_mul_f32_e32 v43, 0x41800000, v55
	v_med3_f32 v49, v50, s25, v218
	v_med3_f32 v43, v43, s25, v218
	v_cvt_pk_fp8_f32 v56, v49, v43 op_sel:[0,0,1]
	v_mul_f32_e32 v43, 0x41800000, v41
	v_mul_f32_e32 v49, 0x41800000, v42
	v_med3_f32 v43, v43, s25, v218
	v_med3_f32 v49, v49, s25, v218
	v_cvt_pk_fp8_f32 v57, v43, v49
	v_mul_f32_e32 v50, 0x41800000, v48
	v_mul_f32_e32 v43, 0x41800000, v51
	v_med3_f32 v49, v50, s25, v218
	v_med3_f32 v43, v43, s25, v218
	v_cvt_pk_fp8_f32 v57, v49, v43 op_sel:[0,0,1]
	global_store_dwordx2 v[144:145], v[56:57], off offset:672
.LBB0_1274:
	s_or_b64 exec, exec, s[0:1]
	v_cvt_pk_bf16_f32 v56, v52, v40
	v_cvt_pk_bf16_f32 v57, v53, v55
	v_cvt_pk_bf16_f32 v58, v41, v42
	v_cvt_pk_bf16_f32 v59, v48, v51
	s_nop 0
	v_and_b32_e32 v49, 0xffff0000, v56
	v_lshlrev_b32_e32 v43, 16, v56
	v_sub_f32_e32 v40, v40, v49
	v_sub_f32_e32 v43, v52, v43
	v_cvt_pk_bf16_f32 v52, v43, v40
	v_lshlrev_b32_e32 v40, 16, v57
	v_sub_f32_e32 v40, v53, v40
	v_and_b32_e32 v43, 0xffff0000, v57
	v_sub_f32_e32 v43, v55, v43
	v_cvt_pk_bf16_f32 v53, v40, v43
	v_lshlrev_b32_e32 v40, 16, v58
	v_sub_f32_e32 v40, v41, v40
	v_and_b32_e32 v41, 0xffff0000, v58
	v_sub_f32_e32 v41, v42, v41
	v_cvt_pk_bf16_f32 v54, v40, v41
	v_lshlrev_b32_e32 v40, 16, v59
	v_and_b32_e32 v41, 0xffff0000, v59
	v_sub_f32_e32 v40, v48, v40
	v_sub_f32_e32 v41, v51, v41
	v_cvt_pk_bf16_f32 v55, v40, v41
	ds_read_b128 v[40:43], v153 offset:2368
	s_waitcnt lgkmcnt(0)
	v_mfma_f32_16x16x32_bf16 v[44:47], v[56:59], v[40:43], v[44:47]
	v_mfma_f32_16x16x32_bf16 v[40:43], v[52:55], v[40:43], v[44:47]
	s_nop 6
	ds_read_b128 v[44:47], v153 offset:35392
	s_waitcnt lgkmcnt(0)
	v_mfma_f32_16x16x32_bf16 v[40:43], v[56:59], v[44:47], v[40:43]
	ds_read_b128 v[48:51], v162 offset:6912
	ds_read_b128 v[52:55], v162 offset:2816
	ds_read_b128 v[56:59], v162 offset:2832
	ds_read_b128 v[44:47], v162 offset:6928
	v_lshlrev_b32_e32 v60, 16, v36
	v_and_b32_e32 v36, 0xffff0000, v36
	v_mul_f32_e32 v36, v112, v36
	s_waitcnt lgkmcnt(2)
	v_fma_f32 v36, v36, v53, v49
	v_lshlrev_b32_e32 v49, 16, v37
	v_and_b32_e32 v37, 0xffff0000, v37
	v_mul_f32_e32 v37, v112, v37
	v_fmac_f32_e32 v51, v37, v55
	v_lshlrev_b32_e32 v37, 16, v38
	v_mul_f32_e32 v37, v112, v37
	s_waitcnt lgkmcnt(0)
	v_fma_f32 v37, v37, v56, v44
	v_and_b32_e32 v38, 0xffff0000, v38
	v_lshlrev_b32_e32 v44, 16, v39
	v_and_b32_e32 v39, 0xffff0000, v39
	v_mul_f32_e32 v60, v112, v60
	v_mul_f32_e32 v49, v112, v49
	v_mul_f32_e32 v38, v112, v38
	v_mul_f32_e32 v44, v112, v44
	v_mul_f32_e32 v39, v112, v39
	v_fma_f32 v48, v60, v52, v48
	v_fma_f32 v49, v49, v54, v50
	v_fma_f32 v38, v38, v57, v45
	v_fma_f32 v44, v44, v58, v46
	v_fmac_f32_e32 v47, v39, v59
	s_and_saveexec_b64 s[0:1], s[42:43]
	s_cbranch_execz .LBB0_1276
	v_mul_f32_e32 v39, 0x41800000, v48
	v_mul_f32_e32 v45, 0x41800000, v36
	v_med3_f32 v39, v39, s25, v218
	v_med3_f32 v45, v45, s25, v218
	v_cvt_pk_fp8_f32 v52, v39, v45
	v_mul_f32_e32 v46, 0x41800000, v49
	v_mul_f32_e32 v39, 0x41800000, v51
	v_med3_f32 v45, v46, s25, v218
	v_med3_f32 v39, v39, s25, v218
	v_cvt_pk_fp8_f32 v52, v45, v39 op_sel:[0,0,1]
	v_mul_f32_e32 v39, 0x41800000, v37
	v_mul_f32_e32 v45, 0x41800000, v38
	v_med3_f32 v39, v39, s25, v218
	v_med3_f32 v45, v45, s25, v218
	v_cvt_pk_fp8_f32 v53, v39, v45
	v_mul_f32_e32 v46, 0x41800000, v44
	v_mul_f32_e32 v39, 0x41800000, v47
	v_med3_f32 v45, v46, s25, v218
	v_med3_f32 v39, v39, s25, v218
	v_cvt_pk_fp8_f32 v53, v45, v39 op_sel:[0,0,1]
	global_store_dwordx2 v[144:145], v[52:53], off offset:704
.LBB0_1276:
	s_or_b64 exec, exec, s[0:1]
	v_cvt_pk_bf16_f32 v52, v48, v36
	v_cvt_pk_bf16_f32 v53, v49, v51
	v_cvt_pk_bf16_f32 v54, v37, v38
	v_cvt_pk_bf16_f32 v55, v44, v47
	v_lshlrev_b32_e32 v56, 16, v32
	v_and_b32_e32 v45, 0xffff0000, v52
	v_lshlrev_b32_e32 v39, 16, v52
	v_sub_f32_e32 v36, v36, v45
	v_sub_f32_e32 v39, v48, v39
	v_cvt_pk_bf16_f32 v48, v39, v36
	v_lshlrev_b32_e32 v36, 16, v53
	v_sub_f32_e32 v36, v49, v36
	v_and_b32_e32 v39, 0xffff0000, v53
	v_sub_f32_e32 v39, v51, v39
	v_cvt_pk_bf16_f32 v49, v36, v39
	v_lshlrev_b32_e32 v36, 16, v54
	v_sub_f32_e32 v36, v37, v36
	v_and_b32_e32 v37, 0xffff0000, v54
	v_sub_f32_e32 v37, v38, v37
	v_cvt_pk_bf16_f32 v50, v36, v37
	v_lshlrev_b32_e32 v36, 16, v55
	v_and_b32_e32 v37, 0xffff0000, v55
	v_sub_f32_e32 v36, v44, v36
	v_sub_f32_e32 v37, v47, v37
	v_cvt_pk_bf16_f32 v51, v36, v37
	ds_read_b128 v[36:39], v153 offset:2432
	v_and_b32_e32 v32, 0xffff0000, v32
	s_waitcnt lgkmcnt(0)
	v_mfma_f32_16x16x32_bf16 v[40:43], v[52:55], v[36:39], v[40:43]
	v_mul_f32_e32 v32, v112, v32
	v_mul_f32_e32 v56, v112, v56
	v_mfma_f32_16x16x32_bf16 v[36:39], v[48:51], v[36:39], v[40:43]
	s_nop 4
	ds_read_b128 v[40:43], v153 offset:35456
	s_waitcnt lgkmcnt(0)
	v_mfma_f32_16x16x32_bf16 v[36:39], v[52:55], v[40:43], v[36:39]
	ds_read_b128 v[44:47], v162 offset:7040
	ds_read_b128 v[48:51], v162 offset:2944
	ds_read_b128 v[40:43], v162 offset:7056
	ds_read_b128 v[52:55], v162 offset:2960
	s_waitcnt lgkmcnt(2)
	v_fma_f32 v32, v32, v49, v45
	v_lshlrev_b32_e32 v45, 16, v33
	v_and_b32_e32 v33, 0xffff0000, v33
	v_mul_f32_e32 v33, v112, v33
	v_fmac_f32_e32 v47, v33, v51
	v_lshlrev_b32_e32 v33, 16, v34
	v_mul_f32_e32 v33, v112, v33
	s_waitcnt lgkmcnt(0)
	v_fma_f32 v33, v33, v52, v40
	v_and_b32_e32 v34, 0xffff0000, v34
	v_lshlrev_b32_e32 v40, 16, v35
	v_and_b32_e32 v35, 0xffff0000, v35
	v_mul_f32_e32 v45, v112, v45
	v_mul_f32_e32 v34, v112, v34
	v_mul_f32_e32 v40, v112, v40
	v_mul_f32_e32 v35, v112, v35
	v_fma_f32 v44, v56, v48, v44
	v_fma_f32 v45, v45, v50, v46
	v_fma_f32 v34, v34, v53, v41
	v_fma_f32 v40, v40, v54, v42
	v_fmac_f32_e32 v43, v35, v55
	s_and_saveexec_b64 s[0:1], s[42:43]
	s_cbranch_execz .LBB0_1278
	v_mul_f32_e32 v35, 0x41800000, v44
	v_mul_f32_e32 v41, 0x41800000, v32
	v_med3_f32 v35, v35, s25, v218
	v_med3_f32 v41, v41, s25, v218
	v_cvt_pk_fp8_f32 v48, v35, v41
	v_mul_f32_e32 v42, 0x41800000, v45
	v_mul_f32_e32 v35, 0x41800000, v47
	v_med3_f32 v41, v42, s25, v218
	v_med3_f32 v35, v35, s25, v218
	v_cvt_pk_fp8_f32 v48, v41, v35 op_sel:[0,0,1]
	v_mul_f32_e32 v35, 0x41800000, v33
	v_mul_f32_e32 v41, 0x41800000, v34
	v_med3_f32 v35, v35, s25, v218
	v_med3_f32 v41, v41, s25, v218
	v_cvt_pk_fp8_f32 v49, v35, v41
	v_mul_f32_e32 v42, 0x41800000, v40
	v_mul_f32_e32 v35, 0x41800000, v43
	v_med3_f32 v41, v42, s25, v218
	v_med3_f32 v35, v35, s25, v218
	v_cvt_pk_fp8_f32 v49, v41, v35 op_sel:[0,0,1]
	global_store_dwordx2 v[144:145], v[48:49], off offset:736
.LBB0_1278:
	s_or_b64 exec, exec, s[0:1]
	v_cvt_pk_bf16_f32 v48, v44, v32
	v_cvt_pk_bf16_f32 v49, v45, v47
	v_cvt_pk_bf16_f32 v50, v33, v34
	v_cvt_pk_bf16_f32 v51, v40, v43
	s_nop 0
	v_and_b32_e32 v41, 0xffff0000, v48
	v_lshlrev_b32_e32 v35, 16, v48
	v_sub_f32_e32 v32, v32, v41
	v_sub_f32_e32 v35, v44, v35
	v_cvt_pk_bf16_f32 v44, v35, v32
	v_lshlrev_b32_e32 v32, 16, v49
	v_sub_f32_e32 v32, v45, v32
	v_and_b32_e32 v35, 0xffff0000, v49
	v_sub_f32_e32 v35, v47, v35
	v_cvt_pk_bf16_f32 v45, v32, v35
	v_lshlrev_b32_e32 v32, 16, v50
	v_sub_f32_e32 v32, v33, v32
	v_and_b32_e32 v33, 0xffff0000, v50
	v_sub_f32_e32 v33, v34, v33
	v_cvt_pk_bf16_f32 v46, v32, v33
	v_lshlrev_b32_e32 v32, 16, v51
	v_and_b32_e32 v33, 0xffff0000, v51
	v_sub_f32_e32 v32, v40, v32
	v_sub_f32_e32 v33, v43, v33
	v_cvt_pk_bf16_f32 v47, v32, v33
	ds_read_b128 v[32:35], v153 offset:2496
	s_waitcnt lgkmcnt(0)
	v_mfma_f32_16x16x32_bf16 v[36:39], v[48:51], v[32:35], v[36:39]
	v_mfma_f32_16x16x32_bf16 v[32:35], v[44:47], v[32:35], v[36:39]
	s_nop 6
	ds_read_b128 v[36:39], v153 offset:35520
	s_waitcnt lgkmcnt(0)
	v_mfma_f32_16x16x32_bf16 v[32:35], v[48:51], v[36:39], v[32:35]
	ds_read_b128 v[40:43], v162 offset:7168
	ds_read_b128 v[44:47], v162 offset:3072
	ds_read_b128 v[48:51], v162 offset:3088
	ds_read_b128 v[36:39], v162 offset:7184
	v_lshlrev_b32_e32 v52, 16, v28
	v_and_b32_e32 v28, 0xffff0000, v28
	v_mul_f32_e32 v28, v112, v28
	s_waitcnt lgkmcnt(2)
	v_fma_f32 v28, v28, v45, v41
	v_lshlrev_b32_e32 v41, 16, v29
	v_and_b32_e32 v29, 0xffff0000, v29
	v_mul_f32_e32 v29, v112, v29
	v_fmac_f32_e32 v43, v29, v47
	v_lshlrev_b32_e32 v29, 16, v30
	v_mul_f32_e32 v29, v112, v29
	s_waitcnt lgkmcnt(0)
	v_fma_f32 v29, v29, v48, v36
	v_and_b32_e32 v30, 0xffff0000, v30
	v_lshlrev_b32_e32 v36, 16, v31
	v_and_b32_e32 v31, 0xffff0000, v31
	v_mul_f32_e32 v52, v112, v52
	v_mul_f32_e32 v41, v112, v41
	v_mul_f32_e32 v30, v112, v30
	v_mul_f32_e32 v36, v112, v36
	v_mul_f32_e32 v31, v112, v31
	v_fma_f32 v40, v52, v44, v40
	v_fma_f32 v41, v41, v46, v42
	v_fma_f32 v30, v30, v49, v37
	v_fma_f32 v36, v36, v50, v38
	v_fmac_f32_e32 v39, v31, v51
	s_and_saveexec_b64 s[0:1], s[42:43]
	s_cbranch_execz .LBB0_1280
	v_mul_f32_e32 v31, 0x41800000, v40
	v_mul_f32_e32 v37, 0x41800000, v28
	v_med3_f32 v31, v31, s25, v218
	v_med3_f32 v37, v37, s25, v218
	v_cvt_pk_fp8_f32 v44, v31, v37
	v_mul_f32_e32 v38, 0x41800000, v41
	v_mul_f32_e32 v31, 0x41800000, v43
	v_med3_f32 v37, v38, s25, v218
	v_med3_f32 v31, v31, s25, v218
	v_cvt_pk_fp8_f32 v44, v37, v31 op_sel:[0,0,1]
	v_mul_f32_e32 v31, 0x41800000, v29
	v_mul_f32_e32 v37, 0x41800000, v30
	v_med3_f32 v31, v31, s25, v218
	v_med3_f32 v37, v37, s25, v218
	v_cvt_pk_fp8_f32 v45, v31, v37
	v_mul_f32_e32 v38, 0x41800000, v36
	v_mul_f32_e32 v31, 0x41800000, v39
	v_med3_f32 v37, v38, s25, v218
	v_med3_f32 v31, v31, s25, v218
	v_cvt_pk_fp8_f32 v45, v37, v31 op_sel:[0,0,1]
	global_store_dwordx2 v[144:145], v[44:45], off offset:768
.LBB0_1280:
	s_or_b64 exec, exec, s[0:1]
	v_cvt_pk_bf16_f32 v44, v40, v28
	v_cvt_pk_bf16_f32 v45, v41, v43
	v_cvt_pk_bf16_f32 v46, v29, v30
	v_cvt_pk_bf16_f32 v47, v36, v39
	v_lshlrev_b32_e32 v48, 16, v24
	v_and_b32_e32 v37, 0xffff0000, v44
	v_lshlrev_b32_e32 v31, 16, v44
	v_sub_f32_e32 v28, v28, v37
	v_sub_f32_e32 v31, v40, v31
	v_cvt_pk_bf16_f32 v40, v31, v28
	v_lshlrev_b32_e32 v28, 16, v45
	v_sub_f32_e32 v28, v41, v28
	v_and_b32_e32 v31, 0xffff0000, v45
	v_sub_f32_e32 v31, v43, v31
	v_cvt_pk_bf16_f32 v41, v28, v31
	v_lshlrev_b32_e32 v28, 16, v46
	v_sub_f32_e32 v28, v29, v28
	v_and_b32_e32 v29, 0xffff0000, v46
	v_sub_f32_e32 v29, v30, v29
	v_cvt_pk_bf16_f32 v42, v28, v29
	v_lshlrev_b32_e32 v28, 16, v47
	v_and_b32_e32 v29, 0xffff0000, v47
	v_sub_f32_e32 v28, v36, v28
	v_sub_f32_e32 v29, v39, v29
	v_cvt_pk_bf16_f32 v43, v28, v29
	ds_read_b128 v[28:31], v153 offset:2560
	v_and_b32_e32 v24, 0xffff0000, v24
	s_waitcnt lgkmcnt(0)
	v_mfma_f32_16x16x32_bf16 v[32:35], v[44:47], v[28:31], v[32:35]
	v_mul_f32_e32 v24, v112, v24
	v_mul_f32_e32 v48, v112, v48
	v_mfma_f32_16x16x32_bf16 v[28:31], v[40:43], v[28:31], v[32:35]
	s_nop 4
	ds_read_b128 v[32:35], v153 offset:35584
	s_waitcnt lgkmcnt(0)
	v_mfma_f32_16x16x32_bf16 v[28:31], v[44:47], v[32:35], v[28:31]
	ds_read_b128 v[36:39], v162 offset:7296
	ds_read_b128 v[40:43], v162 offset:3200
	ds_read_b128 v[32:35], v162 offset:7312
	ds_read_b128 v[44:47], v162 offset:3216
	s_waitcnt lgkmcnt(2)
	v_fma_f32 v24, v24, v41, v37
	v_lshlrev_b32_e32 v37, 16, v25
	v_and_b32_e32 v25, 0xffff0000, v25
	v_mul_f32_e32 v25, v112, v25
	v_fmac_f32_e32 v39, v25, v43
	v_lshlrev_b32_e32 v25, 16, v26
	v_mul_f32_e32 v25, v112, v25
	s_waitcnt lgkmcnt(0)
	v_fma_f32 v25, v25, v44, v32
	v_and_b32_e32 v26, 0xffff0000, v26
	v_lshlrev_b32_e32 v32, 16, v27
	v_and_b32_e32 v27, 0xffff0000, v27
	v_mul_f32_e32 v37, v112, v37
	v_mul_f32_e32 v26, v112, v26
	v_mul_f32_e32 v32, v112, v32
	v_mul_f32_e32 v27, v112, v27
	v_fma_f32 v36, v48, v40, v36
	v_fma_f32 v37, v37, v42, v38
	v_fma_f32 v26, v26, v45, v33
	v_fma_f32 v32, v32, v46, v34
	v_fmac_f32_e32 v35, v27, v47
	s_and_saveexec_b64 s[0:1], s[42:43]
	s_cbranch_execz .LBB0_1282
	v_mul_f32_e32 v27, 0x41800000, v36
	v_mul_f32_e32 v33, 0x41800000, v24
	v_med3_f32 v27, v27, s25, v218
	v_med3_f32 v33, v33, s25, v218
	v_cvt_pk_fp8_f32 v40, v27, v33
	v_mul_f32_e32 v34, 0x41800000, v37
	v_mul_f32_e32 v27, 0x41800000, v39
	v_med3_f32 v33, v34, s25, v218
	v_med3_f32 v27, v27, s25, v218
	v_cvt_pk_fp8_f32 v40, v33, v27 op_sel:[0,0,1]
	v_mul_f32_e32 v27, 0x41800000, v25
	v_mul_f32_e32 v33, 0x41800000, v26
	v_med3_f32 v27, v27, s25, v218
	v_med3_f32 v33, v33, s25, v218
	v_cvt_pk_fp8_f32 v41, v27, v33
	v_mul_f32_e32 v34, 0x41800000, v32
	v_mul_f32_e32 v27, 0x41800000, v35
	v_med3_f32 v33, v34, s25, v218
	v_med3_f32 v27, v27, s25, v218
	v_cvt_pk_fp8_f32 v41, v33, v27 op_sel:[0,0,1]
	global_store_dwordx2 v[144:145], v[40:41], off offset:800
.LBB0_1282:
	s_or_b64 exec, exec, s[0:1]
	v_cvt_pk_bf16_f32 v40, v36, v24
	v_cvt_pk_bf16_f32 v41, v37, v39
	v_cvt_pk_bf16_f32 v42, v25, v26
	v_cvt_pk_bf16_f32 v43, v32, v35
	s_nop 0
	v_and_b32_e32 v33, 0xffff0000, v40
	v_lshlrev_b32_e32 v27, 16, v40
	v_sub_f32_e32 v24, v24, v33
	v_sub_f32_e32 v27, v36, v27
	v_cvt_pk_bf16_f32 v36, v27, v24
	v_lshlrev_b32_e32 v24, 16, v41
	v_sub_f32_e32 v24, v37, v24
	v_and_b32_e32 v27, 0xffff0000, v41
	v_sub_f32_e32 v27, v39, v27
	v_cvt_pk_bf16_f32 v37, v24, v27
	v_lshlrev_b32_e32 v24, 16, v42
	v_sub_f32_e32 v24, v25, v24
	v_and_b32_e32 v25, 0xffff0000, v42
	v_sub_f32_e32 v25, v26, v25
	v_cvt_pk_bf16_f32 v38, v24, v25
	v_lshlrev_b32_e32 v24, 16, v43
	v_and_b32_e32 v25, 0xffff0000, v43
	v_sub_f32_e32 v24, v32, v24
	v_sub_f32_e32 v25, v35, v25
	v_cvt_pk_bf16_f32 v39, v24, v25
	ds_read_b128 v[24:27], v153 offset:2624
	s_waitcnt lgkmcnt(0)
	v_mfma_f32_16x16x32_bf16 v[28:31], v[40:43], v[24:27], v[28:31]
	v_mfma_f32_16x16x32_bf16 v[24:27], v[36:39], v[24:27], v[28:31]
	s_nop 6
	ds_read_b128 v[28:31], v153 offset:35648
	s_waitcnt lgkmcnt(0)
	v_mfma_f32_16x16x32_bf16 v[24:27], v[40:43], v[28:31], v[24:27]
	ds_read_b128 v[32:35], v162 offset:7424
	ds_read_b128 v[36:39], v162 offset:3328
	ds_read_b128 v[40:43], v162 offset:3344
	ds_read_b128 v[28:31], v162 offset:7440
	v_lshlrev_b32_e32 v44, 16, v20
	v_and_b32_e32 v20, 0xffff0000, v20
	v_mul_f32_e32 v20, v112, v20
	s_waitcnt lgkmcnt(2)
	v_fma_f32 v20, v20, v37, v33
	v_lshlrev_b32_e32 v33, 16, v21
	v_and_b32_e32 v21, 0xffff0000, v21
	v_mul_f32_e32 v21, v112, v21
	v_fmac_f32_e32 v35, v21, v39
	v_lshlrev_b32_e32 v21, 16, v22
	v_mul_f32_e32 v21, v112, v21
	s_waitcnt lgkmcnt(0)
	v_fma_f32 v21, v21, v40, v28
	v_and_b32_e32 v22, 0xffff0000, v22
	v_lshlrev_b32_e32 v28, 16, v23
	v_and_b32_e32 v23, 0xffff0000, v23
	v_mul_f32_e32 v44, v112, v44
	v_mul_f32_e32 v33, v112, v33
	v_mul_f32_e32 v22, v112, v22
	v_mul_f32_e32 v28, v112, v28
	v_mul_f32_e32 v23, v112, v23
	v_fma_f32 v32, v44, v36, v32
	v_fma_f32 v33, v33, v38, v34
	v_fma_f32 v22, v22, v41, v29
	v_fma_f32 v28, v28, v42, v30
	v_fmac_f32_e32 v31, v23, v43
	s_and_saveexec_b64 s[0:1], s[42:43]
	s_cbranch_execz .LBB0_1284
	v_mul_f32_e32 v23, 0x41800000, v32
	v_mul_f32_e32 v29, 0x41800000, v20
	v_med3_f32 v23, v23, s25, v218
	v_med3_f32 v29, v29, s25, v218
	v_cvt_pk_fp8_f32 v36, v23, v29
	v_mul_f32_e32 v30, 0x41800000, v33
	v_mul_f32_e32 v23, 0x41800000, v35
	v_med3_f32 v29, v30, s25, v218
	v_med3_f32 v23, v23, s25, v218
	v_cvt_pk_fp8_f32 v36, v29, v23 op_sel:[0,0,1]
	v_mul_f32_e32 v23, 0x41800000, v21
	v_mul_f32_e32 v29, 0x41800000, v22
	v_med3_f32 v23, v23, s25, v218
	v_med3_f32 v29, v29, s25, v218
	v_cvt_pk_fp8_f32 v37, v23, v29
	v_mul_f32_e32 v30, 0x41800000, v28
	v_mul_f32_e32 v23, 0x41800000, v31
	v_med3_f32 v29, v30, s25, v218
	v_med3_f32 v23, v23, s25, v218
	v_cvt_pk_fp8_f32 v37, v29, v23 op_sel:[0,0,1]
	global_store_dwordx2 v[144:145], v[36:37], off offset:832
.LBB0_1284:
	s_or_b64 exec, exec, s[0:1]
	v_cvt_pk_bf16_f32 v36, v32, v20
	v_cvt_pk_bf16_f32 v37, v33, v35
	v_cvt_pk_bf16_f32 v38, v21, v22
	v_cvt_pk_bf16_f32 v39, v28, v31
	v_lshlrev_b32_e32 v40, 16, v16
	v_and_b32_e32 v29, 0xffff0000, v36
	v_lshlrev_b32_e32 v23, 16, v36
	v_sub_f32_e32 v20, v20, v29
	v_sub_f32_e32 v23, v32, v23
	v_cvt_pk_bf16_f32 v32, v23, v20
	v_lshlrev_b32_e32 v20, 16, v37
	v_sub_f32_e32 v20, v33, v20
	v_and_b32_e32 v23, 0xffff0000, v37
	v_sub_f32_e32 v23, v35, v23
	v_cvt_pk_bf16_f32 v33, v20, v23
	v_lshlrev_b32_e32 v20, 16, v38
	v_sub_f32_e32 v20, v21, v20
	v_and_b32_e32 v21, 0xffff0000, v38
	v_sub_f32_e32 v21, v22, v21
	v_cvt_pk_bf16_f32 v34, v20, v21
	v_lshlrev_b32_e32 v20, 16, v39
	v_and_b32_e32 v21, 0xffff0000, v39
	v_sub_f32_e32 v20, v28, v20
	v_sub_f32_e32 v21, v31, v21
	v_cvt_pk_bf16_f32 v35, v20, v21
	ds_read_b128 v[20:23], v153 offset:2688
	v_and_b32_e32 v16, 0xffff0000, v16
	s_waitcnt lgkmcnt(0)
	v_mfma_f32_16x16x32_bf16 v[24:27], v[36:39], v[20:23], v[24:27]
	v_mul_f32_e32 v16, v112, v16
	v_mul_f32_e32 v40, v112, v40
	v_mfma_f32_16x16x32_bf16 v[20:23], v[32:35], v[20:23], v[24:27]
	s_nop 4
	ds_read_b128 v[24:27], v153 offset:35712
	s_waitcnt lgkmcnt(0)
	v_mfma_f32_16x16x32_bf16 v[20:23], v[36:39], v[24:27], v[20:23]
	ds_read_b128 v[28:31], v162 offset:7552
	ds_read_b128 v[32:35], v162 offset:3456
	ds_read_b128 v[24:27], v162 offset:7568
	ds_read_b128 v[36:39], v162 offset:3472
	s_waitcnt lgkmcnt(2)
	v_fma_f32 v16, v16, v33, v29
	v_lshlrev_b32_e32 v29, 16, v17
	v_and_b32_e32 v17, 0xffff0000, v17
	v_mul_f32_e32 v17, v112, v17
	v_fmac_f32_e32 v31, v17, v35
	v_lshlrev_b32_e32 v17, 16, v18
	v_mul_f32_e32 v17, v112, v17
	s_waitcnt lgkmcnt(0)
	v_fma_f32 v17, v17, v36, v24
	v_and_b32_e32 v18, 0xffff0000, v18
	v_lshlrev_b32_e32 v24, 16, v19
	v_and_b32_e32 v19, 0xffff0000, v19
	v_mul_f32_e32 v29, v112, v29
	v_mul_f32_e32 v18, v112, v18
	v_mul_f32_e32 v24, v112, v24
	v_mul_f32_e32 v19, v112, v19
	v_fma_f32 v28, v40, v32, v28
	v_fma_f32 v29, v29, v34, v30
	v_fma_f32 v18, v18, v37, v25
	v_fma_f32 v24, v24, v38, v26
	v_fmac_f32_e32 v27, v19, v39
	s_and_saveexec_b64 s[0:1], s[42:43]
	s_cbranch_execz .LBB0_1286
	v_mul_f32_e32 v19, 0x41800000, v28
	v_mul_f32_e32 v25, 0x41800000, v16
	v_med3_f32 v19, v19, s25, v218
	v_med3_f32 v25, v25, s25, v218
	v_cvt_pk_fp8_f32 v32, v19, v25
	v_mul_f32_e32 v26, 0x41800000, v29
	v_mul_f32_e32 v19, 0x41800000, v31
	v_med3_f32 v25, v26, s25, v218
	v_med3_f32 v19, v19, s25, v218
	v_cvt_pk_fp8_f32 v32, v25, v19 op_sel:[0,0,1]
	v_mul_f32_e32 v19, 0x41800000, v17
	v_mul_f32_e32 v25, 0x41800000, v18
	v_med3_f32 v19, v19, s25, v218
	v_med3_f32 v25, v25, s25, v218
	v_cvt_pk_fp8_f32 v33, v19, v25
	v_mul_f32_e32 v26, 0x41800000, v24
	v_mul_f32_e32 v19, 0x41800000, v27
	v_med3_f32 v25, v26, s25, v218
	v_med3_f32 v19, v19, s25, v218
	v_cvt_pk_fp8_f32 v33, v25, v19 op_sel:[0,0,1]
	global_store_dwordx2 v[144:145], v[32:33], off offset:864
.LBB0_1286:
	s_or_b64 exec, exec, s[0:1]
	v_cvt_pk_bf16_f32 v32, v28, v16
	v_cvt_pk_bf16_f32 v33, v29, v31
	v_cvt_pk_bf16_f32 v34, v17, v18
	v_cvt_pk_bf16_f32 v35, v24, v27
	s_nop 0
	v_and_b32_e32 v25, 0xffff0000, v32
	v_lshlrev_b32_e32 v19, 16, v32
	v_sub_f32_e32 v16, v16, v25
	v_sub_f32_e32 v19, v28, v19
	v_cvt_pk_bf16_f32 v28, v19, v16
	v_lshlrev_b32_e32 v16, 16, v33
	v_sub_f32_e32 v16, v29, v16
	v_and_b32_e32 v19, 0xffff0000, v33
	v_sub_f32_e32 v19, v31, v19
	v_cvt_pk_bf16_f32 v29, v16, v19
	v_lshlrev_b32_e32 v16, 16, v34
	v_sub_f32_e32 v16, v17, v16
	v_and_b32_e32 v17, 0xffff0000, v34
	v_sub_f32_e32 v17, v18, v17
	v_cvt_pk_bf16_f32 v30, v16, v17
	v_lshlrev_b32_e32 v16, 16, v35
	v_and_b32_e32 v17, 0xffff0000, v35
	v_sub_f32_e32 v16, v24, v16
	v_sub_f32_e32 v17, v27, v17
	v_cvt_pk_bf16_f32 v31, v16, v17
	ds_read_b128 v[16:19], v153 offset:2752
	s_waitcnt lgkmcnt(0)
	v_mfma_f32_16x16x32_bf16 v[20:23], v[32:35], v[16:19], v[20:23]
	v_mfma_f32_16x16x32_bf16 v[16:19], v[28:31], v[16:19], v[20:23]
	s_nop 6
	ds_read_b128 v[20:23], v153 offset:35776
	s_waitcnt lgkmcnt(0)
	v_mfma_f32_16x16x32_bf16 v[16:19], v[32:35], v[20:23], v[16:19]
	ds_read_b128 v[24:27], v162 offset:7680
	ds_read_b128 v[28:31], v162 offset:3584
	ds_read_b128 v[32:35], v162 offset:3600
	ds_read_b128 v[20:23], v162 offset:7696
	v_lshlrev_b32_e32 v36, 16, v12
	v_and_b32_e32 v12, 0xffff0000, v12
	v_mul_f32_e32 v12, v112, v12
	s_waitcnt lgkmcnt(2)
	v_fma_f32 v12, v12, v29, v25
	v_lshlrev_b32_e32 v25, 16, v13
	v_and_b32_e32 v13, 0xffff0000, v13
	v_mul_f32_e32 v13, v112, v13
	v_fmac_f32_e32 v27, v13, v31
	v_lshlrev_b32_e32 v13, 16, v14
	v_mul_f32_e32 v13, v112, v13
	s_waitcnt lgkmcnt(0)
	v_fma_f32 v13, v13, v32, v20
	v_and_b32_e32 v14, 0xffff0000, v14
	v_lshlrev_b32_e32 v20, 16, v15
	v_and_b32_e32 v15, 0xffff0000, v15
	v_mul_f32_e32 v36, v112, v36
	v_mul_f32_e32 v25, v112, v25
	v_mul_f32_e32 v14, v112, v14
	v_mul_f32_e32 v20, v112, v20
	v_mul_f32_e32 v15, v112, v15
	v_fma_f32 v24, v36, v28, v24
	v_fma_f32 v25, v25, v30, v26
	v_fma_f32 v14, v14, v33, v21
	v_fma_f32 v20, v20, v34, v22
	v_fmac_f32_e32 v23, v15, v35
	s_and_saveexec_b64 s[0:1], s[42:43]
	s_cbranch_execz .LBB0_1288
	v_mul_f32_e32 v15, 0x41800000, v24
	v_mul_f32_e32 v21, 0x41800000, v12
	v_med3_f32 v15, v15, s25, v218
	v_med3_f32 v21, v21, s25, v218
	v_cvt_pk_fp8_f32 v28, v15, v21
	v_mul_f32_e32 v22, 0x41800000, v25
	v_mul_f32_e32 v15, 0x41800000, v27
	v_med3_f32 v21, v22, s25, v218
	v_med3_f32 v15, v15, s25, v218
	v_cvt_pk_fp8_f32 v28, v21, v15 op_sel:[0,0,1]
	v_mul_f32_e32 v15, 0x41800000, v13
	v_mul_f32_e32 v21, 0x41800000, v14
	v_med3_f32 v15, v15, s25, v218
	v_med3_f32 v21, v21, s25, v218
	v_cvt_pk_fp8_f32 v29, v15, v21
	v_mul_f32_e32 v22, 0x41800000, v20
	v_mul_f32_e32 v15, 0x41800000, v23
	v_med3_f32 v21, v22, s25, v218
	v_med3_f32 v15, v15, s25, v218
	v_cvt_pk_fp8_f32 v29, v21, v15 op_sel:[0,0,1]
	global_store_dwordx2 v[144:145], v[28:29], off offset:896
.LBB0_1288:
	s_or_b64 exec, exec, s[0:1]
	v_cvt_pk_bf16_f32 v28, v24, v12
	v_cvt_pk_bf16_f32 v29, v25, v27
	v_cvt_pk_bf16_f32 v30, v13, v14
	v_cvt_pk_bf16_f32 v31, v20, v23
	v_lshlrev_b32_e32 v32, 16, v8
	v_and_b32_e32 v21, 0xffff0000, v28
	v_lshlrev_b32_e32 v15, 16, v28
	v_sub_f32_e32 v12, v12, v21
	v_sub_f32_e32 v15, v24, v15
	v_cvt_pk_bf16_f32 v24, v15, v12
	v_lshlrev_b32_e32 v12, 16, v29
	v_sub_f32_e32 v12, v25, v12
	v_and_b32_e32 v15, 0xffff0000, v29
	v_sub_f32_e32 v15, v27, v15
	v_cvt_pk_bf16_f32 v25, v12, v15
	v_lshlrev_b32_e32 v12, 16, v30
	v_sub_f32_e32 v12, v13, v12
	v_and_b32_e32 v13, 0xffff0000, v30
	v_sub_f32_e32 v13, v14, v13
	v_cvt_pk_bf16_f32 v26, v12, v13
	v_lshlrev_b32_e32 v12, 16, v31
	v_and_b32_e32 v13, 0xffff0000, v31
	v_sub_f32_e32 v12, v20, v12
	v_sub_f32_e32 v13, v23, v13
	v_cvt_pk_bf16_f32 v27, v12, v13
	ds_read_b128 v[12:15], v153 offset:2816
	v_and_b32_e32 v8, 0xffff0000, v8
	s_waitcnt lgkmcnt(0)
	v_mfma_f32_16x16x32_bf16 v[16:19], v[28:31], v[12:15], v[16:19]
	v_mul_f32_e32 v8, v112, v8
	v_mul_f32_e32 v32, v112, v32
	v_mfma_f32_16x16x32_bf16 v[12:15], v[24:27], v[12:15], v[16:19]
	s_nop 4
	ds_read_b128 v[16:19], v153 offset:35840
	s_waitcnt lgkmcnt(0)
	v_mfma_f32_16x16x32_bf16 v[12:15], v[28:31], v[16:19], v[12:15]
	ds_read_b128 v[20:23], v162 offset:7808
	ds_read_b128 v[24:27], v162 offset:3712
	ds_read_b128 v[16:19], v162 offset:7824
	ds_read_b128 v[28:31], v162 offset:3728
	s_waitcnt lgkmcnt(2)
	v_fma_f32 v8, v8, v25, v21
	v_lshlrev_b32_e32 v21, 16, v9
	v_and_b32_e32 v9, 0xffff0000, v9
	v_mul_f32_e32 v9, v112, v9
	v_fmac_f32_e32 v23, v9, v27
	v_lshlrev_b32_e32 v9, 16, v10
	v_mul_f32_e32 v9, v112, v9
	s_waitcnt lgkmcnt(0)
	v_fma_f32 v9, v9, v28, v16
	v_and_b32_e32 v10, 0xffff0000, v10
	v_lshlrev_b32_e32 v16, 16, v11
	v_and_b32_e32 v11, 0xffff0000, v11
	v_mul_f32_e32 v21, v112, v21
	v_mul_f32_e32 v10, v112, v10
	v_mul_f32_e32 v16, v112, v16
	v_mul_f32_e32 v11, v112, v11
	v_fma_f32 v20, v32, v24, v20
	v_fma_f32 v21, v21, v26, v22
	v_fma_f32 v10, v10, v29, v17
	v_fma_f32 v16, v16, v30, v18
	v_fmac_f32_e32 v19, v11, v31
	s_and_saveexec_b64 s[0:1], s[42:43]
	s_cbranch_execz .LBB0_1290
	v_mul_f32_e32 v11, 0x41800000, v20
	v_mul_f32_e32 v17, 0x41800000, v8
	v_med3_f32 v11, v11, s25, v218
	v_med3_f32 v17, v17, s25, v218
	v_cvt_pk_fp8_f32 v24, v11, v17
	v_mul_f32_e32 v18, 0x41800000, v21
	v_mul_f32_e32 v11, 0x41800000, v23
	v_med3_f32 v17, v18, s25, v218
	v_med3_f32 v11, v11, s25, v218
	v_cvt_pk_fp8_f32 v24, v17, v11 op_sel:[0,0,1]
	v_mul_f32_e32 v11, 0x41800000, v9
	v_mul_f32_e32 v17, 0x41800000, v10
	v_med3_f32 v11, v11, s25, v218
	v_med3_f32 v17, v17, s25, v218
	v_cvt_pk_fp8_f32 v25, v11, v17
	v_mul_f32_e32 v18, 0x41800000, v16
	v_mul_f32_e32 v11, 0x41800000, v19
	v_med3_f32 v17, v18, s25, v218
	v_med3_f32 v11, v11, s25, v218
	v_cvt_pk_fp8_f32 v25, v17, v11 op_sel:[0,0,1]
	global_store_dwordx2 v[144:145], v[24:25], off offset:928
.LBB0_1290:
	s_or_b64 exec, exec, s[0:1]
	v_cvt_pk_bf16_f32 v24, v20, v8
	v_cvt_pk_bf16_f32 v25, v21, v23
	v_cvt_pk_bf16_f32 v26, v9, v10
	v_cvt_pk_bf16_f32 v27, v16, v19
	s_nop 0
	v_and_b32_e32 v17, 0xffff0000, v24
	v_lshlrev_b32_e32 v11, 16, v24
	v_sub_f32_e32 v8, v8, v17
	v_sub_f32_e32 v11, v20, v11
	v_cvt_pk_bf16_f32 v20, v11, v8
	v_lshlrev_b32_e32 v8, 16, v25
	v_sub_f32_e32 v8, v21, v8
	v_and_b32_e32 v11, 0xffff0000, v25
	v_sub_f32_e32 v11, v23, v11
	v_cvt_pk_bf16_f32 v21, v8, v11
	v_lshlrev_b32_e32 v8, 16, v26
	v_sub_f32_e32 v8, v9, v8
	v_and_b32_e32 v9, 0xffff0000, v26
	v_sub_f32_e32 v9, v10, v9
	v_cvt_pk_bf16_f32 v22, v8, v9
	v_lshlrev_b32_e32 v8, 16, v27
	v_and_b32_e32 v9, 0xffff0000, v27
	v_sub_f32_e32 v8, v16, v8
	v_sub_f32_e32 v9, v19, v9
	v_cvt_pk_bf16_f32 v23, v8, v9
	ds_read_b128 v[8:11], v153 offset:2880
	s_waitcnt lgkmcnt(0)
	v_mfma_f32_16x16x32_bf16 v[12:15], v[24:27], v[8:11], v[12:15]
	v_mfma_f32_16x16x32_bf16 v[8:11], v[20:23], v[8:11], v[12:15]
	s_nop 6
	ds_read_b128 v[12:15], v153 offset:35904
	s_waitcnt lgkmcnt(0)
	v_mfma_f32_16x16x32_bf16 v[8:11], v[24:27], v[12:15], v[8:11]
	ds_read_b128 v[16:19], v162 offset:7936
	ds_read_b128 v[20:23], v162 offset:3840
	ds_read_b128 v[24:27], v162 offset:3856
	ds_read_b128 v[12:15], v162 offset:7952
	v_lshlrev_b32_e32 v28, 16, v4
	v_and_b32_e32 v4, 0xffff0000, v4
	v_mul_f32_e32 v4, v112, v4
	s_waitcnt lgkmcnt(2)
	v_fma_f32 v4, v4, v21, v17
	v_lshlrev_b32_e32 v17, 16, v5
	v_and_b32_e32 v5, 0xffff0000, v5
	v_mul_f32_e32 v5, v112, v5
	v_fmac_f32_e32 v19, v5, v23
	v_lshlrev_b32_e32 v5, 16, v6
	v_mul_f32_e32 v5, v112, v5
	s_waitcnt lgkmcnt(0)
	v_fma_f32 v5, v5, v24, v12
	v_and_b32_e32 v6, 0xffff0000, v6
	v_lshlrev_b32_e32 v12, 16, v7
	v_and_b32_e32 v7, 0xffff0000, v7
	v_mul_f32_e32 v28, v112, v28
	v_mul_f32_e32 v17, v112, v17
	v_mul_f32_e32 v6, v112, v6
	v_mul_f32_e32 v12, v112, v12
	v_mul_f32_e32 v7, v112, v7
	v_fma_f32 v16, v28, v20, v16
	v_fma_f32 v17, v17, v22, v18
	v_fma_f32 v6, v6, v25, v13
	v_fma_f32 v12, v12, v26, v14
	v_fmac_f32_e32 v15, v7, v27
	s_and_saveexec_b64 s[0:1], s[42:43]
	s_cbranch_execz .LBB0_1292
	v_mul_f32_e32 v7, 0x41800000, v16
	v_mul_f32_e32 v13, 0x41800000, v4
	v_med3_f32 v7, v7, s25, v218
	v_med3_f32 v13, v13, s25, v218
	v_cvt_pk_fp8_f32 v20, v7, v13
	v_mul_f32_e32 v14, 0x41800000, v17
	v_mul_f32_e32 v7, 0x41800000, v19
	v_med3_f32 v13, v14, s25, v218
	v_med3_f32 v7, v7, s25, v218
	v_cvt_pk_fp8_f32 v20, v13, v7 op_sel:[0,0,1]
	v_mul_f32_e32 v7, 0x41800000, v5
	v_mul_f32_e32 v13, 0x41800000, v6
	v_med3_f32 v7, v7, s25, v218
	v_med3_f32 v13, v13, s25, v218
	v_cvt_pk_fp8_f32 v21, v7, v13
	v_mul_f32_e32 v14, 0x41800000, v12
	v_mul_f32_e32 v7, 0x41800000, v15
	v_med3_f32 v13, v14, s25, v218
	v_med3_f32 v7, v7, s25, v218
	v_cvt_pk_fp8_f32 v21, v13, v7 op_sel:[0,0,1]
	global_store_dwordx2 v[144:145], v[20:21], off offset:960
.LBB0_1292:
	s_or_b64 exec, exec, s[0:1]
	v_cvt_pk_bf16_f32 v20, v16, v4
	v_cvt_pk_bf16_f32 v21, v17, v19
	v_cvt_pk_bf16_f32 v22, v5, v6
	v_cvt_pk_bf16_f32 v23, v12, v15
	v_lshlrev_b32_e32 v24, 16, v0
	v_and_b32_e32 v13, 0xffff0000, v20
	v_lshlrev_b32_e32 v7, 16, v20
	v_sub_f32_e32 v4, v4, v13
	v_sub_f32_e32 v7, v16, v7
	v_cvt_pk_bf16_f32 v16, v7, v4
	v_lshlrev_b32_e32 v4, 16, v21
	v_sub_f32_e32 v4, v17, v4
	v_and_b32_e32 v7, 0xffff0000, v21
	v_sub_f32_e32 v7, v19, v7
	v_cvt_pk_bf16_f32 v17, v4, v7
	v_lshlrev_b32_e32 v4, 16, v22
	v_sub_f32_e32 v4, v5, v4
	v_and_b32_e32 v5, 0xffff0000, v22
	v_sub_f32_e32 v5, v6, v5
	v_cvt_pk_bf16_f32 v18, v4, v5
	v_lshlrev_b32_e32 v4, 16, v23
	v_and_b32_e32 v5, 0xffff0000, v23
	v_sub_f32_e32 v4, v12, v4
	v_sub_f32_e32 v5, v15, v5
	v_cvt_pk_bf16_f32 v19, v4, v5
	ds_read_b128 v[4:7], v153 offset:2944
	v_and_b32_e32 v0, 0xffff0000, v0
	s_waitcnt lgkmcnt(0)
	v_mfma_f32_16x16x32_bf16 v[8:11], v[20:23], v[4:7], v[8:11]
	v_mul_f32_e32 v0, v112, v0
	v_mul_f32_e32 v24, v112, v24
	v_mfma_f32_16x16x32_bf16 v[4:7], v[16:19], v[4:7], v[8:11]
	s_nop 4
	ds_read_b128 v[8:11], v153 offset:35968
	s_waitcnt lgkmcnt(0)
	v_mfma_f32_16x16x32_bf16 v[4:7], v[20:23], v[8:11], v[4:7]
	ds_read_b128 v[12:15], v162 offset:8064
	ds_read_b128 v[16:19], v162 offset:3968
	ds_read_b128 v[8:11], v162 offset:8080
	ds_read_b128 v[20:23], v162 offset:3984
	s_waitcnt lgkmcnt(2)
	v_fma_f32 v0, v0, v17, v13
	v_lshlrev_b32_e32 v13, 16, v1
	v_and_b32_e32 v1, 0xffff0000, v1
	v_mul_f32_e32 v1, v112, v1
	v_fmac_f32_e32 v15, v1, v19
	v_lshlrev_b32_e32 v1, 16, v2
	v_mul_f32_e32 v1, v112, v1
	s_waitcnt lgkmcnt(0)
	v_fma_f32 v1, v1, v20, v8
	v_and_b32_e32 v2, 0xffff0000, v2
	v_lshlrev_b32_e32 v8, 16, v3
	v_and_b32_e32 v3, 0xffff0000, v3
	v_mul_f32_e32 v13, v112, v13
	v_mul_f32_e32 v2, v112, v2
	v_mul_f32_e32 v8, v112, v8
	v_mul_f32_e32 v3, v112, v3
	v_fma_f32 v12, v24, v16, v12
	v_fma_f32 v13, v13, v18, v14
	v_fma_f32 v2, v2, v21, v9
	v_fma_f32 v8, v8, v22, v10
	v_fmac_f32_e32 v11, v3, v23
	s_and_saveexec_b64 s[0:1], s[42:43]
	s_cbranch_execz .LBB0_1294
	v_mul_f32_e32 v3, 0x41800000, v12
	v_mul_f32_e32 v9, 0x41800000, v0
	v_med3_f32 v3, v3, s25, v218
	v_med3_f32 v9, v9, s25, v218
	v_cvt_pk_fp8_f32 v16, v3, v9
	v_mul_f32_e32 v10, 0x41800000, v13
	v_mul_f32_e32 v14, 0x41800000, v15
	v_med3_f32 v3, v10, s25, v218
	v_med3_f32 v9, v14, s25, v218
	v_cvt_pk_fp8_f32 v16, v3, v9 op_sel:[0,0,1]
	v_mul_f32_e32 v3, 0x41800000, v1
	v_mul_f32_e32 v9, 0x41800000, v2
	v_med3_f32 v3, v3, s25, v218
	v_med3_f32 v9, v9, s25, v218
	v_cvt_pk_fp8_f32 v17, v3, v9
	v_mul_f32_e32 v10, 0x41800000, v8
	v_mul_f32_e32 v14, 0x41800000, v11
	v_med3_f32 v3, v10, s25, v218
	v_med3_f32 v9, v14, s25, v218
	v_cvt_pk_fp8_f32 v17, v3, v9 op_sel:[0,0,1]
	global_store_dwordx2 v[144:145], v[16:17], off offset:992

.LBB0_1591:
	s_mov_b32 s6, 0xb838aa3b
	v_pk_mul_f32 v[6:7], v[186:187], s[6:7] op_sel_hi:[1,0]
	v_pk_mul_f32 v[10:11], v[178:179], s[6:7] op_sel_hi:[1,0]
	v_exp_f32_e32 v6, v6
	v_exp_f32_e32 v7, v7
	v_exp_f32_e32 v10, v10
	v_exp_f32_e32 v11, v11
	v_pk_mul_f32 v[4:5], v[186:187], v[190:191]
	v_pk_fma_f32 v[6:7], v[6:7], s[34:35], s[34:35] op_sel_hi:[1,0,0]
	v_pk_mul_f32 v[8:9], v[178:179], v[182:183]
	v_rcp_f32_e32 v6, v6
	v_rcp_f32_e32 v7, v7
	v_pk_fma_f32 v[10:11], v[10:11], s[34:35], s[34:35] op_sel_hi:[1,0,0]
	v_mbcnt_lo_u32_b32 v2, -1, 0
	v_mbcnt_hi_u32_b32 v2, -1, v2
	s_lshl_b32 s2, s76, 8
	v_rcp_f32_e32 v10, v10
	v_rcp_f32_e32 v11, v11
	v_pk_mul_f32 v[4:5], v[6:7], v[4:5]
	v_pk_mul_f32 v[6:7], v[188:189], s[6:7] op_sel_hi:[1,0]
	v_and_or_b32 v0, v2, 15, s64
	v_exp_f32_e32 v6, v6
	v_exp_f32_e32 v7, v7
	v_pk_mul_f32 v[8:9], v[10:11], v[8:9]
	v_pk_mul_f32 v[10:11], v[180:181], s[6:7] op_sel_hi:[1,0]
	v_ashrrev_i32_e32 v2, 1, v2
	v_exp_f32_e32 v10, v10
	v_exp_f32_e32 v11, v11
	v_pk_fma_f32 v[6:7], v[6:7], s[34:35], s[34:35] op_sel_hi:[1,0,0]
	v_and_b32_e32 v12, -8, v2
	v_rcp_f32_e32 v6, v6
	v_rcp_f32_e32 v7, v7
	v_pk_fma_f32 v[10:11], v[10:11], s[34:35], s[34:35] op_sel_hi:[1,0,0]
	v_pk_mul_f32 v[2:3], v[188:189], v[192:193]
	v_rcp_f32_e32 v10, v10
	v_rcp_f32_e32 v11, v11
	v_pk_mul_f32 v[2:3], v[6:7], v[2:3]
	v_pk_mul_f32 v[6:7], v[180:181], v[184:185]
	v_med3_f32 v5, v5, s25, v218
	v_pk_mul_f32 v[6:7], v[10:11], v[6:7]
	v_med3_f32 v11, v4, s25, v218
	s_mul_i32 s0, s58, 0x1200
	s_lshl_b32 s3, s20, 7
	s_ashr_i32 s4, s2, 31
	v_cvt_pk_fp8_f32 v4, v11, v5
	s_mul_hi_i32 s1, s58, 0x1200
	s_add_u32 s0, s0, s2
	v_mov_b32_e32 v1, s74
	s_addc_u32 s1, s1, s4
	v_lshl_add_u64 v[0:1], v[0:1], 0, s[0:1]
	s_or_b32 s0, s3, s65
	v_med3_f32 v2, v2, s25, v218
	v_med3_f32 v3, v3, s25, v218
	v_add_u32_e32 v10, s0, v12
	v_cvt_pk_fp8_f32 v4, v2, v3 op_sel:[0,0,1]
	v_med3_f32 v2, v8, s25, v218
	v_med3_f32 v3, v9, s25, v218
	v_lshlrev_b64 v[0:1], 11, v[0:1]
	v_cvt_pk_fp8_f32 v5, v2, v3
	v_med3_f32 v2, v6, s25, v218
	v_med3_f32 v3, v7, s25, v218
	v_lshl_add_u64 v[0:1], s[46:47], 0, v[0:1]
	v_ashrrev_i32_e32 v11, 31, v10
	v_pk_mul_f32 v[6:7], v[170:171], s[6:7] op_sel_hi:[1,0]
	v_lshl_add_u64 v[0:1], v[0:1], 0, v[10:11]
	v_exp_f32_e32 v6, v6
	v_exp_f32_e32 v7, v7
	v_pk_mul_f32 v[10:11], v[162:163], s[6:7] op_sel_hi:[1,0]
	v_cvt_pk_fp8_f32 v5, v2, v3 op_sel:[0,0,1]
	v_exp_f32_e32 v10, v10
	v_exp_f32_e32 v11, v11
	v_pk_fma_f32 v[6:7], v[6:7], s[34:35], s[34:35] op_sel_hi:[1,0,0]
	global_store_dwordx2 v[0:1], v[4:5], off
	v_rcp_f32_e32 v6, v6
	v_rcp_f32_e32 v7, v7
	v_pk_fma_f32 v[10:11], v[10:11], s[34:35], s[34:35] op_sel_hi:[1,0,0]
	v_pk_mul_f32 v[4:5], v[170:171], v[174:175]
	v_rcp_f32_e32 v10, v10
	v_rcp_f32_e32 v11, v11
	v_pk_mul_f32 v[4:5], v[6:7], v[4:5]
	v_pk_mul_f32 v[6:7], v[172:173], s[6:7] op_sel_hi:[1,0]
	v_pk_mul_f32 v[8:9], v[162:163], v[166:167]
	v_exp_f32_e32 v6, v6
	v_exp_f32_e32 v7, v7
	v_pk_mul_f32 v[8:9], v[10:11], v[8:9]
	v_pk_mul_f32 v[10:11], v[164:165], s[6:7] op_sel_hi:[1,0]
	v_pk_mul_f32 v[2:3], v[172:173], v[176:177]
	v_exp_f32_e32 v10, v10
	v_exp_f32_e32 v11, v11
	v_pk_fma_f32 v[6:7], v[6:7], s[34:35], s[34:35] op_sel_hi:[1,0,0]
	v_med3_f32 v5, v5, s25, v218
	v_rcp_f32_e32 v6, v6
	v_rcp_f32_e32 v7, v7
	v_pk_fma_f32 v[10:11], v[10:11], s[34:35], s[34:35] op_sel_hi:[1,0,0]
	s_mov_b32 s0, 0x10000
	v_rcp_f32_e32 v10, v10
	v_rcp_f32_e32 v11, v11
	v_pk_mul_f32 v[2:3], v[6:7], v[2:3]
	v_pk_mul_f32 v[6:7], v[164:165], v[168:169]
	v_med3_f32 v2, v2, s25, v218
	v_pk_mul_f32 v[6:7], v[10:11], v[6:7]
	v_med3_f32 v10, v4, s25, v218
	v_cvt_pk_fp8_f32 v4, v10, v5
	v_med3_f32 v3, v3, s25, v218
	v_pk_mul_f32 v[10:11], v[146:147], s[6:7] op_sel_hi:[1,0]
	v_cvt_pk_fp8_f32 v4, v2, v3 op_sel:[0,0,1]
	v_med3_f32 v2, v8, s25, v218
	v_med3_f32 v3, v9, s25, v218
	v_cvt_pk_fp8_f32 v5, v2, v3
	v_med3_f32 v2, v6, s25, v218
	v_med3_f32 v3, v7, s25, v218
	v_pk_mul_f32 v[6:7], v[154:155], s[6:7] op_sel_hi:[1,0]
	v_exp_f32_e32 v10, v10
	v_exp_f32_e32 v6, v6
	v_exp_f32_e32 v7, v7
	v_exp_f32_e32 v11, v11
	v_cvt_pk_fp8_f32 v5, v2, v3 op_sel:[0,0,1]
	v_add_co_u32_e32 v2, vcc, s91, v0
	v_pk_fma_f32 v[6:7], v[6:7], s[34:35], s[34:35] op_sel_hi:[1,0,0]
	v_pk_fma_f32 v[10:11], v[10:11], s[34:35], s[34:35] op_sel_hi:[1,0,0]
	v_rcp_f32_e32 v6, v6
	v_rcp_f32_e32 v7, v7
	v_rcp_f32_e32 v10, v10
	v_rcp_f32_e32 v11, v11
	v_addc_co_u32_e32 v3, vcc, 0, v1, vcc
	global_store_dwordx2 v[2:3], v[4:5], off
	v_pk_mul_f32 v[4:5], v[154:155], v[158:159]
	v_pk_mul_f32 v[8:9], v[146:147], v[150:151]
	v_pk_mul_f32 v[4:5], v[6:7], v[4:5]
	v_pk_mul_f32 v[6:7], v[156:157], s[6:7] op_sel_hi:[1,0]
	v_pk_mul_f32 v[8:9], v[10:11], v[8:9]
	v_exp_f32_e32 v6, v6
	v_exp_f32_e32 v7, v7
	v_pk_mul_f32 v[10:11], v[148:149], s[6:7] op_sel_hi:[1,0]
	v_pk_mul_f32 v[2:3], v[156:157], v[160:161]
	v_exp_f32_e32 v10, v10
	v_exp_f32_e32 v11, v11
	v_pk_fma_f32 v[6:7], v[6:7], s[34:35], s[34:35] op_sel_hi:[1,0,0]
	v_med3_f32 v5, v5, s25, v218
	v_rcp_f32_e32 v6, v6
	v_rcp_f32_e32 v7, v7
	v_pk_fma_f32 v[10:11], v[10:11], s[34:35], s[34:35] op_sel_hi:[1,0,0]
	v_pk_mul_f32 v[2:3], v[6:7], v[2:3]
	v_rcp_f32_e32 v10, v10
	v_rcp_f32_e32 v11, v11
	v_pk_mul_f32 v[6:7], v[148:149], v[152:153]
	v_med3_f32 v2, v2, s25, v218
	v_med3_f32 v3, v3, s25, v218
	v_pk_mul_f32 v[6:7], v[10:11], v[6:7]
	v_med3_f32 v10, v4, s25, v218
	v_cvt_pk_fp8_f32 v4, v10, v5
	v_pk_mul_f32 v[10:11], v[130:131], s[6:7] op_sel_hi:[1,0]
	v_cvt_pk_fp8_f32 v4, v2, v3 op_sel:[0,0,1]
	v_med3_f32 v2, v8, s25, v218
	v_med3_f32 v3, v9, s25, v218
	v_cvt_pk_fp8_f32 v5, v2, v3
	v_med3_f32 v2, v6, s25, v218
	v_med3_f32 v3, v7, s25, v218
	v_pk_mul_f32 v[6:7], v[138:139], s[6:7] op_sel_hi:[1,0]
	v_exp_f32_e32 v10, v10
	v_exp_f32_e32 v6, v6
	v_exp_f32_e32 v7, v7
	v_exp_f32_e32 v11, v11
	v_cvt_pk_fp8_f32 v5, v2, v3 op_sel:[0,0,1]
	v_add_co_u32_e32 v2, vcc, s0, v0
	v_pk_fma_f32 v[6:7], v[6:7], s[34:35], s[34:35] op_sel_hi:[1,0,0]
	v_pk_fma_f32 v[10:11], v[10:11], s[34:35], s[34:35] op_sel_hi:[1,0,0]
	v_rcp_f32_e32 v6, v6
	v_rcp_f32_e32 v7, v7
	v_rcp_f32_e32 v10, v10
	v_rcp_f32_e32 v11, v11
	v_addc_co_u32_e32 v3, vcc, 0, v1, vcc
	global_store_dwordx2 v[2:3], v[4:5], off
	v_pk_mul_f32 v[4:5], v[138:139], v[142:143]
	v_pk_mul_f32 v[8:9], v[130:131], v[134:135]
	v_pk_mul_f32 v[4:5], v[6:7], v[4:5]
	v_pk_mul_f32 v[6:7], v[140:141], s[6:7] op_sel_hi:[1,0]
	v_pk_mul_f32 v[8:9], v[10:11], v[8:9]
	v_exp_f32_e32 v6, v6
	v_exp_f32_e32 v7, v7
	v_pk_mul_f32 v[10:11], v[132:133], s[6:7] op_sel_hi:[1,0]
	v_pk_mul_f32 v[2:3], v[140:141], v[144:145]
	v_exp_f32_e32 v10, v10
	v_exp_f32_e32 v11, v11
	v_pk_fma_f32 v[6:7], v[6:7], s[34:35], s[34:35] op_sel_hi:[1,0,0]
	v_med3_f32 v5, v5, s25, v218
	v_rcp_f32_e32 v6, v6
	v_rcp_f32_e32 v7, v7
	v_pk_fma_f32 v[10:11], v[10:11], s[34:35], s[34:35] op_sel_hi:[1,0,0]
	s_mov_b32 s0, 0x18000
	v_rcp_f32_e32 v10, v10
	v_rcp_f32_e32 v11, v11
	v_pk_mul_f32 v[2:3], v[6:7], v[2:3]
	v_pk_mul_f32 v[6:7], v[132:133], v[136:137]
	v_med3_f32 v2, v2, s25, v218
	v_pk_mul_f32 v[6:7], v[10:11], v[6:7]
	v_med3_f32 v10, v4, s25, v218
	v_cvt_pk_fp8_f32 v4, v10, v5
	v_med3_f32 v3, v3, s25, v218
	v_pk_mul_f32 v[10:11], v[114:115], s[6:7] op_sel_hi:[1,0]
	v_cvt_pk_fp8_f32 v4, v2, v3 op_sel:[0,0,1]
	v_med3_f32 v2, v8, s25, v218
	v_med3_f32 v3, v9, s25, v218
	v_cvt_pk_fp8_f32 v5, v2, v3
	v_med3_f32 v2, v6, s25, v218
	v_med3_f32 v3, v7, s25, v218
	v_pk_mul_f32 v[6:7], v[122:123], s[6:7] op_sel_hi:[1,0]
	v_exp_f32_e32 v10, v10
	v_exp_f32_e32 v6, v6
	v_exp_f32_e32 v7, v7
	v_exp_f32_e32 v11, v11
	v_cvt_pk_fp8_f32 v5, v2, v3 op_sel:[0,0,1]
	v_add_co_u32_e32 v2, vcc, s0, v0
	v_pk_fma_f32 v[6:7], v[6:7], s[34:35], s[34:35] op_sel_hi:[1,0,0]
	v_pk_fma_f32 v[10:11], v[10:11], s[34:35], s[34:35] op_sel_hi:[1,0,0]
	v_rcp_f32_e32 v6, v6
	v_rcp_f32_e32 v7, v7
	v_rcp_f32_e32 v10, v10
	v_rcp_f32_e32 v11, v11
	v_addc_co_u32_e32 v3, vcc, 0, v1, vcc
	global_store_dwordx2 v[2:3], v[4:5], off
	v_pk_mul_f32 v[4:5], v[122:123], v[126:127]
	v_pk_mul_f32 v[8:9], v[114:115], v[118:119]
	v_pk_mul_f32 v[4:5], v[6:7], v[4:5]
	v_pk_mul_f32 v[6:7], v[124:125], s[6:7] op_sel_hi:[1,0]
	v_pk_mul_f32 v[8:9], v[10:11], v[8:9]
	v_exp_f32_e32 v6, v6
	v_exp_f32_e32 v7, v7
	v_pk_mul_f32 v[10:11], v[116:117], s[6:7] op_sel_hi:[1,0]
	v_pk_mul_f32 v[2:3], v[124:125], v[128:129]
	v_exp_f32_e32 v10, v10
	v_exp_f32_e32 v11, v11
	v_pk_fma_f32 v[6:7], v[6:7], s[34:35], s[34:35] op_sel_hi:[1,0,0]
	v_med3_f32 v5, v5, s25, v218
	v_rcp_f32_e32 v6, v6
	v_rcp_f32_e32 v7, v7
	v_pk_fma_f32 v[10:11], v[10:11], s[34:35], s[34:35] op_sel_hi:[1,0,0]
	s_mov_b32 s0, 0x40000
	v_rcp_f32_e32 v10, v10
	v_rcp_f32_e32 v11, v11
	v_pk_mul_f32 v[2:3], v[6:7], v[2:3]
	v_pk_mul_f32 v[6:7], v[116:117], v[120:121]
	v_med3_f32 v2, v2, s25, v218
	v_pk_mul_f32 v[6:7], v[10:11], v[6:7]
	v_med3_f32 v10, v4, s25, v218
	v_cvt_pk_fp8_f32 v4, v10, v5
	v_med3_f32 v3, v3, s25, v218
	v_pk_mul_f32 v[10:11], v[96:97], s[6:7] op_sel_hi:[1,0]
	v_cvt_pk_fp8_f32 v4, v2, v3 op_sel:[0,0,1]
	v_med3_f32 v2, v8, s25, v218
	v_med3_f32 v3, v9, s25, v218
	v_cvt_pk_fp8_f32 v5, v2, v3
	v_med3_f32 v2, v6, s25, v218
	v_med3_f32 v3, v7, s25, v218
	v_pk_mul_f32 v[6:7], v[104:105], s[6:7] op_sel_hi:[1,0]
	v_exp_f32_e32 v10, v10
	v_exp_f32_e32 v6, v6
	v_exp_f32_e32 v7, v7
	v_exp_f32_e32 v11, v11
	v_cvt_pk_fp8_f32 v5, v2, v3 op_sel:[0,0,1]
	v_add_co_u32_e32 v2, vcc, s0, v0
	v_pk_fma_f32 v[6:7], v[6:7], s[34:35], s[34:35] op_sel_hi:[1,0,0]
	v_pk_fma_f32 v[10:11], v[10:11], s[34:35], s[34:35] op_sel_hi:[1,0,0]
	v_rcp_f32_e32 v6, v6
	v_rcp_f32_e32 v7, v7
	v_rcp_f32_e32 v10, v10
	v_rcp_f32_e32 v11, v11
	v_addc_co_u32_e32 v3, vcc, 0, v1, vcc
	global_store_dwordx2 v[2:3], v[4:5], off
	v_pk_mul_f32 v[4:5], v[104:105], v[108:109]
	v_pk_mul_f32 v[8:9], v[96:97], v[100:101]
	v_pk_mul_f32 v[4:5], v[6:7], v[4:5]
	v_pk_mul_f32 v[6:7], v[106:107], s[6:7] op_sel_hi:[1,0]
	v_pk_mul_f32 v[8:9], v[10:11], v[8:9]
	v_exp_f32_e32 v6, v6
	v_exp_f32_e32 v7, v7
	v_pk_mul_f32 v[10:11], v[98:99], s[6:7] op_sel_hi:[1,0]
	v_pk_mul_f32 v[2:3], v[106:107], v[110:111]
	v_exp_f32_e32 v10, v10
	v_exp_f32_e32 v11, v11
	v_pk_fma_f32 v[6:7], v[6:7], s[34:35], s[34:35] op_sel_hi:[1,0,0]
	v_med3_f32 v5, v5, s25, v218
	v_rcp_f32_e32 v6, v6
	v_rcp_f32_e32 v7, v7
	v_pk_fma_f32 v[10:11], v[10:11], s[34:35], s[34:35] op_sel_hi:[1,0,0]
	s_mov_b32 s0, 0x48000
	v_rcp_f32_e32 v10, v10
	v_rcp_f32_e32 v11, v11
	v_pk_mul_f32 v[2:3], v[6:7], v[2:3]
	v_pk_mul_f32 v[6:7], v[98:99], v[102:103]
	v_med3_f32 v2, v2, s25, v218
	v_pk_mul_f32 v[6:7], v[10:11], v[6:7]
	v_med3_f32 v10, v4, s25, v218
	v_cvt_pk_fp8_f32 v4, v10, v5
	v_med3_f32 v3, v3, s25, v218
	v_pk_mul_f32 v[10:11], v[80:81], s[6:7] op_sel_hi:[1,0]
	v_cvt_pk_fp8_f32 v4, v2, v3 op_sel:[0,0,1]
	v_med3_f32 v2, v8, s25, v218
	v_med3_f32 v3, v9, s25, v218
	v_cvt_pk_fp8_f32 v5, v2, v3
	v_med3_f32 v2, v6, s25, v218
	v_med3_f32 v3, v7, s25, v218
	v_pk_mul_f32 v[6:7], v[88:89], s[6:7] op_sel_hi:[1,0]
	v_exp_f32_e32 v10, v10
	v_exp_f32_e32 v6, v6
	v_exp_f32_e32 v7, v7
	v_exp_f32_e32 v11, v11
	v_cvt_pk_fp8_f32 v5, v2, v3 op_sel:[0,0,1]
	v_add_co_u32_e32 v2, vcc, s0, v0
	v_pk_fma_f32 v[6:7], v[6:7], s[34:35], s[34:35] op_sel_hi:[1,0,0]
	v_pk_fma_f32 v[10:11], v[10:11], s[34:35], s[34:35] op_sel_hi:[1,0,0]
	v_rcp_f32_e32 v6, v6
	v_rcp_f32_e32 v7, v7
	v_rcp_f32_e32 v10, v10
	v_rcp_f32_e32 v11, v11
	v_addc_co_u32_e32 v3, vcc, 0, v1, vcc
	global_store_dwordx2 v[2:3], v[4:5], off
	v_pk_mul_f32 v[4:5], v[88:89], v[92:93]
	v_pk_mul_f32 v[8:9], v[80:81], v[84:85]
	v_pk_mul_f32 v[4:5], v[6:7], v[4:5]
	v_pk_mul_f32 v[6:7], v[90:91], s[6:7] op_sel_hi:[1,0]
	v_pk_mul_f32 v[8:9], v[10:11], v[8:9]
	v_exp_f32_e32 v6, v6
	v_exp_f32_e32 v7, v7
	v_pk_mul_f32 v[10:11], v[82:83], s[6:7] op_sel_hi:[1,0]
	v_pk_mul_f32 v[2:3], v[90:91], v[94:95]
	v_exp_f32_e32 v10, v10
	v_exp_f32_e32 v11, v11
	v_pk_fma_f32 v[6:7], v[6:7], s[34:35], s[34:35] op_sel_hi:[1,0,0]
	v_med3_f32 v5, v5, s25, v218
	v_rcp_f32_e32 v6, v6
	v_rcp_f32_e32 v7, v7
	v_pk_fma_f32 v[10:11], v[10:11], s[34:35], s[34:35] op_sel_hi:[1,0,0]
	s_mov_b32 s0, 0x50000
	v_rcp_f32_e32 v10, v10
	v_rcp_f32_e32 v11, v11
	v_pk_mul_f32 v[2:3], v[6:7], v[2:3]
	v_pk_mul_f32 v[6:7], v[82:83], v[86:87]
	v_med3_f32 v2, v2, s25, v218
	v_pk_mul_f32 v[6:7], v[10:11], v[6:7]
	v_med3_f32 v10, v4, s25, v218
	v_cvt_pk_fp8_f32 v4, v10, v5
	v_med3_f32 v3, v3, s25, v218
	v_pk_mul_f32 v[10:11], v[68:69], s[6:7] op_sel_hi:[1,0]
	v_cvt_pk_fp8_f32 v4, v2, v3 op_sel:[0,0,1]
	v_med3_f32 v2, v8, s25, v218
	v_med3_f32 v3, v9, s25, v218
	v_cvt_pk_fp8_f32 v5, v2, v3
	v_med3_f32 v2, v6, s25, v218
	v_med3_f32 v3, v7, s25, v218
	v_pk_mul_f32 v[6:7], v[72:73], s[6:7] op_sel_hi:[1,0]
	v_exp_f32_e32 v10, v10
	v_exp_f32_e32 v6, v6
	v_exp_f32_e32 v7, v7
	v_exp_f32_e32 v11, v11
	v_cvt_pk_fp8_f32 v5, v2, v3 op_sel:[0,0,1]
	v_add_co_u32_e32 v2, vcc, s0, v0
	v_pk_fma_f32 v[6:7], v[6:7], s[34:35], s[34:35] op_sel_hi:[1,0,0]
	v_pk_fma_f32 v[10:11], v[10:11], s[34:35], s[34:35] op_sel_hi:[1,0,0]
	v_rcp_f32_e32 v6, v6
	v_rcp_f32_e32 v7, v7
	v_rcp_f32_e32 v10, v10
	v_rcp_f32_e32 v11, v11
	v_addc_co_u32_e32 v3, vcc, 0, v1, vcc
	global_store_dwordx2 v[2:3], v[4:5], off
	v_pk_mul_f32 v[4:5], v[72:73], v[76:77]
	v_pk_mul_f32 v[8:9], v[68:69], v[64:65]
	v_pk_mul_f32 v[4:5], v[6:7], v[4:5]
	v_pk_mul_f32 v[6:7], v[74:75], s[6:7] op_sel_hi:[1,0]
	v_pk_mul_f32 v[8:9], v[10:11], v[8:9]
	v_exp_f32_e32 v6, v6
	v_exp_f32_e32 v7, v7
	v_pk_mul_f32 v[10:11], v[70:71], s[6:7] op_sel_hi:[1,0]
	v_pk_mul_f32 v[2:3], v[74:75], v[78:79]
	v_exp_f32_e32 v10, v10
	v_exp_f32_e32 v11, v11
	v_pk_fma_f32 v[6:7], v[6:7], s[34:35], s[34:35] op_sel_hi:[1,0,0]
	v_med3_f32 v5, v5, s25, v218
	v_rcp_f32_e32 v6, v6
	v_rcp_f32_e32 v7, v7
	v_pk_fma_f32 v[10:11], v[10:11], s[34:35], s[34:35] op_sel_hi:[1,0,0]
	v_add_co_u32_e32 v0, vcc, 0x58000, v0
	v_rcp_f32_e32 v10, v10
	v_rcp_f32_e32 v11, v11
	v_pk_mul_f32 v[2:3], v[6:7], v[2:3]
	v_pk_mul_f32 v[6:7], v[70:71], v[66:67]
	v_med3_f32 v2, v2, s25, v218
	v_pk_mul_f32 v[6:7], v[10:11], v[6:7]
	v_med3_f32 v10, v4, s25, v218
	v_cvt_pk_fp8_f32 v4, v10, v5
	v_med3_f32 v3, v3, s25, v218
	v_addc_co_u32_e32 v1, vcc, 0, v1, vcc
	v_cvt_pk_fp8_f32 v4, v2, v3 op_sel:[0,0,1]
	v_med3_f32 v2, v8, s25, v218
	v_med3_f32 v3, v9, s25, v218
	v_cvt_pk_fp8_f32 v5, v2, v3
	v_med3_f32 v2, v6, s25, v218
	v_med3_f32 v3, v7, s25, v218
	s_mov_b64 s[0:1], -1
	v_cvt_pk_fp8_f32 v5, v2, v3 op_sel:[0,0,1]
	s_and_b64 vcc, exec, s[38:39]
	global_store_dwordx2 v[0:1], v[4:5], off
	s_cbranch_vccnz .LBB0_1579
	s_andn2_b64 vcc, exec, s[44:45]
	s_cbranch_vccnz .LBB0_1578
	s_barrier
	s_branch .LBB0_1578

.LBB0_1665:
	v_pk_mul_f32 v[6:7], v[190:191], s[36:37] op_sel_hi:[1,0]
	v_pk_mul_f32 v[4:5], v[192:193], s[36:37] op_sel_hi:[1,0]
	v_pk_mul_f32 v[10:11], v[186:187], s[36:37] op_sel_hi:[1,0]
	v_med3_f32 v3, v6, s25, v218
	v_med3_f32 v7, v7, s25, v218
	v_cvt_pk_fp8_f32 v6, v3, v7
	v_med3_f32 v3, v4, s25, v218
	v_med3_f32 v4, v5, s25, v218
	v_med3_f32 v5, v10, s25, v218
	v_med3_f32 v10, v11, s25, v218
	v_cvt_pk_fp8_f32 v7, v5, v10
	v_pk_mul_f32 v[8:9], v[188:189], s[36:37] op_sel_hi:[1,0]
	v_cvt_pk_fp8_f32 v6, v3, v4 op_sel:[0,0,1]
	v_med3_f32 v3, v8, s25, v218
	v_med3_f32 v4, v9, s25, v218
	v_pk_mul_f32 v[8:9], v[182:183], s[36:37] op_sel_hi:[1,0]
	v_cvt_pk_fp8_f32 v7, v3, v4 op_sel:[0,0,1]
	v_pk_mul_f32 v[4:5], v[184:185], s[36:37] op_sel_hi:[1,0]
	v_pk_mul_f32 v[12:13], v[174:175], s[36:37] op_sel_hi:[1,0]
	v_med3_f32 v3, v8, s25, v218
	v_med3_f32 v9, v9, s25, v218
	s_lshl_b32 s2, s20, 8
	v_cvt_pk_fp8_f32 v8, v3, v9
	v_med3_f32 v3, v4, s25, v218
	v_med3_f32 v4, v5, s25, v218
	v_med3_f32 v5, v12, s25, v218
	v_med3_f32 v12, v13, s25, v218
	s_mul_hi_i32 s3, s0, 0x1200
	s_mulk_i32 s0, 0x1200
	s_ashr_i32 s4, s2, 31
	v_cvt_pk_fp8_f32 v9, v5, v12
	v_mbcnt_lo_u32_b32 v2, -1, 0
	v_mbcnt_hi_u32_b32 v2, -1, v2
	s_add_u32 s2, s0, s2
	v_and_or_b32 v0, v2, 15, s67
	v_mov_b32_e32 v1, s76
	v_ashrrev_i32_e32 v2, 1, v2
	s_addc_u32 s3, s3, s4
	s_lshl_b32 s0, s1, 8
	v_pk_mul_f32 v[10:11], v[176:177], s[36:37] op_sel_hi:[1,0]
	v_and_b32_e32 v2, -8, v2
	v_lshl_add_u64 v[0:1], v[0:1], 0, s[2:3]
	s_or_b32 s0, s0, s68
	v_cvt_pk_fp8_f32 v8, v3, v4 op_sel:[0,0,1]
	v_med3_f32 v3, v10, s25, v218
	v_med3_f32 v4, v11, s25, v218
	v_lshlrev_b64 v[0:1], 10, v[0:1]
	v_add_u32_e32 v2, s0, v2
	v_cvt_pk_fp8_f32 v9, v3, v4 op_sel:[0,0,1]
	v_lshl_add_u64 v[0:1], s[42:43], 0, v[0:1]
	v_ashrrev_i32_e32 v3, 31, v2
	v_lshl_add_u64 v[0:1], v[0:1], 0, v[2:3]
	v_pk_mul_f32 v[4:5], v[178:179], s[36:37] op_sel_hi:[1,0]
	global_store_dwordx2 v[0:1], v[6:7], off
	global_store_dwordx2 v[0:1], v[8:9], off offset:128
	v_pk_mul_f32 v[8:9], v[170:171], s[36:37] op_sel_hi:[1,0]
	v_med3_f32 v10, v4, s25, v218
	v_med3_f32 v5, v5, s25, v218
	v_cvt_pk_fp8_f32 v4, v10, v5
	v_med3_f32 v8, v8, s25, v218
	v_med3_f32 v9, v9, s25, v218
	v_cvt_pk_fp8_f32 v5, v8, v9
	v_pk_mul_f32 v[8:9], v[166:167], s[36:37] op_sel_hi:[1,0]
	v_pk_mul_f32 v[12:13], v[158:159], s[36:37] op_sel_hi:[1,0]
	v_med3_f32 v14, v8, s25, v218
	v_med3_f32 v9, v9, s25, v218
	v_pk_mul_f32 v[2:3], v[180:181], s[36:37] op_sel_hi:[1,0]
	v_cvt_pk_fp8_f32 v8, v14, v9
	v_med3_f32 v12, v12, s25, v218
	v_med3_f32 v13, v13, s25, v218
	v_pk_mul_f32 v[6:7], v[172:173], s[36:37] op_sel_hi:[1,0]
	v_med3_f32 v2, v2, s25, v218
	v_med3_f32 v3, v3, s25, v218
	v_cvt_pk_fp8_f32 v9, v12, v13
	v_cvt_pk_fp8_f32 v4, v2, v3 op_sel:[0,0,1]
	v_med3_f32 v2, v6, s25, v218
	v_med3_f32 v3, v7, s25, v218
	v_pk_mul_f32 v[6:7], v[168:169], s[36:37] op_sel_hi:[1,0]
	v_pk_mul_f32 v[10:11], v[160:161], s[36:37] op_sel_hi:[1,0]
	v_med3_f32 v6, v6, s25, v218
	v_med3_f32 v7, v7, s25, v218
	v_cvt_pk_fp8_f32 v5, v2, v3 op_sel:[0,0,1]
	s_mov_b64 s[0:1], 0x4000
	v_cvt_pk_fp8_f32 v8, v6, v7 op_sel:[0,0,1]
	v_med3_f32 v6, v10, s25, v218
	v_med3_f32 v7, v11, s25, v218
	v_lshl_add_u64 v[2:3], v[0:1], 0, s[0:1]
	v_cvt_pk_fp8_f32 v9, v6, v7 op_sel:[0,0,1]
	s_movk_i32 s0, 0x4000
	v_add_co_u32_e32 v6, vcc, s0, v0
	v_pk_mul_f32 v[12:13], v[142:143], s[36:37] op_sel_hi:[1,0]
	s_nop 0
	v_addc_co_u32_e32 v7, vcc, 0, v1, vcc
	global_store_dwordx2 v[6:7], v[4:5], off
	global_store_dwordx2 v[2:3], v[8:9], off offset:128
	v_pk_mul_f32 v[4:5], v[162:163], s[36:37] op_sel_hi:[1,0]
	v_pk_mul_f32 v[8:9], v[154:155], s[36:37] op_sel_hi:[1,0]
	v_med3_f32 v10, v4, s25, v218
	v_med3_f32 v5, v5, s25, v218
	v_cvt_pk_fp8_f32 v4, v10, v5
	v_med3_f32 v8, v8, s25, v218
	v_med3_f32 v9, v9, s25, v218
	v_cvt_pk_fp8_f32 v5, v8, v9
	v_pk_mul_f32 v[8:9], v[150:151], s[36:37] op_sel_hi:[1,0]
	v_pk_mul_f32 v[2:3], v[164:165], s[36:37] op_sel_hi:[1,0]
	v_med3_f32 v14, v8, s25, v218
	v_med3_f32 v9, v9, s25, v218
	v_cvt_pk_fp8_f32 v8, v14, v9
	v_med3_f32 v12, v12, s25, v218
	v_med3_f32 v13, v13, s25, v218
	v_pk_mul_f32 v[6:7], v[156:157], s[36:37] op_sel_hi:[1,0]
	v_med3_f32 v2, v2, s25, v218
	v_med3_f32 v3, v3, s25, v218
	v_cvt_pk_fp8_f32 v9, v12, v13
	v_cvt_pk_fp8_f32 v4, v2, v3 op_sel:[0,0,1]
	v_med3_f32 v2, v6, s25, v218
	v_med3_f32 v3, v7, s25, v218
	v_pk_mul_f32 v[6:7], v[152:153], s[36:37] op_sel_hi:[1,0]
	v_pk_mul_f32 v[10:11], v[144:145], s[36:37] op_sel_hi:[1,0]
	v_med3_f32 v6, v6, s25, v218
	v_med3_f32 v7, v7, s25, v218
	v_cvt_pk_fp8_f32 v5, v2, v3 op_sel:[0,0,1]
	v_cvt_pk_fp8_f32 v8, v6, v7 op_sel:[0,0,1]
	v_med3_f32 v6, v10, s25, v218
	v_med3_f32 v7, v11, s25, v218
	v_cvt_pk_fp8_f32 v9, v6, v7 op_sel:[0,0,1]
	v_add_co_u32_e32 v6, vcc, s91, v0
	s_mov_b64 s[0:1], 0x8000
	s_nop 0
	v_addc_co_u32_e32 v7, vcc, 0, v1, vcc
	v_lshl_add_u64 v[2:3], v[0:1], 0, s[0:1]
	global_store_dwordx2 v[6:7], v[4:5], off
	global_store_dwordx2 v[2:3], v[8:9], off offset:128
	v_pk_mul_f32 v[4:5], v[146:147], s[36:37] op_sel_hi:[1,0]
	v_pk_mul_f32 v[8:9], v[138:139], s[36:37] op_sel_hi:[1,0]
	v_med3_f32 v10, v4, s25, v218
	v_med3_f32 v5, v5, s25, v218
	v_cvt_pk_fp8_f32 v4, v10, v5
	v_med3_f32 v8, v8, s25, v218
	v_med3_f32 v9, v9, s25, v218
	v_cvt_pk_fp8_f32 v5, v8, v9
	v_pk_mul_f32 v[8:9], v[134:135], s[36:37] op_sel_hi:[1,0]
	v_pk_mul_f32 v[12:13], v[130:131], s[36:37] op_sel_hi:[1,0]
	v_med3_f32 v14, v8, s25, v218
	v_med3_f32 v9, v9, s25, v218
	v_pk_mul_f32 v[2:3], v[148:149], s[36:37] op_sel_hi:[1,0]
	v_cvt_pk_fp8_f32 v8, v14, v9
	v_med3_f32 v12, v12, s25, v218
	v_med3_f32 v13, v13, s25, v218
	v_pk_mul_f32 v[6:7], v[140:141], s[36:37] op_sel_hi:[1,0]
	v_med3_f32 v2, v2, s25, v218
	v_med3_f32 v3, v3, s25, v218
	v_cvt_pk_fp8_f32 v9, v12, v13
	v_cvt_pk_fp8_f32 v4, v2, v3 op_sel:[0,0,1]
	v_med3_f32 v2, v6, s25, v218
	v_med3_f32 v3, v7, s25, v218
	v_pk_mul_f32 v[6:7], v[136:137], s[36:37] op_sel_hi:[1,0]
	v_pk_mul_f32 v[10:11], v[132:133], s[36:37] op_sel_hi:[1,0]
	v_med3_f32 v6, v6, s25, v218
	v_med3_f32 v7, v7, s25, v218
	v_cvt_pk_fp8_f32 v5, v2, v3 op_sel:[0,0,1]
	s_mov_b64 s[0:1], 0xc000
	v_cvt_pk_fp8_f32 v8, v6, v7 op_sel:[0,0,1]
	v_med3_f32 v6, v10, s25, v218
	v_med3_f32 v7, v11, s25, v218
	v_lshl_add_u64 v[2:3], v[0:1], 0, s[0:1]
	v_cvt_pk_fp8_f32 v9, v6, v7 op_sel:[0,0,1]
	s_mov_b32 s0, 0xc000
	v_add_co_u32_e32 v6, vcc, s0, v0
	v_pk_mul_f32 v[12:13], v[108:109], s[36:37] op_sel_hi:[1,0]
	s_nop 0
	v_addc_co_u32_e32 v7, vcc, 0, v1, vcc
	global_store_dwordx2 v[6:7], v[4:5], off
	global_store_dwordx2 v[2:3], v[8:9], off offset:128
	v_pk_mul_f32 v[4:5], v[126:127], s[36:37] op_sel_hi:[1,0]
	v_pk_mul_f32 v[8:9], v[122:123], s[36:37] op_sel_hi:[1,0]
	v_med3_f32 v10, v4, s25, v218
	v_med3_f32 v5, v5, s25, v218
	v_cvt_pk_fp8_f32 v4, v10, v5
	v_med3_f32 v8, v8, s25, v218
	v_med3_f32 v9, v9, s25, v218
	v_cvt_pk_fp8_f32 v5, v8, v9
	v_pk_mul_f32 v[8:9], v[118:119], s[36:37] op_sel_hi:[1,0]
	v_pk_mul_f32 v[2:3], v[128:129], s[36:37] op_sel_hi:[1,0]
	v_med3_f32 v14, v8, s25, v218
	v_med3_f32 v9, v9, s25, v218
	v_cvt_pk_fp8_f32 v8, v14, v9
	v_med3_f32 v12, v12, s25, v218
	v_med3_f32 v13, v13, s25, v218
	v_pk_mul_f32 v[6:7], v[124:125], s[36:37] op_sel_hi:[1,0]
	v_med3_f32 v2, v2, s25, v218
	v_med3_f32 v3, v3, s25, v218
	v_cvt_pk_fp8_f32 v9, v12, v13
	v_cvt_pk_fp8_f32 v4, v2, v3 op_sel:[0,0,1]
	v_med3_f32 v2, v6, s25, v218
	v_med3_f32 v3, v7, s25, v218
	v_pk_mul_f32 v[6:7], v[120:121], s[36:37] op_sel_hi:[1,0]
	v_pk_mul_f32 v[10:11], v[110:111], s[36:37] op_sel_hi:[1,0]
	v_med3_f32 v6, v6, s25, v218
	v_med3_f32 v7, v7, s25, v218
	v_cvt_pk_fp8_f32 v5, v2, v3 op_sel:[0,0,1]
	s_mov_b64 s[0:1], 0x20000
	v_cvt_pk_fp8_f32 v8, v6, v7 op_sel:[0,0,1]
	v_med3_f32 v6, v10, s25, v218
	v_med3_f32 v7, v11, s25, v218
	v_lshl_add_u64 v[2:3], v[0:1], 0, s[0:1]
	v_cvt_pk_fp8_f32 v9, v6, v7 op_sel:[0,0,1]
	s_mov_b32 s0, 0x20000
	v_add_co_u32_e32 v6, vcc, s0, v0
	v_pk_mul_f32 v[12:13], v[92:93], s[36:37] op_sel_hi:[1,0]
	s_nop 0
	v_addc_co_u32_e32 v7, vcc, 0, v1, vcc
	global_store_dwordx2 v[6:7], v[4:5], off
	global_store_dwordx2 v[2:3], v[8:9], off offset:128
	v_pk_mul_f32 v[4:5], v[114:115], s[36:37] op_sel_hi:[1,0]
	v_pk_mul_f32 v[8:9], v[104:105], s[36:37] op_sel_hi:[1,0]
	v_med3_f32 v10, v4, s25, v218
	v_med3_f32 v5, v5, s25, v218
	v_cvt_pk_fp8_f32 v4, v10, v5
	v_med3_f32 v8, v8, s25, v218
	v_med3_f32 v9, v9, s25, v218
	v_cvt_pk_fp8_f32 v5, v8, v9
	v_pk_mul_f32 v[8:9], v[100:101], s[36:37] op_sel_hi:[1,0]
	v_pk_mul_f32 v[2:3], v[116:117], s[36:37] op_sel_hi:[1,0]
	v_med3_f32 v14, v8, s25, v218
	v_med3_f32 v9, v9, s25, v218
	v_cvt_pk_fp8_f32 v8, v14, v9
	v_med3_f32 v12, v12, s25, v218
	v_med3_f32 v13, v13, s25, v218
	v_pk_mul_f32 v[6:7], v[106:107], s[36:37] op_sel_hi:[1,0]
	v_med3_f32 v2, v2, s25, v218
	v_med3_f32 v3, v3, s25, v218
	v_cvt_pk_fp8_f32 v9, v12, v13
	v_cvt_pk_fp8_f32 v4, v2, v3 op_sel:[0,0,1]
	v_med3_f32 v2, v6, s25, v218
	v_med3_f32 v3, v7, s25, v218
	v_pk_mul_f32 v[6:7], v[102:103], s[36:37] op_sel_hi:[1,0]
	v_pk_mul_f32 v[10:11], v[94:95], s[36:37] op_sel_hi:[1,0]
	v_med3_f32 v6, v6, s25, v218
	v_med3_f32 v7, v7, s25, v218
	v_cvt_pk_fp8_f32 v5, v2, v3 op_sel:[0,0,1]
	s_mov_b64 s[0:1], 0x24000
	v_cvt_pk_fp8_f32 v8, v6, v7 op_sel:[0,0,1]
	v_med3_f32 v6, v10, s25, v218
	v_med3_f32 v7, v11, s25, v218
	v_lshl_add_u64 v[2:3], v[0:1], 0, s[0:1]
	v_cvt_pk_fp8_f32 v9, v6, v7 op_sel:[0,0,1]
	s_mov_b32 s0, 0x24000
	v_add_co_u32_e32 v6, vcc, s0, v0
	v_pk_mul_f32 v[12:13], v[76:77], s[36:37] op_sel_hi:[1,0]
	s_nop 0
	v_addc_co_u32_e32 v7, vcc, 0, v1, vcc
	global_store_dwordx2 v[6:7], v[4:5], off
	global_store_dwordx2 v[2:3], v[8:9], off offset:128
	v_pk_mul_f32 v[4:5], v[96:97], s[36:37] op_sel_hi:[1,0]
	v_pk_mul_f32 v[8:9], v[88:89], s[36:37] op_sel_hi:[1,0]
	v_med3_f32 v10, v4, s25, v218
	v_med3_f32 v5, v5, s25, v218
	v_cvt_pk_fp8_f32 v4, v10, v5
	v_med3_f32 v8, v8, s25, v218
	v_med3_f32 v9, v9, s25, v218
	v_cvt_pk_fp8_f32 v5, v8, v9
	v_pk_mul_f32 v[8:9], v[84:85], s[36:37] op_sel_hi:[1,0]
	v_pk_mul_f32 v[2:3], v[98:99], s[36:37] op_sel_hi:[1,0]
	v_med3_f32 v14, v8, s25, v218
	v_med3_f32 v9, v9, s25, v218
	v_cvt_pk_fp8_f32 v8, v14, v9
	v_med3_f32 v12, v12, s25, v218
	v_med3_f32 v13, v13, s25, v218
	v_pk_mul_f32 v[6:7], v[90:91], s[36:37] op_sel_hi:[1,0]
	v_med3_f32 v2, v2, s25, v218
	v_med3_f32 v3, v3, s25, v218
	v_cvt_pk_fp8_f32 v9, v12, v13
	v_cvt_pk_fp8_f32 v4, v2, v3 op_sel:[0,0,1]
	v_med3_f32 v2, v6, s25, v218
	v_med3_f32 v3, v7, s25, v218
	v_pk_mul_f32 v[6:7], v[86:87], s[36:37] op_sel_hi:[1,0]
	v_pk_mul_f32 v[10:11], v[78:79], s[36:37] op_sel_hi:[1,0]
	v_med3_f32 v6, v6, s25, v218
	v_med3_f32 v7, v7, s25, v218
	v_cvt_pk_fp8_f32 v5, v2, v3 op_sel:[0,0,1]
	s_mov_b64 s[0:1], 0x28000
	v_cvt_pk_fp8_f32 v8, v6, v7 op_sel:[0,0,1]
	v_med3_f32 v6, v10, s25, v218
	v_med3_f32 v7, v11, s25, v218
	v_lshl_add_u64 v[2:3], v[0:1], 0, s[0:1]
	v_cvt_pk_fp8_f32 v9, v6, v7 op_sel:[0,0,1]
	s_mov_b32 s0, 0x28000
	v_add_co_u32_e32 v6, vcc, s0, v0
	v_pk_mul_f32 v[12:13], v[64:65], s[36:37] op_sel_hi:[1,0]
	s_nop 0
	v_addc_co_u32_e32 v7, vcc, 0, v1, vcc
	global_store_dwordx2 v[6:7], v[4:5], off
	global_store_dwordx2 v[2:3], v[8:9], off offset:128
	v_pk_mul_f32 v[4:5], v[80:81], s[36:37] op_sel_hi:[1,0]
	v_pk_mul_f32 v[8:9], v[72:73], s[36:37] op_sel_hi:[1,0]
	v_med3_f32 v10, v4, s25, v218
	v_med3_f32 v5, v5, s25, v218
	v_cvt_pk_fp8_f32 v4, v10, v5
	v_med3_f32 v8, v8, s25, v218
	v_med3_f32 v9, v9, s25, v218
	v_cvt_pk_fp8_f32 v5, v8, v9
	v_pk_mul_f32 v[8:9], v[68:69], s[36:37] op_sel_hi:[1,0]
	v_pk_mul_f32 v[2:3], v[82:83], s[36:37] op_sel_hi:[1,0]
	v_med3_f32 v14, v8, s25, v218
	v_med3_f32 v9, v9, s25, v218
	v_cvt_pk_fp8_f32 v8, v14, v9
	v_med3_f32 v12, v12, s25, v218
	v_med3_f32 v13, v13, s25, v218
	v_pk_mul_f32 v[6:7], v[74:75], s[36:37] op_sel_hi:[1,0]
	v_med3_f32 v2, v2, s25, v218
	v_med3_f32 v3, v3, s25, v218
	v_cvt_pk_fp8_f32 v9, v12, v13
	v_cvt_pk_fp8_f32 v4, v2, v3 op_sel:[0,0,1]
	v_med3_f32 v2, v6, s25, v218
	v_med3_f32 v3, v7, s25, v218
	v_pk_mul_f32 v[6:7], v[70:71], s[36:37] op_sel_hi:[1,0]
	s_mov_b64 s[0:1], 0x2c000
	v_pk_mul_f32 v[10:11], v[66:67], s[36:37] op_sel_hi:[1,0]
	v_med3_f32 v6, v6, s25, v218
	v_med3_f32 v7, v7, s25, v218
	v_cvt_pk_fp8_f32 v5, v2, v3 op_sel:[0,0,1]
	v_lshl_add_u64 v[2:3], v[0:1], 0, s[0:1]
	v_cvt_pk_fp8_f32 v8, v6, v7 op_sel:[0,0,1]
	v_med3_f32 v6, v10, s25, v218
	v_med3_f32 v7, v11, s25, v218
	s_mov_b32 s0, 0x2c000
	v_cvt_pk_fp8_f32 v9, v6, v7 op_sel:[0,0,1]
	v_add_co_u32_e32 v0, vcc, s0, v0
	s_mov_b64 s[0:1], -1
	s_nop 0
	v_addc_co_u32_e32 v1, vcc, 0, v1, vcc
	s_andn2_b64 vcc, exec, s[54:55]
	global_store_dwordx2 v[0:1], v[4:5], off
	global_store_dwordx2 v[2:3], v[8:9], off offset:128
	s_cbranch_vccnz .LBB0_1655
	s_andn2_b64 vcc, exec, s[40:41]
	s_cbranch_vccnz .LBB0_1654
	s_barrier
	s_branch .LBB0_1654
